# hand-written post phases (x += gate*rmsnorm(y)*g; h = modulate(rmsnorm(x))): one row per wave, folded vectors in registers, loads two rows ahead; plus earlier indexer and stick-breaking edits
# speedup vs baseline: 1.0097x; 1.0010x over previous
_Z10fwd_kernel4Args:
	s_mov_b32 s101, s2
	s_load_dwordx4 s[4:7], s[0:1], 0x98
	s_load_dwordx2 s[66:67], s[0:1], 0xa8
	s_load_dword s28, s[0:1], 0xb0
	s_mov_b32 s52, s2
	s_add_u32 s2, s0, 0xb0
	v_readfirstlane_b32 s22, v0
	s_waitcnt lgkmcnt(0)
	v_writelane_b32 v252, s4, 0
	v_cmp_gt_u32_e32 vcc, 64, v0
	s_nop 0
	v_writelane_b32 v252, s5, 1
	v_writelane_b32 v252, s6, 2
	v_writelane_b32 v252, s7, 3
	v_writelane_b32 v252, s0, 4
	s_addc_u32 s3, s1, 0
	s_nop 0
	v_writelane_b32 v252, s1, 5
	s_and_saveexec_b64 s[0:1], vcc
	v_lshl_add_u32 v1, v0, 2, 0
	v_add_u32_e32 v1, 0x27f00, v1
	v_mov_b32_e32 v2, 0
	ds_write_b32 v1, v2
	s_or_b64 exec, exec, s[0:1]
	v_readlane_b32 s4, v252, 0
	v_readlane_b32 s6, v252, 2
	v_readlane_b32 s7, v252, 3
	s_add_u32 s0, s6, 0x4000
	s_addc_u32 s1, s7, 0
	v_readlane_b32 s5, v252, 1
	v_writelane_b32 v252, s0, 6
	s_mov_b32 s95, 0
	v_cmp_eq_u32_e32 vcc, 0, v0
	v_writelane_b32 v252, s1, 7
	s_sub_i32 s0, s67, s66
	s_cmp_lt_i32 s0, 2
	s_mov_b32 s64, 0
	s_waitcnt lgkmcnt(0)
	s_barrier
	s_cbranch_scc1 .LBB0_59
	s_getreg_b32 s0, hwreg(HW_REG_XCC_ID, 0, 4)
	s_and_b32 s64, s0, 15
	s_and_saveexec_b64 s[0:1], vcc
	s_cbranch_execz .LBB0_6
	s_mov_b64 s[6:7], exec
	v_mbcnt_lo_u32_b32 v1, s6, 0
	v_mbcnt_hi_u32_b32 v1, s7, v1
	v_cmp_eq_u32_e64 s[4:5], 0, v1
	s_and_b64 s[4:5], exec, s[4:5]
	s_mov_b64 exec, s[4:5]
	s_cbranch_execz .LBB0_6
	s_lshl_b32 s4, s64, 8
	s_bcnt1_i32_b64 s5, s[6:7]
	v_mov_b32_e32 v1, s4
	v_mov_b32_e32 v2, s5
	v_readlane_b32 s4, v252, 6
	v_readlane_b32 s5, v252, 7
	s_nop 4
	global_atomic_add v1, v2, s[4:5] offset:1024

.LBB0_452:
	s_or_b64 exec, exec, s[10:11]
	v_readfirstlane_b32 s10, v0
	s_cmpk_gt_i32 s10, 0x7ff
	s_cselect_b64 s[30:31], -1, 0
	s_and_b64 vcc, exec, s[30:31]
	s_cbranch_vccnz .LBB0_447
	s_lshl_b32 s14, s10, 1
	s_and_b32 s47, s10, 0x780
	s_lshl_b32 s11, s10, 5
	s_add_i32 s10, s14, s46
	s_and_b32 s56, s11, 0xfe0
	s_and_b32 s57, s10, 0xfffff000
	s_or_b32 s15, s57, s56
	s_lshl_b32 s10, s47, 1
	s_add_u32 s10, s50, s10
	s_addc_u32 s11, s51, 0
	v_add_u32_e32 v32, s15, v174
	v_mov_b64_e32 v[24:25], s[10:11]
	v_add_u32_e32 v34, s15, v175
	v_add_u32_e32 v36, s15, v176
	v_add_u32_e32 v38, s15, v177
	v_add_u32_e32 v40, s15, v178
	v_add_u32_e32 v41, s15, v179
	v_mad_i64_i32 v[0:1], s[12:13], v32, s3, v[24:25]
	v_mad_i64_i32 v[2:3], s[12:13], v34, s3, v[24:25]
	v_mad_i64_i32 v[8:9], s[12:13], v36, s3, v[24:25]
	v_mad_i64_i32 v[10:11], s[12:13], v38, s3, v[24:25]
	v_mad_i64_i32 v[16:17], s[12:13], v40, s3, v[24:25]
	v_mad_i64_i32 v[18:19], s[12:13], v41, s3, v[24:25]
	v_lshl_add_u64 v[0:1], v[0:1], 0, v[160:161]
	v_lshl_add_u64 v[4:5], v[2:3], 0, v[160:161]
	v_lshl_add_u64 v[8:9], v[8:9], 0, v[160:161]
	v_lshl_add_u64 v[12:13], v[10:11], 0, v[160:161]
	v_lshl_add_u64 v[16:17], v[16:17], 0, v[160:161]
	v_lshl_add_u64 v[20:21], v[18:19], 0, v[160:161]
	global_load_dwordx4 v[0:3], v[0:1], off
	s_nop 0
	global_load_dwordx4 v[4:7], v[4:5], off
	s_nop 0
	global_load_dwordx4 v[8:11], v[8:9], off
	s_nop 0
	global_load_dwordx4 v[12:15], v[12:13], off
	s_nop 0
	global_load_dwordx4 v[16:19], v[16:17], off
	s_nop 0
	global_load_dwordx4 v[20:23], v[20:21], off
	v_mov_b32_e32 v147, v161
	v_lshl_add_u64 v[148:149], s[10:11], 0, v[146:147]
	s_mov_b64 s[98:99], 0x2000
	v_lshl_add_u64 v[216:217], v[148:149], 0, s[98:99]
	v_mad_i64_i32 v[32:33], s[10:11], v32, s3, v[148:149]
	v_add_co_u32_e32 v32, vcc, s93, v32
	v_mad_i64_i32 v[34:35], s[10:11], v34, s3, v[148:149]
	s_nop 0
	v_addc_co_u32_e32 v33, vcc, 0, v33, vcc
	v_add_co_u32_e32 v34, vcc, s93, v34
	v_mad_i64_i32 v[36:37], s[10:11], v36, s3, v[148:149]
	s_nop 0
	v_addc_co_u32_e32 v35, vcc, 0, v35, vcc
	v_add_u32_e32 v42, s15, v180
	v_add_u32_e32 v43, s15, v181
	v_add_co_u32_e32 v36, vcc, s93, v36
	v_mad_i64_i32 v[26:27], s[12:13], v42, s3, v[24:25]
	v_mad_i64_i32 v[24:25], s[12:13], v43, s3, v[24:25]
	v_mad_i64_i32 v[38:39], s[10:11], v38, s3, v[148:149]
	v_addc_co_u32_e32 v37, vcc, 0, v37, vcc
	v_lshl_add_u64 v[26:27], v[26:27], 0, v[160:161]
	v_lshl_add_u64 v[28:29], v[24:25], 0, v[160:161]
	v_add_co_u32_e32 v38, vcc, s93, v38
	global_load_dwordx4 v[24:27], v[26:27], off
	s_nop 0
	global_load_dwordx4 v[28:31], v[28:29], off
	v_addc_co_u32_e32 v39, vcc, 0, v39, vcc
	global_load_dwordx4 v[80:83], v[32:33], off offset:-4096
	global_load_dwordx4 v[84:87], v[32:33], off
	global_load_dwordx4 v[88:91], v[34:35], off offset:-4096
	global_load_dwordx4 v[92:95], v[34:35], off
	global_load_dwordx4 v[96:99], v[36:37], off offset:-4096
	global_load_dwordx4 v[100:103], v[36:37], off
	v_mov_b32_e32 v48, 0
	s_mov_b32 s58, 0
	v_mov_b32_e32 v205, 1.0
	v_mov_b32_e32 v49, v48
	v_mov_b32_e32 v50, v48
	v_mov_b32_e32 v51, v48
	v_mov_b32_e32 v52, v48
	v_mov_b32_e32 v53, v48
	v_mov_b32_e32 v54, v48
	v_mov_b32_e32 v55, v48
	v_mov_b32_e32 v56, v48
	v_mov_b32_e32 v57, v48
	v_mov_b32_e32 v58, v48
	v_mov_b32_e32 v59, v48
	v_mov_b32_e32 v60, v48
	s_waitcnt vmcnt(0)
	ds_write_b128 v190, v[0:3] offset:8192
	ds_write_b128 v191, v[4:7] offset:8192
	ds_write_b128 v192, v[8:11] offset:8192
	ds_write_b128 v193, v[12:15] offset:8192
	ds_write_b128 v194, v[16:19] offset:8192
	ds_write_b128 v195, v[20:23] offset:8192
	v_mad_i64_i32 v[0:1], s[10:11], v40, s3, v[148:149]
	v_add_co_u32_e32 v0, vcc, s93, v0
	global_load_dwordx4 v[104:107], v[38:39], off offset:-4096
	global_load_dwordx4 v[108:111], v[38:39], off
	v_addc_co_u32_e32 v1, vcc, 0, v1, vcc
	global_load_dwordx4 v[112:115], v[0:1], off offset:-4096
	global_load_dwordx4 v[116:119], v[0:1], off
	v_mad_i64_i32 v[0:1], s[10:11], v41, s3, v[148:149]
	v_add_co_u32_e32 v0, vcc, s93, v0
	v_mov_b32_e32 v61, v48
	s_nop 0
	v_addc_co_u32_e32 v1, vcc, 0, v1, vcc
	global_load_dwordx4 v[120:123], v[0:1], off offset:-4096
	global_load_dwordx4 v[124:127], v[0:1], off
	v_mad_i64_i32 v[0:1], s[10:11], v42, s3, v[148:149]
	v_add_co_u32_e32 v0, vcc, s93, v0
	v_mov_b32_e32 v62, v48
	s_nop 0
	v_addc_co_u32_e32 v1, vcc, 0, v1, vcc
	global_load_dwordx4 v[128:131], v[0:1], off offset:-4096
	global_load_dwordx4 v[132:135], v[0:1], off
	v_mad_i64_i32 v[0:1], s[10:11], v43, s3, v[148:149]
	v_add_co_u32_e32 v0, vcc, s93, v0
	s_add_i32 s10, s43, s14
	s_nop 0
	v_addc_co_u32_e32 v1, vcc, 0, v1, vcc
	global_load_dwordx4 v[136:139], v[0:1], off offset:-4096
	global_load_dwordx4 v[140:143], v[0:1], off
	s_and_b32 s10, s10, 0xfffff000
	s_or_b32 s10, s56, s10
	ds_write_b128 v196, v[24:27] offset:8192
	ds_write_b128 v197, v[28:31] offset:8192
	v_add_u32_e32 v147, s10, v182
	v_add_u32_e32 v198, s10, v183
	v_add_u32_e32 v199, s10, v184
	v_add_u32_e32 v200, s10, v185
	v_add_u32_e32 v201, s10, v186
	v_add_u32_e32 v202, s10, v187
	v_add_u32_e32 v203, s10, v188
	v_add_u32_e32 v204, s10, v189
	v_mov_b32_e32 v63, v48
	v_mov_b32_e32 v32, v48
	v_mov_b32_e32 v33, v48
	v_mov_b32_e32 v34, v48
	v_mov_b32_e32 v35, v48
	v_mov_b32_e32 v36, v48
	v_mov_b32_e32 v37, v48
	v_mov_b32_e32 v38, v48
	v_mov_b32_e32 v39, v48
	v_mov_b32_e32 v40, v48
	v_mov_b32_e32 v41, v48
	v_mov_b32_e32 v42, v48
	v_mov_b32_e32 v43, v48
	v_mov_b32_e32 v44, v48
	v_mov_b32_e32 v45, v48
	v_mov_b32_e32 v46, v48
	v_mov_b32_e32 v47, v48
	v_mov_b32_e32 v16, v48
	v_mov_b32_e32 v17, v48
	v_mov_b32_e32 v18, v48
	v_mov_b32_e32 v19, v48
	v_mov_b32_e32 v20, v48
	v_mov_b32_e32 v21, v48
	v_mov_b32_e32 v22, v48
	v_mov_b32_e32 v23, v48
	v_mov_b32_e32 v24, v48
	v_mov_b32_e32 v25, v48
	v_mov_b32_e32 v26, v48
	v_mov_b32_e32 v27, v48
	v_mov_b32_e32 v28, v48
	v_mov_b32_e32 v29, v48
	v_mov_b32_e32 v30, v48
	v_mov_b32_e32 v31, v48
	v_mov_b32_e32 v0, v48
	v_mov_b32_e32 v1, v48
	v_mov_b32_e32 v2, v48
	v_mov_b32_e32 v3, v48
	v_mov_b32_e32 v4, v48
	v_mov_b32_e32 v5, v48
	v_mov_b32_e32 v6, v48
	v_mov_b32_e32 v7, v48
	v_mov_b32_e32 v8, v48
	v_mov_b32_e32 v9, v48
	v_mov_b32_e32 v10, v48
	v_mov_b32_e32 v11, v48
	v_mov_b32_e32 v12, v48
	v_mov_b32_e32 v13, v48
	v_mov_b32_e32 v14, v48
	v_mov_b32_e32 v15, v48
	s_branch .LBB0_455

.LBB0_455:
	v_mov_b32_e32 v206, v172
	s_cmp_lg_u32 s58, 0
	v_lshrrev_b32_e32 v64, 4, v206
	v_lshlrev_b32_e32 v66, 4, v206
	v_lshlrev_b32_e32 v65, 8, v64
	v_lshlrev_b32_e32 v64, 6, v64
	v_and_b32_e32 v66, 0xf0, v66
	v_xad_u32 v64, v64, v66, v65
	v_lshlrev_b32_e32 v65, 2, v206
	v_and_b32_e32 v168, 31, v206
	v_ashrrev_i32_e32 v169, 5, v206
	v_and_b32_e32 v65, 12, v65
	v_bfe_u32 v207, v206, 2, 2
	v_bitop3_b32 v65, v65, v169, v207 bitop3:0x36
	v_add_u32_e32 v158, s42, v64
	v_xad_u32 v159, v64, 16, s42
	v_xad_u32 v162, v64, 32, s42
	v_xad_u32 v163, v64, 48, s42
	v_lshlrev_b32_e32 v64, 8, v168
	v_lshl_add_u32 v166, v65, 4, v64
	s_waitcnt vmcnt(15)
	ds_write_b128 v158, v[80:83]
	s_waitcnt vmcnt(13)
	ds_write_b128 v159, v[88:91] offset:1024
	s_waitcnt vmcnt(11)
	ds_write_b128 v162, v[96:99] offset:2048
	s_waitcnt vmcnt(9)
	ds_write_b128 v163, v[104:107] offset:3072
	s_waitcnt vmcnt(7)
	ds_write_b128 v158, v[112:115] offset:4096
	s_waitcnt vmcnt(5)
	ds_write_b128 v159, v[120:123] offset:5120
	s_waitcnt vmcnt(3)
	ds_write_b128 v162, v[128:131] offset:6144
	s_waitcnt vmcnt(1)
	ds_write_b128 v163, v[136:139] offset:7168
	v_add_u32_e32 v218, s58, v204
	v_mad_i64_i32 v[80:81], s[98:99], v218, s3, v[216:217]
	global_load_dwordx4 v[80:83], v[80:81], off offset:-4096
	v_add_u32_e32 v218, s58, v203
	v_mad_i64_i32 v[88:89], s[98:99], v218, s3, v[216:217]
	global_load_dwordx4 v[88:91], v[88:89], off offset:-4096
	v_add_u32_e32 v218, s58, v202
	v_mad_i64_i32 v[96:97], s[98:99], v218, s3, v[216:217]
	global_load_dwordx4 v[96:99], v[96:97], off offset:-4096
	v_add_u32_e32 v218, s58, v201
	v_mad_i64_i32 v[104:105], s[98:99], v218, s3, v[216:217]
	global_load_dwordx4 v[104:107], v[104:105], off offset:-4096
	v_add_u32_e32 v218, s58, v200
	v_mad_i64_i32 v[112:113], s[98:99], v218, s3, v[216:217]
	global_load_dwordx4 v[112:115], v[112:113], off offset:-4096
	v_add_u32_e32 v218, s58, v199
	v_mad_i64_i32 v[120:121], s[98:99], v218, s3, v[216:217]
	global_load_dwordx4 v[120:123], v[120:121], off offset:-4096
	v_add_u32_e32 v218, s58, v198
	v_mad_i64_i32 v[128:129], s[98:99], v218, s3, v[216:217]
	global_load_dwordx4 v[128:131], v[128:129], off offset:-4096
	v_add_u32_e32 v218, s58, v147
	v_mad_i64_i32 v[136:137], s[98:99], v218, s3, v[216:217]
	global_load_dwordx4 v[136:139], v[136:137], off offset:-4096
	v_add_u32_e32 v68, s42, v166
	ds_read_b128 v[64:67], v68
	ds_read_b128 v[68:71], v68 offset:8192
	s_waitcnt lgkmcnt(0)
	v_mfma_f32_32x32x16_bf16 v[64:79], v[64:67], v[68:71], 0
	v_xad_u32 v154, v166, 32, s42
	ds_read_b128 v[150:153], v154
	ds_read_b128 v[154:157], v154 offset:8192
	v_xad_u32 v167, v166, 64, s42
	s_waitcnt lgkmcnt(0)
	v_mfma_f32_32x32x16_bf16 v[64:79], v[150:153], v[154:157], v[64:79]
	ds_read_b128 v[150:153], v167
	ds_read_b128 v[154:157], v167 offset:8192
	v_xor_b32_e32 v167, 0x60, v166
	v_add_u32_e32 v167, s42, v167
	s_waitcnt lgkmcnt(0)
	v_mfma_f32_32x32x16_bf16 v[64:79], v[150:153], v[154:157], v[64:79]
	ds_read_b128 v[150:153], v167
	ds_read_b128 v[154:157], v167 offset:8192
	v_xor_b32_e32 v167, 0x80, v166
	v_add_u32_e32 v167, s42, v167
	s_waitcnt lgkmcnt(0)
	v_mfma_f32_32x32x16_bf16 v[64:79], v[150:153], v[154:157], v[64:79]
	ds_read_b128 v[150:153], v167
	ds_read_b128 v[154:157], v167 offset:8192
	v_xor_b32_e32 v167, 0xa0, v166
	v_add_u32_e32 v167, s42, v167
	s_waitcnt lgkmcnt(0)
	v_mfma_f32_32x32x16_bf16 v[64:79], v[150:153], v[154:157], v[64:79]
	ds_read_b128 v[150:153], v167
	ds_read_b128 v[154:157], v167 offset:8192
	v_xor_b32_e32 v167, 0xc0, v166
	v_add_u32_e32 v167, s42, v167
	ds_read_b128 v[208:211], v167
	s_waitcnt lgkmcnt(1)
	v_mfma_f32_32x32x16_bf16 v[64:79], v[150:153], v[154:157], v[64:79]
	ds_read_b128 v[150:153], v167 offset:8192
	v_xor_b32_e32 v154, 0xe0, v166
	v_add_u32_e32 v166, s42, v154
	ds_read_b128 v[154:157], v166
	ds_read_b128 v[212:215], v166 offset:8192
	s_waitcnt lgkmcnt(0)
	ds_write_b128 v158, v[84:87]
	ds_write_b128 v159, v[92:95] offset:1024
	ds_write_b128 v162, v[100:103] offset:2048
	ds_write_b128 v163, v[108:111] offset:3072
	ds_write_b128 v158, v[116:119] offset:4096
	ds_write_b128 v159, v[124:127] offset:5120
	ds_write_b128 v162, v[132:135] offset:6144
	s_waitcnt vmcnt(8)
	ds_write_b128 v163, v[140:143] offset:7168
	v_add_u32_e32 v218, s58, v204
	v_mad_i64_i32 v[84:85], s[98:99], v218, s3, v[216:217]
	global_load_dwordx4 v[84:87], v[84:85], off
	v_add_u32_e32 v218, s58, v203
	v_mad_i64_i32 v[92:93], s[98:99], v218, s3, v[216:217]
	global_load_dwordx4 v[92:95], v[92:93], off
	v_add_u32_e32 v218, s58, v202
	v_mad_i64_i32 v[100:101], s[98:99], v218, s3, v[216:217]
	global_load_dwordx4 v[100:103], v[100:101], off
	v_add_u32_e32 v218, s58, v201
	v_mad_i64_i32 v[108:109], s[98:99], v218, s3, v[216:217]
	global_load_dwordx4 v[108:111], v[108:109], off
	v_add_u32_e32 v218, s58, v200
	v_mad_i64_i32 v[116:117], s[98:99], v218, s3, v[216:217]
	global_load_dwordx4 v[116:119], v[116:117], off
	v_add_u32_e32 v218, s58, v199
	v_mad_i64_i32 v[124:125], s[98:99], v218, s3, v[216:217]
	global_load_dwordx4 v[124:127], v[124:125], off
	v_add_u32_e32 v218, s58, v198
	v_mad_i64_i32 v[132:133], s[98:99], v218, s3, v[216:217]
	global_load_dwordx4 v[132:135], v[132:133], off
	v_add_u32_e32 v218, s58, v147
	v_mad_i64_i32 v[140:141], s[98:99], v218, s3, v[216:217]
	global_load_dwordx4 v[140:143], v[140:141], off
	s_waitcnt lgkmcnt(10)
	v_mfma_f32_32x32x16_bf16 v[64:79], v[208:211], v[150:153], v[64:79]
	s_waitcnt lgkmcnt(8)
	v_mfma_f32_32x32x16_bf16 v[64:79], v[154:157], v[212:215], v[64:79]
	s_nop 11
	v_mul_f32_e32 v64, 0x3db504f3, v64
	v_mul_f32_e32 v65, 0x3db504f3, v65
	v_min_f32_e32 v64, 0x42a00000, v64
	v_min_f32_e32 v65, 0x42a00000, v65
	v_mul_f32_e32 v67, 0x3db504f3, v67
	v_mul_f32_e32 v64, 0x3fb8aa3b, v64
	v_mul_f32_e32 v65, 0x3fb8aa3b, v65
	v_min_f32_e32 v67, 0x42a00000, v67
	v_exp_f32_e32 v64, v64
	v_exp_f32_e32 v65, v65
	v_mul_f32_e32 v67, 0x3fb8aa3b, v67
	v_exp_f32_e32 v152, v67
	v_mul_f32_e32 v67, 0x3db504f3, v68
	v_min_f32_e32 v67, 0x42a00000, v67
	v_mul_f32_e32 v67, 0x3fb8aa3b, v67
	v_add_f32_e32 v150, 1.0, v64
	v_add_f32_e32 v151, 1.0, v65
	v_exp_f32_e32 v68, v67
	v_mul_f32_e32 v67, 0x3db504f3, v69
	v_rcp_f32_e32 v154, v150
	v_rcp_f32_e32 v155, v151
	v_min_f32_e32 v67, 0x42a00000, v67
	v_mul_f32_e32 v67, 0x3fb8aa3b, v67
	v_exp_f32_e32 v69, v67
	v_pk_mul_f32 v[150:151], v[64:65], v[154:155]
	v_add_f32_e32 v65, 1.0, v152
	v_rcp_f32_e32 v67, v65
	v_add_f32_e32 v65, 1.0, v68
	v_rcp_f32_e32 v156, v65
	v_add_f32_e32 v65, 1.0, v69
	v_mul_f32_e32 v66, 0x3db504f3, v66
	v_rcp_f32_e32 v157, v65
	v_min_f32_e32 v66, 0x42a00000, v66
	v_mul_f32_e32 v66, 0x3fb8aa3b, v66
	v_exp_f32_e32 v66, v66
	v_mul_f32_e32 v210, v152, v67
	v_pk_mul_f32 v[152:153], v[68:69], v[156:157]
	v_mul_f32_e32 v68, 0x3db504f3, v71
	v_mul_f32_e32 v65, 0x3db504f3, v70
	v_min_f32_e32 v68, 0x42a00000, v68
	v_min_f32_e32 v65, 0x42a00000, v65
	v_mul_f32_e32 v68, 0x3fb8aa3b, v68
	v_add_f32_e32 v64, 1.0, v66
	v_mul_f32_e32 v65, 0x3fb8aa3b, v65
	v_exp_f32_e32 v162, v68
	v_mul_f32_e32 v68, 0x3db504f3, v72
	v_rcp_f32_e32 v64, v64
	v_exp_f32_e32 v65, v65
	v_min_f32_e32 v68, 0x42a00000, v68
	v_mul_f32_e32 v68, 0x3fb8aa3b, v68
	v_exp_f32_e32 v70, v68
	v_mul_f32_e32 v68, 0x3db504f3, v73
	v_min_f32_e32 v68, 0x42a00000, v68
	v_mul_f32_e32 v211, v66, v64
	v_add_f32_e32 v66, 1.0, v65
	v_mul_f32_e32 v68, 0x3fb8aa3b, v68
	v_rcp_f32_e32 v66, v66
	v_exp_f32_e32 v71, v68
	v_mul_f32_e32 v68, 0x3db504f3, v74
	v_min_f32_e32 v68, 0x42a00000, v68
	v_mul_f32_e32 v68, 0x3fb8aa3b, v68
	v_exp_f32_e32 v72, v68
	v_mul_f32_e32 v212, v65, v66
	v_add_f32_e32 v65, 1.0, v162
	v_rcp_f32_e32 v69, v65
	v_add_f32_e32 v65, 1.0, v70
	v_rcp_f32_e32 v158, v65
	v_add_f32_e32 v65, 1.0, v71
	v_rcp_f32_e32 v159, v65
	v_add_f32_e32 v65, 1.0, v72
	v_rcp_f32_e32 v68, v65
	v_mul_f32_e32 v65, 0x3db504f3, v75
	v_min_f32_e32 v65, 0x42a00000, v65
	v_mul_f32_e32 v65, 0x3fb8aa3b, v65
	v_exp_f32_e32 v65, v65
	v_pk_mul_f32 v[74:75], v[70:71], v[158:159]
	v_mul_f32_e32 v213, v72, v68
	v_mul_f32_e32 v214, v162, v69
	v_add_f32_e32 v70, 1.0, v65
	v_rcp_f32_e32 v71, v70
	v_mul_f32_e32 v70, 0x3db504f3, v76
	v_min_f32_e32 v70, 0x42a00000, v70
	v_mul_f32_e32 v70, 0x3fb8aa3b, v70
	v_exp_f32_e32 v72, v70
	v_mul_f32_e32 v70, 0x3db504f3, v77
	v_min_f32_e32 v70, 0x42a00000, v70
	v_mul_f32_e32 v70, 0x3fb8aa3b, v70
	v_exp_f32_e32 v73, v70
	v_mul_f32_e32 v70, 0x3db504f3, v78
	v_min_f32_e32 v70, 0x42a00000, v70
	v_mul_f32_e32 v70, 0x3fb8aa3b, v70
	v_exp_f32_e32 v76, v70
	v_mul_f32_e32 v70, 0x3db504f3, v79
	v_min_f32_e32 v70, 0x42a00000, v70
	v_mul_f32_e32 v70, 0x3fb8aa3b, v70
	v_exp_f32_e32 v77, v70
	v_mul_f32_e32 v215, v65, v71
	v_add_f32_e32 v65, 1.0, v72
	v_rcp_f32_e32 v166, v65
	v_add_f32_e32 v65, 1.0, v73
	v_rcp_f32_e32 v167, v65
	v_add_f32_e32 v65, 1.0, v76
	v_rcp_f32_e32 v70, v65
	v_add_f32_e32 v65, 1.0, v77
	v_rcp_f32_e32 v65, v65
	v_pk_mul_f32 v[72:73], v[72:73], v[166:167]
	v_mul_f32_e32 v208, v76, v70
	v_mul_f32_e32 v209, v77, v65
	s_cbranch_scc1 .LBB0_457
	v_lshlrev_b32_e32 v76, 2, v169
	v_or_b32_e32 v77, 1, v76
	v_cmp_lt_i32_e32 vcc, v76, v168
	v_cmp_lt_i32_e64 s[10:11], v77, v168
	v_or_b32_e32 v77, 2, v76
	v_cndmask_b32_e32 v150, 0, v150, vcc
	s_or_b64 s[70:71], s[10:11], vcc
	v_cmp_lt_i32_e32 vcc, v77, v168
	v_or_b32_e32 v77, 3, v76
	v_cmp_lt_i32_e64 s[12:13], v77, v168
	v_add_u32_e32 v77, 8, v76
	v_cmp_lt_i32_e64 s[14:15], v77, v168
	v_add_u32_e32 v77, 10, v76
	v_add_u32_e32 v78, 9, v76
	v_cmp_lt_i32_e64 s[16:17], v77, v168
	v_add_u32_e32 v77, 11, v76
	v_cndmask_b32_e32 v211, 0, v211, vcc
	s_or_b64 s[72:73], s[12:13], vcc
	v_cmp_lt_i32_e32 vcc, v78, v168
	v_cmp_lt_i32_e64 s[18:19], v77, v168
	s_or_b64 s[20:21], vcc, s[14:15]
	v_cndmask_b32_e64 v212, 0, v212, s[16:17]
	s_or_b64 s[16:17], s[18:19], s[16:17]
	s_or_b64 s[20:21], s[20:21], s[16:17]
	v_cndmask_b32_e64 v156, 1.0, v156, s[20:21]
	s_or_b64 s[20:21], s[20:21], s[72:73]
	v_cndmask_b32_e64 v151, 0, v151, s[10:11]
	s_or_b64 s[10:11], s[20:21], s[10:11]
	v_cndmask_b32_e32 v153, 0, v153, vcc
	v_cndmask_b32_e64 v155, 1.0, v155, s[10:11]
	s_or_b64 s[10:11], s[20:21], s[70:71]
	s_or_b64 vcc, s[16:17], vcc
	v_cndmask_b32_e64 v154, 1.0, v154, s[10:11]
	s_or_b64 s[10:11], vcc, s[14:15]
	v_add_u32_e32 v77, 16, v76
	v_cndmask_b32_e32 v157, 1.0, v157, vcc
	s_or_b64 vcc, s[10:11], s[12:13]
	v_cmp_lt_i32_e64 s[10:11], v77, v168
	v_add_u32_e32 v77, 18, v76
	v_cndmask_b32_e64 v210, 0, v210, s[12:13]
	v_cmp_lt_i32_e64 s[12:13], v77, v168
	v_add_u32_e32 v77, 19, v76
	v_cndmask_b32_e64 v152, 0, v152, s[14:15]
	v_add_u32_e32 v78, 17, v76
	v_cmp_lt_i32_e64 s[14:15], v77, v168
	v_cndmask_b32_e32 v67, 1.0, v67, vcc
	v_cmp_lt_i32_e32 vcc, v78, v168
	v_cndmask_b32_e64 v213, 0, v213, s[12:13]
	s_or_b64 s[12:13], s[14:15], s[12:13]
	v_cndmask_b32_e32 v75, 0, v75, vcc
	s_or_b64 vcc, s[12:13], vcc
	v_add_u32_e32 v77, 24, v76
	v_cndmask_b32_e64 v74, 0, v74, s[10:11]
	v_cndmask_b32_e32 v159, 1.0, v159, vcc
	s_or_b64 vcc, vcc, s[10:11]
	v_add_u32_e32 v78, 25, v76
	v_cmp_lt_i32_e64 s[10:11], v77, v168
	v_add_u32_e32 v77, 26, v76
	v_add_u32_e32 v76, 27, v76
	v_cndmask_b32_e64 v215, 0, v215, s[14:15]
	v_cndmask_b32_e64 v68, 1.0, v68, s[12:13]
	v_cndmask_b32_e64 v71, 1.0, v71, s[14:15]
	v_cmp_lt_i32_e64 s[12:13], v77, v168
	v_cmp_lt_i32_e64 s[14:15], v76, v168
	v_cndmask_b32_e32 v158, 1.0, v158, vcc
	v_cmp_lt_i32_e32 vcc, v78, v168
	v_cndmask_b32_e64 v208, 0, v208, s[12:13]
	s_or_b64 s[12:13], s[14:15], s[12:13]
	v_cndmask_b32_e32 v73, 0, v73, vcc
	s_or_b64 vcc, s[12:13], vcc
	v_cndmask_b32_e32 v167, 1.0, v167, vcc
	s_or_b64 vcc, vcc, s[10:11]
	v_cndmask_b32_e64 v214, 0, v214, s[18:19]
	v_cndmask_b32_e64 v66, 1.0, v66, s[16:17]
	v_cndmask_b32_e64 v64, 1.0, v64, s[20:21]
	v_cndmask_b32_e64 v69, 1.0, v69, s[18:19]
	v_cndmask_b32_e64 v72, 0, v72, s[10:11]
	v_cndmask_b32_e64 v209, 0, v209, s[14:15]
	v_cndmask_b32_e64 v70, 1.0, v70, s[12:13]
	v_cndmask_b32_e32 v166, 1.0, v166, vcc
	v_cndmask_b32_e64 v65, 1.0, v65, s[14:15]

.LBB0_950:
	s_andn2_b64 vcc, exec, s[4:5]
	s_cbranch_vccnz .LBB0_1024
	s_mov_b32 s99, 0
	s_branch .Lmp_entry
.Lmp_ret1:
.LBB0_988:
	v_readlane_b32 s64, v255, 19
	v_readlane_b32 s95, v255, 20
	s_mov_b32 s97, 0x8000
	s_mov_b32 s90, 0x3fb8aa3b

.LBB0_1001:
	s_mov_b32 s96, 0x10000
	s_branch .LBB0_1024
.LBB0_1004:
	s_or_b64 exec, exec, s[18:19]
	s_xor_b64 s[16:17], s[20:21], -1
	s_and_saveexec_b64 s[18:19], s[16:17]
	s_xor_b64 s[18:19], exec, s[18:19]
	s_cbranch_execz .LBB0_1006
	v_mov_b64_e32 v[0:1], s[6:7]
	flat_atomic_add v[0:1], v220 offset:512

.LBB0_1132:
	s_andn2_b64 vcc, exec, s[4:5]
	s_cbranch_vccnz .LBB0_387
	s_mov_b32 s99, 1
.Lmp_entry:
	v_mbcnt_lo_u32_b32 v162, -1, 0
	v_mbcnt_hi_u32_b32 v162, -1, v162
	v_lshlrev_b32_e32 v163, 4, v162
	v_lshlrev_b32_e32 v162, 3, v162
	v_readlane_b32 s4, v252, 0
	v_readlane_b32 s5, v252, 1
	v_readlane_b32 s6, v252, 2
	v_readlane_b32 s7, v252, 3
	v_readlane_b32 s8, v252, 4
	v_readlane_b32 s9, v252, 5
	s_nop 3
	s_load_dwordx2 s[10:11], s[8:9], 0x0
	s_load_dwordx2 s[90:91], s[8:9], 0x28
	s_lshr_b32 s18, s44, 6
	s_lshl_b32 s19, s101, 7
	s_add_u32 s18, s18, s19
	s_lshr_b32 s19, s101, 5
	s_lshl_b32 s76, s18, 12
	s_lshl_b32 s77, s18, 13
	s_lshl_b32 s88, s68, 3
	s_add_u32 s88, s88, s19
	s_mul_i32 s88, s88, 0xc000
	s_waitcnt lgkmcnt(0)
	s_add_u32 s72, s6, 0x19400000
	s_addc_u32 s73, s7, 0
	s_add_u32 s72, s72, s76
	s_addc_u32 s73, s73, 0
	s_add_u32 s94, s4, 0x8000000
	s_addc_u32 s95, s5, 0
	s_add_u32 s94, s94, s76
	s_addc_u32 s95, s95, 0
	s_add_u32 s56, s6, 0x100000
	s_addc_u32 s57, s7, 0
	s_add_u32 s56, s56, s88
	s_addc_u32 s57, s57, 0
	s_cmp_eq_u32 s99, 0
	s_cbranch_scc0 .Lmp_site1
	s_add_u32 s18, s56, 0x4000
	s_addc_u32 s19, s57, 0
	s_add_u32 s20, s56, 0x6000
	s_addc_u32 s21, s57, 0
	s_add_u32 s30, s56, 0x8000
	s_addc_u32 s31, s57, 0
	s_lshl_b32 s88, s68, 15
	s_add_u32 s88, s88, 0x2000
	s_add_u32 s34, s90, s88
	s_addc_u32 s35, s91, 0
	s_add_u32 s90, s34, 0x2000
	s_addc_u32 s91, s35, 0
	s_add_u32 s56, s6, 0x31400000
	s_addc_u32 s57, s7, 0
	s_add_u32 s56, s56, s76
	s_addc_u32 s57, s57, 0
	s_mov_b64 s[58:59], s[94:95]
	s_mov_b64 s[70:71], s[94:95]
	s_cmp_eq_u32 s68, 3
	s_cbranch_scc0 .Lmp_s0_notlast
	s_add_u32 s70, s6, 0x29400000
	s_addc_u32 s71, s7, 0
	s_add_u32 s70, s70, s76
	s_addc_u32 s71, s71, 0
.Lmp_s0_notlast:
	s_cmp_eq_u32 s68, 0
	s_cbranch_scc0 .Lmp_vec
	s_add_u32 s58, s10, s77
	s_addc_u32 s59, s11, 0
	s_branch .Lmp_vec
.Lmp_site1:
	s_add_u32 s18, s56, 0xa000
	s_addc_u32 s19, s57, 0
	s_add_u32 s20, s56, 0x60000
	s_addc_u32 s21, s57, 0
	s_add_u32 s30, s20, 0x2000
	s_addc_u32 s31, s21, 0
	s_lshl_b32 s88, s68, 15
	s_add_u32 s88, s88, 0x6000
	s_add_u32 s34, s90, s88
	s_addc_u32 s35, s91, 0
	s_add_u32 s90, s34, 0x2000
	s_addc_u32 s91, s35, 0
	s_add_u32 s56, s6, 0x21400000
	s_addc_u32 s57, s7, 0
	s_add_u32 s56, s56, s76
	s_addc_u32 s57, s57, 0
	s_mov_b64 s[58:59], s[94:95]
	s_mov_b64 s[70:71], s[94:95]
	s_cmp_eq_u32 s68, 3
	s_cbranch_scc0 .Lmp_vec
	s_add_u32 s58, s6, 0x29400000
	s_addc_u32 s59, s7, 0
	s_add_u32 s58, s58, s76
	s_addc_u32 s59, s59, 0
	s_add_u32 s70, s4, s77
	s_addc_u32 s71, s5, 0
.Lmp_vec:
	s_add_u32 s36, s18, 0x1000
	s_addc_u32 s37, s19, 0
	global_load_dwordx4 v[32:35], v163, s[18:19]
	global_load_dwordx4 v[36:39], v163, s[18:19] offset:1024
	global_load_dwordx4 v[40:43], v163, s[18:19] offset:2048
	global_load_dwordx4 v[44:47], v163, s[18:19] offset:3072
	global_load_dwordx4 v[48:51], v163, s[36:37]
	global_load_dwordx4 v[52:55], v163, s[36:37] offset:1024
	global_load_dwordx4 v[56:59], v163, s[36:37] offset:2048
	global_load_dwordx4 v[60:63], v163, s[36:37] offset:3072
	s_add_u32 s36, s34, 0x1000
	s_addc_u32 s37, s35, 0
	global_load_dwordx4 v[128:131], v163, s[34:35]
	global_load_dwordx4 v[132:135], v163, s[34:35] offset:1024
	global_load_dwordx4 v[136:139], v163, s[34:35] offset:2048
	global_load_dwordx4 v[140:143], v163, s[34:35] offset:3072
	global_load_dwordx4 v[144:147], v163, s[36:37]
	global_load_dwordx4 v[148:151], v163, s[36:37] offset:1024
	global_load_dwordx4 v[152:155], v163, s[36:37] offset:2048
	global_load_dwordx4 v[156:159], v163, s[36:37] offset:3072
	s_waitcnt vmcnt(0)
	v_mul_f32_e32 v32, v32, v128
	v_mul_f32_e32 v33, v33, v129
	v_mul_f32_e32 v34, v34, v130
	v_mul_f32_e32 v35, v35, v131
	v_mul_f32_e32 v36, v36, v132
	v_mul_f32_e32 v37, v37, v133
	v_mul_f32_e32 v38, v38, v134
	v_mul_f32_e32 v39, v39, v135
	v_mul_f32_e32 v40, v40, v136
	v_mul_f32_e32 v41, v41, v137
	v_mul_f32_e32 v42, v42, v138
	v_mul_f32_e32 v43, v43, v139
	v_mul_f32_e32 v44, v44, v140
	v_mul_f32_e32 v45, v45, v141
	v_mul_f32_e32 v46, v46, v142
	v_mul_f32_e32 v47, v47, v143
	v_mul_f32_e32 v48, v48, v144
	v_mul_f32_e32 v49, v49, v145
	v_mul_f32_e32 v50, v50, v146
	v_mul_f32_e32 v51, v51, v147
	v_mul_f32_e32 v52, v52, v148
	v_mul_f32_e32 v53, v53, v149
	v_mul_f32_e32 v54, v54, v150
	v_mul_f32_e32 v55, v55, v151
	v_mul_f32_e32 v56, v56, v152
	v_mul_f32_e32 v57, v57, v153
	v_mul_f32_e32 v58, v58, v154
	v_mul_f32_e32 v59, v59, v155
	v_mul_f32_e32 v60, v60, v156
	v_mul_f32_e32 v61, v61, v157
	v_mul_f32_e32 v62, v62, v158
	v_mul_f32_e32 v63, v63, v159
	s_cmp_eq_u32 s99, 1
	s_cselect_b32 s88, s68, 0
	s_cmp_eq_u32 s88, 3
	s_cbranch_scc1 .Lmp_noh
	s_add_u32 s36, s90, 0x1000
	s_addc_u32 s37, s91, 0
	global_load_dwordx4 v[64:67], v163, s[90:91]
	global_load_dwordx4 v[68:71], v163, s[90:91] offset:1024
	global_load_dwordx4 v[72:75], v163, s[90:91] offset:2048
	global_load_dwordx4 v[76:79], v163, s[90:91] offset:3072
	global_load_dwordx4 v[80:83], v163, s[36:37]
	global_load_dwordx4 v[84:87], v163, s[36:37] offset:1024
	global_load_dwordx4 v[88:91], v163, s[36:37] offset:2048
	global_load_dwordx4 v[92:95], v163, s[36:37] offset:3072
	s_add_u32 s36, s30, 0x1000
	s_addc_u32 s37, s31, 0
	global_load_dwordx4 v[166:169], v163, s[30:31]
	global_load_dwordx4 v[170:173], v163, s[30:31] offset:1024
	global_load_dwordx4 v[174:177], v163, s[30:31] offset:2048
	global_load_dwordx4 v[178:181], v163, s[30:31] offset:3072
	global_load_dwordx4 v[182:185], v163, s[36:37]
	global_load_dwordx4 v[186:189], v163, s[36:37] offset:1024
	global_load_dwordx4 v[190:193], v163, s[36:37] offset:2048
	global_load_dwordx4 v[194:197], v163, s[36:37] offset:3072
	s_add_u32 s36, s20, 0x1000
	s_addc_u32 s37, s21, 0
	global_load_dwordx4 v[96:99], v163, s[20:21]
	global_load_dwordx4 v[100:103], v163, s[20:21] offset:1024
	global_load_dwordx4 v[104:107], v163, s[20:21] offset:2048
	global_load_dwordx4 v[108:111], v163, s[20:21] offset:3072
	global_load_dwordx4 v[112:115], v163, s[36:37]
	global_load_dwordx4 v[116:119], v163, s[36:37] offset:1024
	global_load_dwordx4 v[120:123], v163, s[36:37] offset:2048
	global_load_dwordx4 v[124:127], v163, s[36:37] offset:3072
	s_waitcnt vmcnt(8)
	v_add_f32_e32 v166, 1.0, v166
	v_add_f32_e32 v167, 1.0, v167
	v_add_f32_e32 v168, 1.0, v168
	v_add_f32_e32 v169, 1.0, v169
	v_add_f32_e32 v170, 1.0, v170
	v_add_f32_e32 v171, 1.0, v171
	v_add_f32_e32 v172, 1.0, v172
	v_add_f32_e32 v173, 1.0, v173
	v_add_f32_e32 v174, 1.0, v174
	v_add_f32_e32 v175, 1.0, v175
	v_add_f32_e32 v176, 1.0, v176
	v_add_f32_e32 v177, 1.0, v177
	v_add_f32_e32 v178, 1.0, v178
	v_add_f32_e32 v179, 1.0, v179
	v_add_f32_e32 v180, 1.0, v180
	v_add_f32_e32 v181, 1.0, v181
	v_add_f32_e32 v182, 1.0, v182
	v_add_f32_e32 v183, 1.0, v183
	v_add_f32_e32 v184, 1.0, v184
	v_add_f32_e32 v185, 1.0, v185
	v_add_f32_e32 v186, 1.0, v186
	v_add_f32_e32 v187, 1.0, v187
	v_add_f32_e32 v188, 1.0, v188
	v_add_f32_e32 v189, 1.0, v189
	v_add_f32_e32 v190, 1.0, v190
	v_add_f32_e32 v191, 1.0, v191
	v_add_f32_e32 v192, 1.0, v192
	v_add_f32_e32 v193, 1.0, v193
	v_add_f32_e32 v194, 1.0, v194
	v_add_f32_e32 v195, 1.0, v195
	v_add_f32_e32 v196, 1.0, v196
	v_add_f32_e32 v197, 1.0, v197
	v_mul_f32_e32 v64, v64, v166
	v_mul_f32_e32 v65, v65, v167
	v_mul_f32_e32 v66, v66, v168
	v_mul_f32_e32 v67, v67, v169
	v_mul_f32_e32 v68, v68, v170
	v_mul_f32_e32 v69, v69, v171
	v_mul_f32_e32 v70, v70, v172
	v_mul_f32_e32 v71, v71, v173
	v_mul_f32_e32 v72, v72, v174
	v_mul_f32_e32 v73, v73, v175
	v_mul_f32_e32 v74, v74, v176
	v_mul_f32_e32 v75, v75, v177
	v_mul_f32_e32 v76, v76, v178
	v_mul_f32_e32 v77, v77, v179
	v_mul_f32_e32 v78, v78, v180
	v_mul_f32_e32 v79, v79, v181
	v_mul_f32_e32 v80, v80, v182
	v_mul_f32_e32 v81, v81, v183
	v_mul_f32_e32 v82, v82, v184
	v_mul_f32_e32 v83, v83, v185
	v_mul_f32_e32 v84, v84, v186
	v_mul_f32_e32 v85, v85, v187
	v_mul_f32_e32 v86, v86, v188
	v_mul_f32_e32 v87, v87, v189
	v_mul_f32_e32 v88, v88, v190
	v_mul_f32_e32 v89, v89, v191
	v_mul_f32_e32 v90, v90, v192
	v_mul_f32_e32 v91, v91, v193
	v_mul_f32_e32 v92, v92, v194
	v_mul_f32_e32 v93, v93, v195
	v_mul_f32_e32 v94, v94, v196
	v_mul_f32_e32 v95, v95, v197
	s_waitcnt vmcnt(0)
.Lmp_noh:
	s_mov_b32 s76, 0
	s_cmp_eq_u32 s99, 0
	s_cbranch_scc0 .Lmp_d1
	s_cmp_eq_u32 s68, 0
	s_cbranch_scc1 .Lmp_V2
	s_branch .Lmp_V1
.Lmp_d1:
	s_cmp_eq_u32 s68, 3
	s_cbranch_scc1 .Lmp_V3
.Lmp_V1:
	global_load_dwordx2 v[128:129], v162, s[56:57]
	global_load_dwordx2 v[130:131], v162, s[56:57] offset:512
	global_load_dwordx2 v[132:133], v162, s[56:57] offset:1024
	global_load_dwordx2 v[134:135], v162, s[56:57] offset:1536
	global_load_dwordx2 v[136:137], v162, s[56:57] offset:2048
	global_load_dwordx2 v[138:139], v162, s[56:57] offset:2560
	global_load_dwordx2 v[140:141], v162, s[56:57] offset:3072
	global_load_dwordx2 v[142:143], v162, s[56:57] offset:3584
	global_load_dwordx2 v[144:145], v162, s[58:59]
	global_load_dwordx2 v[146:147], v162, s[58:59] offset:512
	global_load_dwordx2 v[148:149], v162, s[58:59] offset:1024
	global_load_dwordx2 v[150:151], v162, s[58:59] offset:1536
	global_load_dwordx2 v[152:153], v162, s[58:59] offset:2048
	global_load_dwordx2 v[154:155], v162, s[58:59] offset:2560
	global_load_dwordx2 v[156:157], v162, s[58:59] offset:3072
	global_load_dwordx2 v[158:159], v162, s[58:59] offset:3584
	s_add_u32 s58, s58, 0x8000
	s_addc_u32 s59, s59, 0
	s_add_u32 s56, s56, 0x8000
	s_addc_u32 s57, s57, 0
	global_load_dwordx2 v[166:167], v162, s[56:57]
	global_load_dwordx2 v[168:169], v162, s[56:57] offset:512
	global_load_dwordx2 v[170:171], v162, s[56:57] offset:1024
	global_load_dwordx2 v[172:173], v162, s[56:57] offset:1536
	global_load_dwordx2 v[174:175], v162, s[56:57] offset:2048
	global_load_dwordx2 v[176:177], v162, s[56:57] offset:2560
	global_load_dwordx2 v[178:179], v162, s[56:57] offset:3072
	global_load_dwordx2 v[180:181], v162, s[56:57] offset:3584
	global_load_dwordx2 v[182:183], v162, s[58:59]
	global_load_dwordx2 v[184:185], v162, s[58:59] offset:512
	global_load_dwordx2 v[186:187], v162, s[58:59] offset:1024
	global_load_dwordx2 v[188:189], v162, s[58:59] offset:1536
	global_load_dwordx2 v[190:191], v162, s[58:59] offset:2048
	global_load_dwordx2 v[192:193], v162, s[58:59] offset:2560
	global_load_dwordx2 v[194:195], v162, s[58:59] offset:3072
	global_load_dwordx2 v[196:197], v162, s[58:59] offset:3584
	s_add_u32 s58, s58, 0x8000
	s_addc_u32 s59, s59, 0
	s_add_u32 s56, s56, 0x8000
	s_addc_u32 s57, s57, 0
	s_waitcnt vmcnt(16)
.Lmp_V1_loop:
	s_waitcnt vmcnt(32)
	v_mov_b32_e32 v250, 0
	v_mov_b32_e32 v251, 0
	v_lshlrev_b32_e32 v246, 16, v128
	v_and_b32_e32 v247, 0xffff0000, v128
	v_lshlrev_b32_e32 v248, 16, v129
	v_and_b32_e32 v249, 0xffff0000, v129
	v_fmac_f32_e32 v250, v246, v246
	v_fmac_f32_e32 v251, v247, v247
	v_fmac_f32_e32 v250, v248, v248
	v_fmac_f32_e32 v251, v249, v249
	v_lshlrev_b32_e32 v246, 16, v130
	v_and_b32_e32 v247, 0xffff0000, v130
	v_lshlrev_b32_e32 v248, 16, v131
	v_and_b32_e32 v249, 0xffff0000, v131
	v_fmac_f32_e32 v250, v246, v246
	v_fmac_f32_e32 v251, v247, v247
	v_fmac_f32_e32 v250, v248, v248
	v_fmac_f32_e32 v251, v249, v249
	v_lshlrev_b32_e32 v246, 16, v132
	v_and_b32_e32 v247, 0xffff0000, v132
	v_lshlrev_b32_e32 v248, 16, v133
	v_and_b32_e32 v249, 0xffff0000, v133
	v_fmac_f32_e32 v250, v246, v246
	v_fmac_f32_e32 v251, v247, v247
	v_fmac_f32_e32 v250, v248, v248
	v_fmac_f32_e32 v251, v249, v249
	v_lshlrev_b32_e32 v246, 16, v134
	v_and_b32_e32 v247, 0xffff0000, v134
	v_lshlrev_b32_e32 v248, 16, v135
	v_and_b32_e32 v249, 0xffff0000, v135
	v_fmac_f32_e32 v250, v246, v246
	v_fmac_f32_e32 v251, v247, v247
	v_fmac_f32_e32 v250, v248, v248
	v_fmac_f32_e32 v251, v249, v249
	v_lshlrev_b32_e32 v246, 16, v136
	v_and_b32_e32 v247, 0xffff0000, v136
	v_lshlrev_b32_e32 v248, 16, v137
	v_and_b32_e32 v249, 0xffff0000, v137
	v_fmac_f32_e32 v250, v246, v246
	v_fmac_f32_e32 v251, v247, v247
	v_fmac_f32_e32 v250, v248, v248
	v_fmac_f32_e32 v251, v249, v249
	v_lshlrev_b32_e32 v246, 16, v138
	v_and_b32_e32 v247, 0xffff0000, v138
	v_lshlrev_b32_e32 v248, 16, v139
	v_and_b32_e32 v249, 0xffff0000, v139
	v_fmac_f32_e32 v250, v246, v246
	v_fmac_f32_e32 v251, v247, v247
	v_fmac_f32_e32 v250, v248, v248
	v_fmac_f32_e32 v251, v249, v249
	v_lshlrev_b32_e32 v246, 16, v140
	v_and_b32_e32 v247, 0xffff0000, v140
	v_lshlrev_b32_e32 v248, 16, v141
	v_and_b32_e32 v249, 0xffff0000, v141
	v_fmac_f32_e32 v250, v246, v246
	v_fmac_f32_e32 v251, v247, v247
	v_fmac_f32_e32 v250, v248, v248
	v_fmac_f32_e32 v251, v249, v249
	v_lshlrev_b32_e32 v246, 16, v142
	v_and_b32_e32 v247, 0xffff0000, v142
	v_lshlrev_b32_e32 v248, 16, v143
	v_and_b32_e32 v249, 0xffff0000, v143
	v_fmac_f32_e32 v250, v246, v246
	v_fmac_f32_e32 v251, v247, v247
	v_fmac_f32_e32 v250, v248, v248
	v_fmac_f32_e32 v251, v249, v249
	v_add_f32_e32 v250, v250, v251
	s_nop 1
	v_add_f32_dpp v218, v250, v250 quad_perm:[1,0,3,2] row_mask:0xf bank_mask:0xf bound_ctrl:1
	s_nop 1
	v_add_f32_dpp v218, v218, v218 quad_perm:[2,3,0,1] row_mask:0xf bank_mask:0xf bound_ctrl:1
	s_nop 1
	v_add_f32_dpp v218, v218, v218 row_ror:4 row_mask:0xf bank_mask:0xf bound_ctrl:1
	s_nop 1
	v_add_f32_dpp v218, v218, v218 row_ror:8 row_mask:0xf bank_mask:0xf bound_ctrl:1
	s_nop 1
	v_readlane_b32 s8, v218, 0
	v_readlane_b32 s9, v218, 16
	v_readlane_b32 s10, v218, 32
	v_readlane_b32 s11, v218, 48
	s_nop 1
	v_mov_b32_e32 v218, s8
	v_add_f32_e32 v218, s9, v218
	v_mov_b32_e32 v219, s10
	v_add_f32_e32 v219, s11, v219
	v_add_f32_e32 v218, v218, v219
	v_mul_f32_e32 v218, 0x3a000000, v218
	v_add_f32_e32 v218, 0x358637bd, v218
	v_rsq_f32_e32 v218, v218
	s_nop 0
	v_lshlrev_b32_e32 v246, 16, v128
	v_and_b32_e32 v247, 0xffff0000, v128
	v_lshlrev_b32_e32 v248, 16, v129
	v_and_b32_e32 v249, 0xffff0000, v129
	v_mul_f32_e32 v246, v246, v218
	v_mul_f32_e32 v247, v247, v218
	v_mul_f32_e32 v248, v248, v218
	v_mul_f32_e32 v249, v249, v218
	v_lshlrev_b32_e32 v0, 16, v144
	v_and_b32_e32 v1, 0xffff0000, v144
	v_lshlrev_b32_e32 v2, 16, v145
	v_and_b32_e32 v3, 0xffff0000, v145
	v_fmac_f32_e32 v0, v246, v32
	v_fmac_f32_e32 v1, v247, v33
	v_fmac_f32_e32 v2, v248, v34
	v_fmac_f32_e32 v3, v249, v35
	v_lshlrev_b32_e32 v246, 16, v130
	v_and_b32_e32 v247, 0xffff0000, v130
	v_lshlrev_b32_e32 v248, 16, v131
	v_and_b32_e32 v249, 0xffff0000, v131
	v_mul_f32_e32 v246, v246, v218
	v_mul_f32_e32 v247, v247, v218
	v_mul_f32_e32 v248, v248, v218
	v_mul_f32_e32 v249, v249, v218
	v_lshlrev_b32_e32 v4, 16, v146
	v_and_b32_e32 v5, 0xffff0000, v146
	v_lshlrev_b32_e32 v6, 16, v147
	v_and_b32_e32 v7, 0xffff0000, v147
	v_fmac_f32_e32 v4, v246, v36
	v_fmac_f32_e32 v5, v247, v37
	v_fmac_f32_e32 v6, v248, v38
	v_fmac_f32_e32 v7, v249, v39
	v_lshlrev_b32_e32 v246, 16, v132
	v_and_b32_e32 v247, 0xffff0000, v132
	v_lshlrev_b32_e32 v248, 16, v133
	v_and_b32_e32 v249, 0xffff0000, v133
	v_mul_f32_e32 v246, v246, v218
	v_mul_f32_e32 v247, v247, v218
	v_mul_f32_e32 v248, v248, v218
	v_mul_f32_e32 v249, v249, v218
	v_lshlrev_b32_e32 v8, 16, v148
	v_and_b32_e32 v9, 0xffff0000, v148
	v_lshlrev_b32_e32 v10, 16, v149
	v_and_b32_e32 v11, 0xffff0000, v149
	v_fmac_f32_e32 v8, v246, v40
	v_fmac_f32_e32 v9, v247, v41
	v_fmac_f32_e32 v10, v248, v42
	v_fmac_f32_e32 v11, v249, v43
	v_lshlrev_b32_e32 v246, 16, v134
	v_and_b32_e32 v247, 0xffff0000, v134
	v_lshlrev_b32_e32 v248, 16, v135
	v_and_b32_e32 v249, 0xffff0000, v135
	v_mul_f32_e32 v246, v246, v218
	v_mul_f32_e32 v247, v247, v218
	v_mul_f32_e32 v248, v248, v218
	v_mul_f32_e32 v249, v249, v218
	v_lshlrev_b32_e32 v12, 16, v150
	v_and_b32_e32 v13, 0xffff0000, v150
	v_lshlrev_b32_e32 v14, 16, v151
	v_and_b32_e32 v15, 0xffff0000, v151
	v_fmac_f32_e32 v12, v246, v44
	v_fmac_f32_e32 v13, v247, v45
	v_fmac_f32_e32 v14, v248, v46
	v_fmac_f32_e32 v15, v249, v47
	v_lshlrev_b32_e32 v246, 16, v136
	v_and_b32_e32 v247, 0xffff0000, v136
	v_lshlrev_b32_e32 v248, 16, v137
	v_and_b32_e32 v249, 0xffff0000, v137
	v_mul_f32_e32 v246, v246, v218
	v_mul_f32_e32 v247, v247, v218
	v_mul_f32_e32 v248, v248, v218
	v_mul_f32_e32 v249, v249, v218
	v_lshlrev_b32_e32 v16, 16, v152
	v_and_b32_e32 v17, 0xffff0000, v152
	v_lshlrev_b32_e32 v18, 16, v153
	v_and_b32_e32 v19, 0xffff0000, v153
	v_fmac_f32_e32 v16, v246, v48
	v_fmac_f32_e32 v17, v247, v49
	v_fmac_f32_e32 v18, v248, v50
	v_fmac_f32_e32 v19, v249, v51
	v_lshlrev_b32_e32 v246, 16, v138
	v_and_b32_e32 v247, 0xffff0000, v138
	v_lshlrev_b32_e32 v248, 16, v139
	v_and_b32_e32 v249, 0xffff0000, v139
	v_mul_f32_e32 v246, v246, v218
	v_mul_f32_e32 v247, v247, v218
	v_mul_f32_e32 v248, v248, v218
	v_mul_f32_e32 v249, v249, v218
	v_lshlrev_b32_e32 v20, 16, v154
	v_and_b32_e32 v21, 0xffff0000, v154
	v_lshlrev_b32_e32 v22, 16, v155
	v_and_b32_e32 v23, 0xffff0000, v155
	v_fmac_f32_e32 v20, v246, v52
	v_fmac_f32_e32 v21, v247, v53
	v_fmac_f32_e32 v22, v248, v54
	v_fmac_f32_e32 v23, v249, v55
	v_lshlrev_b32_e32 v246, 16, v140
	v_and_b32_e32 v247, 0xffff0000, v140
	v_lshlrev_b32_e32 v248, 16, v141
	v_and_b32_e32 v249, 0xffff0000, v141
	v_mul_f32_e32 v246, v246, v218
	v_mul_f32_e32 v247, v247, v218
	v_mul_f32_e32 v248, v248, v218
	v_mul_f32_e32 v249, v249, v218
	v_lshlrev_b32_e32 v24, 16, v156
	v_and_b32_e32 v25, 0xffff0000, v156
	v_lshlrev_b32_e32 v26, 16, v157
	v_and_b32_e32 v27, 0xffff0000, v157
	v_fmac_f32_e32 v24, v246, v56
	v_fmac_f32_e32 v25, v247, v57
	v_fmac_f32_e32 v26, v248, v58
	v_fmac_f32_e32 v27, v249, v59
	v_lshlrev_b32_e32 v246, 16, v142
	v_and_b32_e32 v247, 0xffff0000, v142
	v_lshlrev_b32_e32 v248, 16, v143
	v_and_b32_e32 v249, 0xffff0000, v143
	v_mul_f32_e32 v246, v246, v218
	v_mul_f32_e32 v247, v247, v218
	v_mul_f32_e32 v248, v248, v218
	v_mul_f32_e32 v249, v249, v218
	v_lshlrev_b32_e32 v28, 16, v158
	v_and_b32_e32 v29, 0xffff0000, v158
	v_lshlrev_b32_e32 v30, 16, v159
	v_and_b32_e32 v31, 0xffff0000, v159
	v_fmac_f32_e32 v28, v246, v60
	v_fmac_f32_e32 v29, v247, v61
	v_fmac_f32_e32 v30, v248, v62
	v_fmac_f32_e32 v31, v249, v63
	global_load_dwordx2 v[128:129], v162, s[56:57]
	global_load_dwordx2 v[130:131], v162, s[56:57] offset:512
	global_load_dwordx2 v[132:133], v162, s[56:57] offset:1024
	global_load_dwordx2 v[134:135], v162, s[56:57] offset:1536
	global_load_dwordx2 v[136:137], v162, s[56:57] offset:2048
	global_load_dwordx2 v[138:139], v162, s[56:57] offset:2560
	global_load_dwordx2 v[140:141], v162, s[56:57] offset:3072
	global_load_dwordx2 v[142:143], v162, s[56:57] offset:3584
	global_load_dwordx2 v[144:145], v162, s[58:59]
	global_load_dwordx2 v[146:147], v162, s[58:59] offset:512
	global_load_dwordx2 v[148:149], v162, s[58:59] offset:1024
	global_load_dwordx2 v[150:151], v162, s[58:59] offset:1536
	global_load_dwordx2 v[152:153], v162, s[58:59] offset:2048
	global_load_dwordx2 v[154:155], v162, s[58:59] offset:2560
	global_load_dwordx2 v[156:157], v162, s[58:59] offset:3072
	global_load_dwordx2 v[158:159], v162, s[58:59] offset:3584
	s_add_u32 s58, s58, 0x8000
	s_addc_u32 s59, s59, 0
	s_add_u32 s56, s56, 0x8000
	s_addc_u32 s57, s57, 0
	v_mov_b32_e32 v250, 0
	v_mov_b32_e32 v251, 0
	v_cvt_pk_bf16_f32 v238, v0, v1
	v_cvt_pk_bf16_f32 v239, v2, v3
	v_fmac_f32_e32 v250, v0, v0
	v_fmac_f32_e32 v251, v1, v1
	v_fmac_f32_e32 v250, v2, v2
	v_fmac_f32_e32 v251, v3, v3
	global_store_dwordx2 v162, v[238:239], s[70:71]
	v_cvt_pk_bf16_f32 v240, v4, v5
	v_cvt_pk_bf16_f32 v241, v6, v7
	v_fmac_f32_e32 v250, v4, v4
	v_fmac_f32_e32 v251, v5, v5
	v_fmac_f32_e32 v250, v6, v6
	v_fmac_f32_e32 v251, v7, v7
	global_store_dwordx2 v162, v[240:241], s[70:71] offset:512
	v_cvt_pk_bf16_f32 v242, v8, v9
	v_cvt_pk_bf16_f32 v243, v10, v11
	v_fmac_f32_e32 v250, v8, v8
	v_fmac_f32_e32 v251, v9, v9
	v_fmac_f32_e32 v250, v10, v10
	v_fmac_f32_e32 v251, v11, v11
	global_store_dwordx2 v162, v[242:243], s[70:71] offset:1024
	v_cvt_pk_bf16_f32 v244, v12, v13
	v_cvt_pk_bf16_f32 v245, v14, v15
	v_fmac_f32_e32 v250, v12, v12
	v_fmac_f32_e32 v251, v13, v13
	v_fmac_f32_e32 v250, v14, v14
	v_fmac_f32_e32 v251, v15, v15
	global_store_dwordx2 v162, v[244:245], s[70:71] offset:1536
	v_cvt_pk_bf16_f32 v238, v16, v17
	v_cvt_pk_bf16_f32 v239, v18, v19
	v_fmac_f32_e32 v250, v16, v16
	v_fmac_f32_e32 v251, v17, v17
	v_fmac_f32_e32 v250, v18, v18
	v_fmac_f32_e32 v251, v19, v19
	global_store_dwordx2 v162, v[238:239], s[70:71] offset:2048
	v_cvt_pk_bf16_f32 v240, v20, v21
	v_cvt_pk_bf16_f32 v241, v22, v23
	v_fmac_f32_e32 v250, v20, v20
	v_fmac_f32_e32 v251, v21, v21
	v_fmac_f32_e32 v250, v22, v22
	v_fmac_f32_e32 v251, v23, v23
	global_store_dwordx2 v162, v[240:241], s[70:71] offset:2560
	v_cvt_pk_bf16_f32 v242, v24, v25
	v_cvt_pk_bf16_f32 v243, v26, v27
	v_fmac_f32_e32 v250, v24, v24
	v_fmac_f32_e32 v251, v25, v25
	v_fmac_f32_e32 v250, v26, v26
	v_fmac_f32_e32 v251, v27, v27
	global_store_dwordx2 v162, v[242:243], s[70:71] offset:3072
	v_cvt_pk_bf16_f32 v244, v28, v29
	v_cvt_pk_bf16_f32 v245, v30, v31
	v_fmac_f32_e32 v250, v28, v28
	v_fmac_f32_e32 v251, v29, v29
	v_fmac_f32_e32 v250, v30, v30
	v_fmac_f32_e32 v251, v31, v31
	global_store_dwordx2 v162, v[244:245], s[70:71] offset:3584
	s_add_u32 s70, s70, 0x8000
	s_addc_u32 s71, s71, 0
	v_add_f32_e32 v250, v250, v251
	s_nop 1
	v_add_f32_dpp v218, v250, v250 quad_perm:[1,0,3,2] row_mask:0xf bank_mask:0xf bound_ctrl:1
	s_nop 1
	v_add_f32_dpp v218, v218, v218 quad_perm:[2,3,0,1] row_mask:0xf bank_mask:0xf bound_ctrl:1
	s_nop 1
	v_add_f32_dpp v218, v218, v218 row_ror:4 row_mask:0xf bank_mask:0xf bound_ctrl:1
	s_nop 1
	v_add_f32_dpp v218, v218, v218 row_ror:8 row_mask:0xf bank_mask:0xf bound_ctrl:1
	s_nop 1
	v_readlane_b32 s8, v218, 0
	v_readlane_b32 s9, v218, 16
	v_readlane_b32 s10, v218, 32
	v_readlane_b32 s11, v218, 48
	s_nop 1
	v_mov_b32_e32 v218, s8
	v_add_f32_e32 v218, s9, v218
	v_mov_b32_e32 v219, s10
	v_add_f32_e32 v219, s11, v219
	v_add_f32_e32 v218, v218, v219
	v_mul_f32_e32 v218, 0x3a000000, v218
	v_add_f32_e32 v218, 0x358637bd, v218
	v_rsq_f32_e32 v218, v218
	s_nop 0
	v_mul_f32_e32 v246, v0, v218
	v_mul_f32_e32 v247, v1, v218
	v_mul_f32_e32 v248, v2, v218
	v_mul_f32_e32 v249, v3, v218
	v_fma_f32 v246, v246, v64, v96
	v_fma_f32 v247, v247, v65, v97
	v_fma_f32 v248, v248, v66, v98
	v_fma_f32 v249, v249, v67, v99
	v_cvt_pk_bf16_f32 v238, v246, v247
	v_cvt_pk_bf16_f32 v239, v248, v249
	global_store_dwordx2 v162, v[238:239], s[72:73]
	v_mul_f32_e32 v246, v4, v218
	v_mul_f32_e32 v247, v5, v218
	v_mul_f32_e32 v248, v6, v218
	v_mul_f32_e32 v249, v7, v218
	v_fma_f32 v246, v246, v68, v100
	v_fma_f32 v247, v247, v69, v101
	v_fma_f32 v248, v248, v70, v102
	v_fma_f32 v249, v249, v71, v103
	v_cvt_pk_bf16_f32 v240, v246, v247
	v_cvt_pk_bf16_f32 v241, v248, v249
	global_store_dwordx2 v162, v[240:241], s[72:73] offset:512
	v_mul_f32_e32 v246, v8, v218
	v_mul_f32_e32 v247, v9, v218
	v_mul_f32_e32 v248, v10, v218
	v_mul_f32_e32 v249, v11, v218
	v_fma_f32 v246, v246, v72, v104
	v_fma_f32 v247, v247, v73, v105
	v_fma_f32 v248, v248, v74, v106
	v_fma_f32 v249, v249, v75, v107
	v_cvt_pk_bf16_f32 v242, v246, v247
	v_cvt_pk_bf16_f32 v243, v248, v249
	global_store_dwordx2 v162, v[242:243], s[72:73] offset:1024
	v_mul_f32_e32 v246, v12, v218
	v_mul_f32_e32 v247, v13, v218
	v_mul_f32_e32 v248, v14, v218
	v_mul_f32_e32 v249, v15, v218
	v_fma_f32 v246, v246, v76, v108
	v_fma_f32 v247, v247, v77, v109
	v_fma_f32 v248, v248, v78, v110
	v_fma_f32 v249, v249, v79, v111
	v_cvt_pk_bf16_f32 v244, v246, v247
	v_cvt_pk_bf16_f32 v245, v248, v249
	global_store_dwordx2 v162, v[244:245], s[72:73] offset:1536
	v_mul_f32_e32 v246, v16, v218
	v_mul_f32_e32 v247, v17, v218
	v_mul_f32_e32 v248, v18, v218
	v_mul_f32_e32 v249, v19, v218
	v_fma_f32 v246, v246, v80, v112
	v_fma_f32 v247, v247, v81, v113
	v_fma_f32 v248, v248, v82, v114
	v_fma_f32 v249, v249, v83, v115
	v_cvt_pk_bf16_f32 v238, v246, v247
	v_cvt_pk_bf16_f32 v239, v248, v249
	global_store_dwordx2 v162, v[238:239], s[72:73] offset:2048
	v_mul_f32_e32 v246, v20, v218
	v_mul_f32_e32 v247, v21, v218
	v_mul_f32_e32 v248, v22, v218
	v_mul_f32_e32 v249, v23, v218
	v_fma_f32 v246, v246, v84, v116
	v_fma_f32 v247, v247, v85, v117
	v_fma_f32 v248, v248, v86, v118
	v_fma_f32 v249, v249, v87, v119
	v_cvt_pk_bf16_f32 v240, v246, v247
	v_cvt_pk_bf16_f32 v241, v248, v249
	global_store_dwordx2 v162, v[240:241], s[72:73] offset:2560
	v_mul_f32_e32 v246, v24, v218
	v_mul_f32_e32 v247, v25, v218
	v_mul_f32_e32 v248, v26, v218
	v_mul_f32_e32 v249, v27, v218
	v_fma_f32 v246, v246, v88, v120
	v_fma_f32 v247, v247, v89, v121
	v_fma_f32 v248, v248, v90, v122
	v_fma_f32 v249, v249, v91, v123
	v_cvt_pk_bf16_f32 v242, v246, v247
	v_cvt_pk_bf16_f32 v243, v248, v249
	global_store_dwordx2 v162, v[242:243], s[72:73] offset:3072
	v_mul_f32_e32 v246, v28, v218
	v_mul_f32_e32 v247, v29, v218
	v_mul_f32_e32 v248, v30, v218
	v_mul_f32_e32 v249, v31, v218
	v_fma_f32 v246, v246, v92, v124
	v_fma_f32 v247, v247, v93, v125
	v_fma_f32 v248, v248, v94, v126
	v_fma_f32 v249, v249, v95, v127
	v_cvt_pk_bf16_f32 v244, v246, v247
	v_cvt_pk_bf16_f32 v245, v248, v249
	global_store_dwordx2 v162, v[244:245], s[72:73] offset:3584
	s_add_u32 s72, s72, 0x8000
	s_addc_u32 s73, s73, 0
	s_waitcnt vmcnt(32)
	v_mov_b32_e32 v250, 0
	v_mov_b32_e32 v251, 0
	v_lshlrev_b32_e32 v246, 16, v166
	v_and_b32_e32 v247, 0xffff0000, v166
	v_lshlrev_b32_e32 v248, 16, v167
	v_and_b32_e32 v249, 0xffff0000, v167
	v_fmac_f32_e32 v250, v246, v246
	v_fmac_f32_e32 v251, v247, v247
	v_fmac_f32_e32 v250, v248, v248
	v_fmac_f32_e32 v251, v249, v249
	v_lshlrev_b32_e32 v246, 16, v168
	v_and_b32_e32 v247, 0xffff0000, v168
	v_lshlrev_b32_e32 v248, 16, v169
	v_and_b32_e32 v249, 0xffff0000, v169
	v_fmac_f32_e32 v250, v246, v246
	v_fmac_f32_e32 v251, v247, v247
	v_fmac_f32_e32 v250, v248, v248
	v_fmac_f32_e32 v251, v249, v249
	v_lshlrev_b32_e32 v246, 16, v170
	v_and_b32_e32 v247, 0xffff0000, v170
	v_lshlrev_b32_e32 v248, 16, v171
	v_and_b32_e32 v249, 0xffff0000, v171
	v_fmac_f32_e32 v250, v246, v246
	v_fmac_f32_e32 v251, v247, v247
	v_fmac_f32_e32 v250, v248, v248
	v_fmac_f32_e32 v251, v249, v249
	v_lshlrev_b32_e32 v246, 16, v172
	v_and_b32_e32 v247, 0xffff0000, v172
	v_lshlrev_b32_e32 v248, 16, v173
	v_and_b32_e32 v249, 0xffff0000, v173
	v_fmac_f32_e32 v250, v246, v246
	v_fmac_f32_e32 v251, v247, v247
	v_fmac_f32_e32 v250, v248, v248
	v_fmac_f32_e32 v251, v249, v249
	v_lshlrev_b32_e32 v246, 16, v174
	v_and_b32_e32 v247, 0xffff0000, v174
	v_lshlrev_b32_e32 v248, 16, v175
	v_and_b32_e32 v249, 0xffff0000, v175
	v_fmac_f32_e32 v250, v246, v246
	v_fmac_f32_e32 v251, v247, v247
	v_fmac_f32_e32 v250, v248, v248
	v_fmac_f32_e32 v251, v249, v249
	v_lshlrev_b32_e32 v246, 16, v176
	v_and_b32_e32 v247, 0xffff0000, v176
	v_lshlrev_b32_e32 v248, 16, v177
	v_and_b32_e32 v249, 0xffff0000, v177
	v_fmac_f32_e32 v250, v246, v246
	v_fmac_f32_e32 v251, v247, v247
	v_fmac_f32_e32 v250, v248, v248
	v_fmac_f32_e32 v251, v249, v249
	v_lshlrev_b32_e32 v246, 16, v178
	v_and_b32_e32 v247, 0xffff0000, v178
	v_lshlrev_b32_e32 v248, 16, v179
	v_and_b32_e32 v249, 0xffff0000, v179
	v_fmac_f32_e32 v250, v246, v246
	v_fmac_f32_e32 v251, v247, v247
	v_fmac_f32_e32 v250, v248, v248
	v_fmac_f32_e32 v251, v249, v249
	v_lshlrev_b32_e32 v246, 16, v180
	v_and_b32_e32 v247, 0xffff0000, v180
	v_lshlrev_b32_e32 v248, 16, v181
	v_and_b32_e32 v249, 0xffff0000, v181
	v_fmac_f32_e32 v250, v246, v246
	v_fmac_f32_e32 v251, v247, v247
	v_fmac_f32_e32 v250, v248, v248
	v_fmac_f32_e32 v251, v249, v249
	v_add_f32_e32 v250, v250, v251
	s_nop 1
	v_add_f32_dpp v218, v250, v250 quad_perm:[1,0,3,2] row_mask:0xf bank_mask:0xf bound_ctrl:1
	s_nop 1
	v_add_f32_dpp v218, v218, v218 quad_perm:[2,3,0,1] row_mask:0xf bank_mask:0xf bound_ctrl:1
	s_nop 1
	v_add_f32_dpp v218, v218, v218 row_ror:4 row_mask:0xf bank_mask:0xf bound_ctrl:1
	s_nop 1
	v_add_f32_dpp v218, v218, v218 row_ror:8 row_mask:0xf bank_mask:0xf bound_ctrl:1
	s_nop 1
	v_readlane_b32 s8, v218, 0
	v_readlane_b32 s9, v218, 16
	v_readlane_b32 s10, v218, 32
	v_readlane_b32 s11, v218, 48
	s_nop 1
	v_mov_b32_e32 v218, s8
	v_add_f32_e32 v218, s9, v218
	v_mov_b32_e32 v219, s10
	v_add_f32_e32 v219, s11, v219
	v_add_f32_e32 v218, v218, v219
	v_mul_f32_e32 v218, 0x3a000000, v218
	v_add_f32_e32 v218, 0x358637bd, v218
	v_rsq_f32_e32 v218, v218
	s_nop 0
	v_lshlrev_b32_e32 v246, 16, v166
	v_and_b32_e32 v247, 0xffff0000, v166
	v_lshlrev_b32_e32 v248, 16, v167
	v_and_b32_e32 v249, 0xffff0000, v167
	v_mul_f32_e32 v246, v246, v218
	v_mul_f32_e32 v247, v247, v218
	v_mul_f32_e32 v248, v248, v218
	v_mul_f32_e32 v249, v249, v218
	v_lshlrev_b32_e32 v0, 16, v182
	v_and_b32_e32 v1, 0xffff0000, v182
	v_lshlrev_b32_e32 v2, 16, v183
	v_and_b32_e32 v3, 0xffff0000, v183
	v_fmac_f32_e32 v0, v246, v32
	v_fmac_f32_e32 v1, v247, v33
	v_fmac_f32_e32 v2, v248, v34
	v_fmac_f32_e32 v3, v249, v35
	v_lshlrev_b32_e32 v246, 16, v168
	v_and_b32_e32 v247, 0xffff0000, v168
	v_lshlrev_b32_e32 v248, 16, v169
	v_and_b32_e32 v249, 0xffff0000, v169
	v_mul_f32_e32 v246, v246, v218
	v_mul_f32_e32 v247, v247, v218
	v_mul_f32_e32 v248, v248, v218
	v_mul_f32_e32 v249, v249, v218
	v_lshlrev_b32_e32 v4, 16, v184
	v_and_b32_e32 v5, 0xffff0000, v184
	v_lshlrev_b32_e32 v6, 16, v185
	v_and_b32_e32 v7, 0xffff0000, v185
	v_fmac_f32_e32 v4, v246, v36
	v_fmac_f32_e32 v5, v247, v37
	v_fmac_f32_e32 v6, v248, v38
	v_fmac_f32_e32 v7, v249, v39
	v_lshlrev_b32_e32 v246, 16, v170
	v_and_b32_e32 v247, 0xffff0000, v170
	v_lshlrev_b32_e32 v248, 16, v171
	v_and_b32_e32 v249, 0xffff0000, v171
	v_mul_f32_e32 v246, v246, v218
	v_mul_f32_e32 v247, v247, v218
	v_mul_f32_e32 v248, v248, v218
	v_mul_f32_e32 v249, v249, v218
	v_lshlrev_b32_e32 v8, 16, v186
	v_and_b32_e32 v9, 0xffff0000, v186
	v_lshlrev_b32_e32 v10, 16, v187
	v_and_b32_e32 v11, 0xffff0000, v187
	v_fmac_f32_e32 v8, v246, v40
	v_fmac_f32_e32 v9, v247, v41
	v_fmac_f32_e32 v10, v248, v42
	v_fmac_f32_e32 v11, v249, v43
	v_lshlrev_b32_e32 v246, 16, v172
	v_and_b32_e32 v247, 0xffff0000, v172
	v_lshlrev_b32_e32 v248, 16, v173
	v_and_b32_e32 v249, 0xffff0000, v173
	v_mul_f32_e32 v246, v246, v218
	v_mul_f32_e32 v247, v247, v218
	v_mul_f32_e32 v248, v248, v218
	v_mul_f32_e32 v249, v249, v218
	v_lshlrev_b32_e32 v12, 16, v188
	v_and_b32_e32 v13, 0xffff0000, v188
	v_lshlrev_b32_e32 v14, 16, v189
	v_and_b32_e32 v15, 0xffff0000, v189
	v_fmac_f32_e32 v12, v246, v44
	v_fmac_f32_e32 v13, v247, v45
	v_fmac_f32_e32 v14, v248, v46
	v_fmac_f32_e32 v15, v249, v47
	v_lshlrev_b32_e32 v246, 16, v174
	v_and_b32_e32 v247, 0xffff0000, v174
	v_lshlrev_b32_e32 v248, 16, v175
	v_and_b32_e32 v249, 0xffff0000, v175
	v_mul_f32_e32 v246, v246, v218
	v_mul_f32_e32 v247, v247, v218
	v_mul_f32_e32 v248, v248, v218
	v_mul_f32_e32 v249, v249, v218
	v_lshlrev_b32_e32 v16, 16, v190
	v_and_b32_e32 v17, 0xffff0000, v190
	v_lshlrev_b32_e32 v18, 16, v191
	v_and_b32_e32 v19, 0xffff0000, v191
	v_fmac_f32_e32 v16, v246, v48
	v_fmac_f32_e32 v17, v247, v49
	v_fmac_f32_e32 v18, v248, v50
	v_fmac_f32_e32 v19, v249, v51
	v_lshlrev_b32_e32 v246, 16, v176
	v_and_b32_e32 v247, 0xffff0000, v176
	v_lshlrev_b32_e32 v248, 16, v177
	v_and_b32_e32 v249, 0xffff0000, v177
	v_mul_f32_e32 v246, v246, v218
	v_mul_f32_e32 v247, v247, v218
	v_mul_f32_e32 v248, v248, v218
	v_mul_f32_e32 v249, v249, v218
	v_lshlrev_b32_e32 v20, 16, v192
	v_and_b32_e32 v21, 0xffff0000, v192
	v_lshlrev_b32_e32 v22, 16, v193
	v_and_b32_e32 v23, 0xffff0000, v193
	v_fmac_f32_e32 v20, v246, v52
	v_fmac_f32_e32 v21, v247, v53
	v_fmac_f32_e32 v22, v248, v54
	v_fmac_f32_e32 v23, v249, v55
	v_lshlrev_b32_e32 v246, 16, v178
	v_and_b32_e32 v247, 0xffff0000, v178
	v_lshlrev_b32_e32 v248, 16, v179
	v_and_b32_e32 v249, 0xffff0000, v179
	v_mul_f32_e32 v246, v246, v218
	v_mul_f32_e32 v247, v247, v218
	v_mul_f32_e32 v248, v248, v218
	v_mul_f32_e32 v249, v249, v218
	v_lshlrev_b32_e32 v24, 16, v194
	v_and_b32_e32 v25, 0xffff0000, v194
	v_lshlrev_b32_e32 v26, 16, v195
	v_and_b32_e32 v27, 0xffff0000, v195
	v_fmac_f32_e32 v24, v246, v56
	v_fmac_f32_e32 v25, v247, v57
	v_fmac_f32_e32 v26, v248, v58
	v_fmac_f32_e32 v27, v249, v59
	v_lshlrev_b32_e32 v246, 16, v180
	v_and_b32_e32 v247, 0xffff0000, v180
	v_lshlrev_b32_e32 v248, 16, v181
	v_and_b32_e32 v249, 0xffff0000, v181
	v_mul_f32_e32 v246, v246, v218
	v_mul_f32_e32 v247, v247, v218
	v_mul_f32_e32 v248, v248, v218
	v_mul_f32_e32 v249, v249, v218
	v_lshlrev_b32_e32 v28, 16, v196
	v_and_b32_e32 v29, 0xffff0000, v196
	v_lshlrev_b32_e32 v30, 16, v197
	v_and_b32_e32 v31, 0xffff0000, v197
	v_fmac_f32_e32 v28, v246, v60
	v_fmac_f32_e32 v29, v247, v61
	v_fmac_f32_e32 v30, v248, v62
	v_fmac_f32_e32 v31, v249, v63
	global_load_dwordx2 v[166:167], v162, s[56:57]
	global_load_dwordx2 v[168:169], v162, s[56:57] offset:512
	global_load_dwordx2 v[170:171], v162, s[56:57] offset:1024
	global_load_dwordx2 v[172:173], v162, s[56:57] offset:1536
	global_load_dwordx2 v[174:175], v162, s[56:57] offset:2048
	global_load_dwordx2 v[176:177], v162, s[56:57] offset:2560
	global_load_dwordx2 v[178:179], v162, s[56:57] offset:3072
	global_load_dwordx2 v[180:181], v162, s[56:57] offset:3584
	global_load_dwordx2 v[182:183], v162, s[58:59]
	global_load_dwordx2 v[184:185], v162, s[58:59] offset:512
	global_load_dwordx2 v[186:187], v162, s[58:59] offset:1024
	global_load_dwordx2 v[188:189], v162, s[58:59] offset:1536
	global_load_dwordx2 v[190:191], v162, s[58:59] offset:2048
	global_load_dwordx2 v[192:193], v162, s[58:59] offset:2560
	global_load_dwordx2 v[194:195], v162, s[58:59] offset:3072
	global_load_dwordx2 v[196:197], v162, s[58:59] offset:3584
	s_add_u32 s58, s58, 0x8000
	s_addc_u32 s59, s59, 0
	s_add_u32 s56, s56, 0x8000
	s_addc_u32 s57, s57, 0
	v_mov_b32_e32 v250, 0
	v_mov_b32_e32 v251, 0
	v_cvt_pk_bf16_f32 v238, v0, v1
	v_cvt_pk_bf16_f32 v239, v2, v3
	v_fmac_f32_e32 v250, v0, v0
	v_fmac_f32_e32 v251, v1, v1
	v_fmac_f32_e32 v250, v2, v2
	v_fmac_f32_e32 v251, v3, v3
	global_store_dwordx2 v162, v[238:239], s[70:71]
	v_cvt_pk_bf16_f32 v240, v4, v5
	v_cvt_pk_bf16_f32 v241, v6, v7
	v_fmac_f32_e32 v250, v4, v4
	v_fmac_f32_e32 v251, v5, v5
	v_fmac_f32_e32 v250, v6, v6
	v_fmac_f32_e32 v251, v7, v7
	global_store_dwordx2 v162, v[240:241], s[70:71] offset:512
	v_cvt_pk_bf16_f32 v242, v8, v9
	v_cvt_pk_bf16_f32 v243, v10, v11
	v_fmac_f32_e32 v250, v8, v8
	v_fmac_f32_e32 v251, v9, v9
	v_fmac_f32_e32 v250, v10, v10
	v_fmac_f32_e32 v251, v11, v11
	global_store_dwordx2 v162, v[242:243], s[70:71] offset:1024
	v_cvt_pk_bf16_f32 v244, v12, v13
	v_cvt_pk_bf16_f32 v245, v14, v15
	v_fmac_f32_e32 v250, v12, v12
	v_fmac_f32_e32 v251, v13, v13
	v_fmac_f32_e32 v250, v14, v14
	v_fmac_f32_e32 v251, v15, v15
	global_store_dwordx2 v162, v[244:245], s[70:71] offset:1536
	v_cvt_pk_bf16_f32 v238, v16, v17
	v_cvt_pk_bf16_f32 v239, v18, v19
	v_fmac_f32_e32 v250, v16, v16
	v_fmac_f32_e32 v251, v17, v17
	v_fmac_f32_e32 v250, v18, v18
	v_fmac_f32_e32 v251, v19, v19
	global_store_dwordx2 v162, v[238:239], s[70:71] offset:2048
	v_cvt_pk_bf16_f32 v240, v20, v21
	v_cvt_pk_bf16_f32 v241, v22, v23
	v_fmac_f32_e32 v250, v20, v20
	v_fmac_f32_e32 v251, v21, v21
	v_fmac_f32_e32 v250, v22, v22
	v_fmac_f32_e32 v251, v23, v23
	global_store_dwordx2 v162, v[240:241], s[70:71] offset:2560
	v_cvt_pk_bf16_f32 v242, v24, v25
	v_cvt_pk_bf16_f32 v243, v26, v27
	v_fmac_f32_e32 v250, v24, v24
	v_fmac_f32_e32 v251, v25, v25
	v_fmac_f32_e32 v250, v26, v26
	v_fmac_f32_e32 v251, v27, v27
	global_store_dwordx2 v162, v[242:243], s[70:71] offset:3072
	v_cvt_pk_bf16_f32 v244, v28, v29
	v_cvt_pk_bf16_f32 v245, v30, v31
	v_fmac_f32_e32 v250, v28, v28
	v_fmac_f32_e32 v251, v29, v29
	v_fmac_f32_e32 v250, v30, v30
	v_fmac_f32_e32 v251, v31, v31
	global_store_dwordx2 v162, v[244:245], s[70:71] offset:3584
	s_add_u32 s70, s70, 0x8000
	s_addc_u32 s71, s71, 0
	v_add_f32_e32 v250, v250, v251
	s_nop 1
	v_add_f32_dpp v218, v250, v250 quad_perm:[1,0,3,2] row_mask:0xf bank_mask:0xf bound_ctrl:1
	s_nop 1
	v_add_f32_dpp v218, v218, v218 quad_perm:[2,3,0,1] row_mask:0xf bank_mask:0xf bound_ctrl:1
	s_nop 1
	v_add_f32_dpp v218, v218, v218 row_ror:4 row_mask:0xf bank_mask:0xf bound_ctrl:1
	s_nop 1
	v_add_f32_dpp v218, v218, v218 row_ror:8 row_mask:0xf bank_mask:0xf bound_ctrl:1
	s_nop 1
	v_readlane_b32 s8, v218, 0
	v_readlane_b32 s9, v218, 16
	v_readlane_b32 s10, v218, 32
	v_readlane_b32 s11, v218, 48
	s_nop 1
	v_mov_b32_e32 v218, s8
	v_add_f32_e32 v218, s9, v218
	v_mov_b32_e32 v219, s10
	v_add_f32_e32 v219, s11, v219
	v_add_f32_e32 v218, v218, v219
	v_mul_f32_e32 v218, 0x3a000000, v218
	v_add_f32_e32 v218, 0x358637bd, v218
	v_rsq_f32_e32 v218, v218
	s_nop 0
	v_mul_f32_e32 v246, v0, v218
	v_mul_f32_e32 v247, v1, v218
	v_mul_f32_e32 v248, v2, v218
	v_mul_f32_e32 v249, v3, v218
	v_fma_f32 v246, v246, v64, v96
	v_fma_f32 v247, v247, v65, v97
	v_fma_f32 v248, v248, v66, v98
	v_fma_f32 v249, v249, v67, v99
	v_cvt_pk_bf16_f32 v238, v246, v247
	v_cvt_pk_bf16_f32 v239, v248, v249
	global_store_dwordx2 v162, v[238:239], s[72:73]
	v_mul_f32_e32 v246, v4, v218
	v_mul_f32_e32 v247, v5, v218
	v_mul_f32_e32 v248, v6, v218
	v_mul_f32_e32 v249, v7, v218
	v_fma_f32 v246, v246, v68, v100
	v_fma_f32 v247, v247, v69, v101
	v_fma_f32 v248, v248, v70, v102
	v_fma_f32 v249, v249, v71, v103
	v_cvt_pk_bf16_f32 v240, v246, v247
	v_cvt_pk_bf16_f32 v241, v248, v249
	global_store_dwordx2 v162, v[240:241], s[72:73] offset:512
	v_mul_f32_e32 v246, v8, v218
	v_mul_f32_e32 v247, v9, v218
	v_mul_f32_e32 v248, v10, v218
	v_mul_f32_e32 v249, v11, v218
	v_fma_f32 v246, v246, v72, v104
	v_fma_f32 v247, v247, v73, v105
	v_fma_f32 v248, v248, v74, v106
	v_fma_f32 v249, v249, v75, v107
	v_cvt_pk_bf16_f32 v242, v246, v247
	v_cvt_pk_bf16_f32 v243, v248, v249
	global_store_dwordx2 v162, v[242:243], s[72:73] offset:1024
	v_mul_f32_e32 v246, v12, v218
	v_mul_f32_e32 v247, v13, v218
	v_mul_f32_e32 v248, v14, v218
	v_mul_f32_e32 v249, v15, v218
	v_fma_f32 v246, v246, v76, v108
	v_fma_f32 v247, v247, v77, v109
	v_fma_f32 v248, v248, v78, v110
	v_fma_f32 v249, v249, v79, v111
	v_cvt_pk_bf16_f32 v244, v246, v247
	v_cvt_pk_bf16_f32 v245, v248, v249
	global_store_dwordx2 v162, v[244:245], s[72:73] offset:1536
	v_mul_f32_e32 v246, v16, v218
	v_mul_f32_e32 v247, v17, v218
	v_mul_f32_e32 v248, v18, v218
	v_mul_f32_e32 v249, v19, v218
	v_fma_f32 v246, v246, v80, v112
	v_fma_f32 v247, v247, v81, v113
	v_fma_f32 v248, v248, v82, v114
	v_fma_f32 v249, v249, v83, v115
	v_cvt_pk_bf16_f32 v238, v246, v247
	v_cvt_pk_bf16_f32 v239, v248, v249
	global_store_dwordx2 v162, v[238:239], s[72:73] offset:2048
	v_mul_f32_e32 v246, v20, v218
	v_mul_f32_e32 v247, v21, v218
	v_mul_f32_e32 v248, v22, v218
	v_mul_f32_e32 v249, v23, v218
	v_fma_f32 v246, v246, v84, v116
	v_fma_f32 v247, v247, v85, v117
	v_fma_f32 v248, v248, v86, v118
	v_fma_f32 v249, v249, v87, v119
	v_cvt_pk_bf16_f32 v240, v246, v247
	v_cvt_pk_bf16_f32 v241, v248, v249
	global_store_dwordx2 v162, v[240:241], s[72:73] offset:2560
	v_mul_f32_e32 v246, v24, v218
	v_mul_f32_e32 v247, v25, v218
	v_mul_f32_e32 v248, v26, v218
	v_mul_f32_e32 v249, v27, v218
	v_fma_f32 v246, v246, v88, v120
	v_fma_f32 v247, v247, v89, v121
	v_fma_f32 v248, v248, v90, v122
	v_fma_f32 v249, v249, v91, v123
	v_cvt_pk_bf16_f32 v242, v246, v247
	v_cvt_pk_bf16_f32 v243, v248, v249
	global_store_dwordx2 v162, v[242:243], s[72:73] offset:3072
	v_mul_f32_e32 v246, v28, v218
	v_mul_f32_e32 v247, v29, v218
	v_mul_f32_e32 v248, v30, v218
	v_mul_f32_e32 v249, v31, v218
	v_fma_f32 v246, v246, v92, v124
	v_fma_f32 v247, v247, v93, v125
	v_fma_f32 v248, v248, v94, v126
	v_fma_f32 v249, v249, v95, v127
	v_cvt_pk_bf16_f32 v244, v246, v247
	v_cvt_pk_bf16_f32 v245, v248, v249
	global_store_dwordx2 v162, v[244:245], s[72:73] offset:3584
	s_add_u32 s72, s72, 0x8000
	s_addc_u32 s73, s73, 0
	s_add_u32 s76, s76, 1
	s_cmp_lt_u32 s76, 7
	s_cbranch_scc1 .Lmp_V1_loop
	s_waitcnt vmcnt(32)
	v_mov_b32_e32 v250, 0
	v_mov_b32_e32 v251, 0
	v_lshlrev_b32_e32 v246, 16, v128
	v_and_b32_e32 v247, 0xffff0000, v128
	v_lshlrev_b32_e32 v248, 16, v129
	v_and_b32_e32 v249, 0xffff0000, v129
	v_fmac_f32_e32 v250, v246, v246
	v_fmac_f32_e32 v251, v247, v247
	v_fmac_f32_e32 v250, v248, v248
	v_fmac_f32_e32 v251, v249, v249
	v_lshlrev_b32_e32 v246, 16, v130
	v_and_b32_e32 v247, 0xffff0000, v130
	v_lshlrev_b32_e32 v248, 16, v131
	v_and_b32_e32 v249, 0xffff0000, v131
	v_fmac_f32_e32 v250, v246, v246
	v_fmac_f32_e32 v251, v247, v247
	v_fmac_f32_e32 v250, v248, v248
	v_fmac_f32_e32 v251, v249, v249
	v_lshlrev_b32_e32 v246, 16, v132
	v_and_b32_e32 v247, 0xffff0000, v132
	v_lshlrev_b32_e32 v248, 16, v133
	v_and_b32_e32 v249, 0xffff0000, v133
	v_fmac_f32_e32 v250, v246, v246
	v_fmac_f32_e32 v251, v247, v247
	v_fmac_f32_e32 v250, v248, v248
	v_fmac_f32_e32 v251, v249, v249
	v_lshlrev_b32_e32 v246, 16, v134
	v_and_b32_e32 v247, 0xffff0000, v134
	v_lshlrev_b32_e32 v248, 16, v135
	v_and_b32_e32 v249, 0xffff0000, v135
	v_fmac_f32_e32 v250, v246, v246
	v_fmac_f32_e32 v251, v247, v247
	v_fmac_f32_e32 v250, v248, v248
	v_fmac_f32_e32 v251, v249, v249
	v_lshlrev_b32_e32 v246, 16, v136
	v_and_b32_e32 v247, 0xffff0000, v136
	v_lshlrev_b32_e32 v248, 16, v137
	v_and_b32_e32 v249, 0xffff0000, v137
	v_fmac_f32_e32 v250, v246, v246
	v_fmac_f32_e32 v251, v247, v247
	v_fmac_f32_e32 v250, v248, v248
	v_fmac_f32_e32 v251, v249, v249
	v_lshlrev_b32_e32 v246, 16, v138
	v_and_b32_e32 v247, 0xffff0000, v138
	v_lshlrev_b32_e32 v248, 16, v139
	v_and_b32_e32 v249, 0xffff0000, v139
	v_fmac_f32_e32 v250, v246, v246
	v_fmac_f32_e32 v251, v247, v247
	v_fmac_f32_e32 v250, v248, v248
	v_fmac_f32_e32 v251, v249, v249
	v_lshlrev_b32_e32 v246, 16, v140
	v_and_b32_e32 v247, 0xffff0000, v140
	v_lshlrev_b32_e32 v248, 16, v141
	v_and_b32_e32 v249, 0xffff0000, v141
	v_fmac_f32_e32 v250, v246, v246
	v_fmac_f32_e32 v251, v247, v247
	v_fmac_f32_e32 v250, v248, v248
	v_fmac_f32_e32 v251, v249, v249
	v_lshlrev_b32_e32 v246, 16, v142
	v_and_b32_e32 v247, 0xffff0000, v142
	v_lshlrev_b32_e32 v248, 16, v143
	v_and_b32_e32 v249, 0xffff0000, v143
	v_fmac_f32_e32 v250, v246, v246
	v_fmac_f32_e32 v251, v247, v247
	v_fmac_f32_e32 v250, v248, v248
	v_fmac_f32_e32 v251, v249, v249
	v_add_f32_e32 v250, v250, v251
	s_nop 1
	v_add_f32_dpp v218, v250, v250 quad_perm:[1,0,3,2] row_mask:0xf bank_mask:0xf bound_ctrl:1
	s_nop 1
	v_add_f32_dpp v218, v218, v218 quad_perm:[2,3,0,1] row_mask:0xf bank_mask:0xf bound_ctrl:1
	s_nop 1
	v_add_f32_dpp v218, v218, v218 row_ror:4 row_mask:0xf bank_mask:0xf bound_ctrl:1
	s_nop 1
	v_add_f32_dpp v218, v218, v218 row_ror:8 row_mask:0xf bank_mask:0xf bound_ctrl:1
	s_nop 1
	v_readlane_b32 s8, v218, 0
	v_readlane_b32 s9, v218, 16
	v_readlane_b32 s10, v218, 32
	v_readlane_b32 s11, v218, 48
	s_nop 1
	v_mov_b32_e32 v218, s8
	v_add_f32_e32 v218, s9, v218
	v_mov_b32_e32 v219, s10
	v_add_f32_e32 v219, s11, v219
	v_add_f32_e32 v218, v218, v219
	v_mul_f32_e32 v218, 0x3a000000, v218
	v_add_f32_e32 v218, 0x358637bd, v218
	v_rsq_f32_e32 v218, v218
	s_nop 0
	v_lshlrev_b32_e32 v246, 16, v128
	v_and_b32_e32 v247, 0xffff0000, v128
	v_lshlrev_b32_e32 v248, 16, v129
	v_and_b32_e32 v249, 0xffff0000, v129
	v_mul_f32_e32 v246, v246, v218
	v_mul_f32_e32 v247, v247, v218
	v_mul_f32_e32 v248, v248, v218
	v_mul_f32_e32 v249, v249, v218
	v_lshlrev_b32_e32 v0, 16, v144
	v_and_b32_e32 v1, 0xffff0000, v144
	v_lshlrev_b32_e32 v2, 16, v145
	v_and_b32_e32 v3, 0xffff0000, v145
	v_fmac_f32_e32 v0, v246, v32
	v_fmac_f32_e32 v1, v247, v33
	v_fmac_f32_e32 v2, v248, v34
	v_fmac_f32_e32 v3, v249, v35
	v_lshlrev_b32_e32 v246, 16, v130
	v_and_b32_e32 v247, 0xffff0000, v130
	v_lshlrev_b32_e32 v248, 16, v131
	v_and_b32_e32 v249, 0xffff0000, v131
	v_mul_f32_e32 v246, v246, v218
	v_mul_f32_e32 v247, v247, v218
	v_mul_f32_e32 v248, v248, v218
	v_mul_f32_e32 v249, v249, v218
	v_lshlrev_b32_e32 v4, 16, v146
	v_and_b32_e32 v5, 0xffff0000, v146
	v_lshlrev_b32_e32 v6, 16, v147
	v_and_b32_e32 v7, 0xffff0000, v147
	v_fmac_f32_e32 v4, v246, v36
	v_fmac_f32_e32 v5, v247, v37
	v_fmac_f32_e32 v6, v248, v38
	v_fmac_f32_e32 v7, v249, v39
	v_lshlrev_b32_e32 v246, 16, v132
	v_and_b32_e32 v247, 0xffff0000, v132
	v_lshlrev_b32_e32 v248, 16, v133
	v_and_b32_e32 v249, 0xffff0000, v133
	v_mul_f32_e32 v246, v246, v218
	v_mul_f32_e32 v247, v247, v218
	v_mul_f32_e32 v248, v248, v218
	v_mul_f32_e32 v249, v249, v218
	v_lshlrev_b32_e32 v8, 16, v148
	v_and_b32_e32 v9, 0xffff0000, v148
	v_lshlrev_b32_e32 v10, 16, v149
	v_and_b32_e32 v11, 0xffff0000, v149
	v_fmac_f32_e32 v8, v246, v40
	v_fmac_f32_e32 v9, v247, v41
	v_fmac_f32_e32 v10, v248, v42
	v_fmac_f32_e32 v11, v249, v43
	v_lshlrev_b32_e32 v246, 16, v134
	v_and_b32_e32 v247, 0xffff0000, v134
	v_lshlrev_b32_e32 v248, 16, v135
	v_and_b32_e32 v249, 0xffff0000, v135
	v_mul_f32_e32 v246, v246, v218
	v_mul_f32_e32 v247, v247, v218
	v_mul_f32_e32 v248, v248, v218
	v_mul_f32_e32 v249, v249, v218
	v_lshlrev_b32_e32 v12, 16, v150
	v_and_b32_e32 v13, 0xffff0000, v150
	v_lshlrev_b32_e32 v14, 16, v151
	v_and_b32_e32 v15, 0xffff0000, v151
	v_fmac_f32_e32 v12, v246, v44
	v_fmac_f32_e32 v13, v247, v45
	v_fmac_f32_e32 v14, v248, v46
	v_fmac_f32_e32 v15, v249, v47
	v_lshlrev_b32_e32 v246, 16, v136
	v_and_b32_e32 v247, 0xffff0000, v136
	v_lshlrev_b32_e32 v248, 16, v137
	v_and_b32_e32 v249, 0xffff0000, v137
	v_mul_f32_e32 v246, v246, v218
	v_mul_f32_e32 v247, v247, v218
	v_mul_f32_e32 v248, v248, v218
	v_mul_f32_e32 v249, v249, v218
	v_lshlrev_b32_e32 v16, 16, v152
	v_and_b32_e32 v17, 0xffff0000, v152
	v_lshlrev_b32_e32 v18, 16, v153
	v_and_b32_e32 v19, 0xffff0000, v153
	v_fmac_f32_e32 v16, v246, v48
	v_fmac_f32_e32 v17, v247, v49
	v_fmac_f32_e32 v18, v248, v50
	v_fmac_f32_e32 v19, v249, v51
	v_lshlrev_b32_e32 v246, 16, v138
	v_and_b32_e32 v247, 0xffff0000, v138
	v_lshlrev_b32_e32 v248, 16, v139
	v_and_b32_e32 v249, 0xffff0000, v139
	v_mul_f32_e32 v246, v246, v218
	v_mul_f32_e32 v247, v247, v218
	v_mul_f32_e32 v248, v248, v218
	v_mul_f32_e32 v249, v249, v218
	v_lshlrev_b32_e32 v20, 16, v154
	v_and_b32_e32 v21, 0xffff0000, v154
	v_lshlrev_b32_e32 v22, 16, v155
	v_and_b32_e32 v23, 0xffff0000, v155
	v_fmac_f32_e32 v20, v246, v52
	v_fmac_f32_e32 v21, v247, v53
	v_fmac_f32_e32 v22, v248, v54
	v_fmac_f32_e32 v23, v249, v55
	v_lshlrev_b32_e32 v246, 16, v140
	v_and_b32_e32 v247, 0xffff0000, v140
	v_lshlrev_b32_e32 v248, 16, v141
	v_and_b32_e32 v249, 0xffff0000, v141
	v_mul_f32_e32 v246, v246, v218
	v_mul_f32_e32 v247, v247, v218
	v_mul_f32_e32 v248, v248, v218
	v_mul_f32_e32 v249, v249, v218
	v_lshlrev_b32_e32 v24, 16, v156
	v_and_b32_e32 v25, 0xffff0000, v156
	v_lshlrev_b32_e32 v26, 16, v157
	v_and_b32_e32 v27, 0xffff0000, v157
	v_fmac_f32_e32 v24, v246, v56
	v_fmac_f32_e32 v25, v247, v57
	v_fmac_f32_e32 v26, v248, v58
	v_fmac_f32_e32 v27, v249, v59
	v_lshlrev_b32_e32 v246, 16, v142
	v_and_b32_e32 v247, 0xffff0000, v142
	v_lshlrev_b32_e32 v248, 16, v143
	v_and_b32_e32 v249, 0xffff0000, v143
	v_mul_f32_e32 v246, v246, v218
	v_mul_f32_e32 v247, v247, v218
	v_mul_f32_e32 v248, v248, v218
	v_mul_f32_e32 v249, v249, v218
	v_lshlrev_b32_e32 v28, 16, v158
	v_and_b32_e32 v29, 0xffff0000, v158
	v_lshlrev_b32_e32 v30, 16, v159
	v_and_b32_e32 v31, 0xffff0000, v159
	v_fmac_f32_e32 v28, v246, v60
	v_fmac_f32_e32 v29, v247, v61
	v_fmac_f32_e32 v30, v248, v62
	v_fmac_f32_e32 v31, v249, v63
	v_mov_b32_e32 v250, 0
	v_mov_b32_e32 v251, 0
	v_cvt_pk_bf16_f32 v238, v0, v1
	v_cvt_pk_bf16_f32 v239, v2, v3
	v_fmac_f32_e32 v250, v0, v0
	v_fmac_f32_e32 v251, v1, v1
	v_fmac_f32_e32 v250, v2, v2
	v_fmac_f32_e32 v251, v3, v3
	global_store_dwordx2 v162, v[238:239], s[70:71]
	v_cvt_pk_bf16_f32 v240, v4, v5
	v_cvt_pk_bf16_f32 v241, v6, v7
	v_fmac_f32_e32 v250, v4, v4
	v_fmac_f32_e32 v251, v5, v5
	v_fmac_f32_e32 v250, v6, v6
	v_fmac_f32_e32 v251, v7, v7
	global_store_dwordx2 v162, v[240:241], s[70:71] offset:512
	v_cvt_pk_bf16_f32 v242, v8, v9
	v_cvt_pk_bf16_f32 v243, v10, v11
	v_fmac_f32_e32 v250, v8, v8
	v_fmac_f32_e32 v251, v9, v9
	v_fmac_f32_e32 v250, v10, v10
	v_fmac_f32_e32 v251, v11, v11
	global_store_dwordx2 v162, v[242:243], s[70:71] offset:1024
	v_cvt_pk_bf16_f32 v244, v12, v13
	v_cvt_pk_bf16_f32 v245, v14, v15
	v_fmac_f32_e32 v250, v12, v12
	v_fmac_f32_e32 v251, v13, v13
	v_fmac_f32_e32 v250, v14, v14
	v_fmac_f32_e32 v251, v15, v15
	global_store_dwordx2 v162, v[244:245], s[70:71] offset:1536
	v_cvt_pk_bf16_f32 v238, v16, v17
	v_cvt_pk_bf16_f32 v239, v18, v19
	v_fmac_f32_e32 v250, v16, v16
	v_fmac_f32_e32 v251, v17, v17
	v_fmac_f32_e32 v250, v18, v18
	v_fmac_f32_e32 v251, v19, v19
	global_store_dwordx2 v162, v[238:239], s[70:71] offset:2048
	v_cvt_pk_bf16_f32 v240, v20, v21
	v_cvt_pk_bf16_f32 v241, v22, v23
	v_fmac_f32_e32 v250, v20, v20
	v_fmac_f32_e32 v251, v21, v21
	v_fmac_f32_e32 v250, v22, v22
	v_fmac_f32_e32 v251, v23, v23
	global_store_dwordx2 v162, v[240:241], s[70:71] offset:2560
	v_cvt_pk_bf16_f32 v242, v24, v25
	v_cvt_pk_bf16_f32 v243, v26, v27
	v_fmac_f32_e32 v250, v24, v24
	v_fmac_f32_e32 v251, v25, v25
	v_fmac_f32_e32 v250, v26, v26
	v_fmac_f32_e32 v251, v27, v27
	global_store_dwordx2 v162, v[242:243], s[70:71] offset:3072
	v_cvt_pk_bf16_f32 v244, v28, v29
	v_cvt_pk_bf16_f32 v245, v30, v31
	v_fmac_f32_e32 v250, v28, v28
	v_fmac_f32_e32 v251, v29, v29
	v_fmac_f32_e32 v250, v30, v30
	v_fmac_f32_e32 v251, v31, v31
	global_store_dwordx2 v162, v[244:245], s[70:71] offset:3584
	s_add_u32 s70, s70, 0x8000
	s_addc_u32 s71, s71, 0
	v_add_f32_e32 v250, v250, v251
	s_nop 1
	v_add_f32_dpp v218, v250, v250 quad_perm:[1,0,3,2] row_mask:0xf bank_mask:0xf bound_ctrl:1
	s_nop 1
	v_add_f32_dpp v218, v218, v218 quad_perm:[2,3,0,1] row_mask:0xf bank_mask:0xf bound_ctrl:1
	s_nop 1
	v_add_f32_dpp v218, v218, v218 row_ror:4 row_mask:0xf bank_mask:0xf bound_ctrl:1
	s_nop 1
	v_add_f32_dpp v218, v218, v218 row_ror:8 row_mask:0xf bank_mask:0xf bound_ctrl:1
	s_nop 1
	v_readlane_b32 s8, v218, 0
	v_readlane_b32 s9, v218, 16
	v_readlane_b32 s10, v218, 32
	v_readlane_b32 s11, v218, 48
	s_nop 1
	v_mov_b32_e32 v218, s8
	v_add_f32_e32 v218, s9, v218
	v_mov_b32_e32 v219, s10
	v_add_f32_e32 v219, s11, v219
	v_add_f32_e32 v218, v218, v219
	v_mul_f32_e32 v218, 0x3a000000, v218
	v_add_f32_e32 v218, 0x358637bd, v218
	v_rsq_f32_e32 v218, v218
	s_nop 0
	v_mul_f32_e32 v246, v0, v218
	v_mul_f32_e32 v247, v1, v218
	v_mul_f32_e32 v248, v2, v218
	v_mul_f32_e32 v249, v3, v218
	v_fma_f32 v246, v246, v64, v96
	v_fma_f32 v247, v247, v65, v97
	v_fma_f32 v248, v248, v66, v98
	v_fma_f32 v249, v249, v67, v99
	v_cvt_pk_bf16_f32 v238, v246, v247
	v_cvt_pk_bf16_f32 v239, v248, v249
	global_store_dwordx2 v162, v[238:239], s[72:73]
	v_mul_f32_e32 v246, v4, v218
	v_mul_f32_e32 v247, v5, v218
	v_mul_f32_e32 v248, v6, v218
	v_mul_f32_e32 v249, v7, v218
	v_fma_f32 v246, v246, v68, v100
	v_fma_f32 v247, v247, v69, v101
	v_fma_f32 v248, v248, v70, v102
	v_fma_f32 v249, v249, v71, v103
	v_cvt_pk_bf16_f32 v240, v246, v247
	v_cvt_pk_bf16_f32 v241, v248, v249
	global_store_dwordx2 v162, v[240:241], s[72:73] offset:512
	v_mul_f32_e32 v246, v8, v218
	v_mul_f32_e32 v247, v9, v218
	v_mul_f32_e32 v248, v10, v218
	v_mul_f32_e32 v249, v11, v218
	v_fma_f32 v246, v246, v72, v104
	v_fma_f32 v247, v247, v73, v105
	v_fma_f32 v248, v248, v74, v106
	v_fma_f32 v249, v249, v75, v107
	v_cvt_pk_bf16_f32 v242, v246, v247
	v_cvt_pk_bf16_f32 v243, v248, v249
	global_store_dwordx2 v162, v[242:243], s[72:73] offset:1024
	v_mul_f32_e32 v246, v12, v218
	v_mul_f32_e32 v247, v13, v218
	v_mul_f32_e32 v248, v14, v218
	v_mul_f32_e32 v249, v15, v218
	v_fma_f32 v246, v246, v76, v108
	v_fma_f32 v247, v247, v77, v109
	v_fma_f32 v248, v248, v78, v110
	v_fma_f32 v249, v249, v79, v111
	v_cvt_pk_bf16_f32 v244, v246, v247
	v_cvt_pk_bf16_f32 v245, v248, v249
	global_store_dwordx2 v162, v[244:245], s[72:73] offset:1536
	v_mul_f32_e32 v246, v16, v218
	v_mul_f32_e32 v247, v17, v218
	v_mul_f32_e32 v248, v18, v218
	v_mul_f32_e32 v249, v19, v218
	v_fma_f32 v246, v246, v80, v112
	v_fma_f32 v247, v247, v81, v113
	v_fma_f32 v248, v248, v82, v114
	v_fma_f32 v249, v249, v83, v115
	v_cvt_pk_bf16_f32 v238, v246, v247
	v_cvt_pk_bf16_f32 v239, v248, v249
	global_store_dwordx2 v162, v[238:239], s[72:73] offset:2048
	v_mul_f32_e32 v246, v20, v218
	v_mul_f32_e32 v247, v21, v218
	v_mul_f32_e32 v248, v22, v218
	v_mul_f32_e32 v249, v23, v218
	v_fma_f32 v246, v246, v84, v116
	v_fma_f32 v247, v247, v85, v117
	v_fma_f32 v248, v248, v86, v118
	v_fma_f32 v249, v249, v87, v119
	v_cvt_pk_bf16_f32 v240, v246, v247
	v_cvt_pk_bf16_f32 v241, v248, v249
	global_store_dwordx2 v162, v[240:241], s[72:73] offset:2560
	v_mul_f32_e32 v246, v24, v218
	v_mul_f32_e32 v247, v25, v218
	v_mul_f32_e32 v248, v26, v218
	v_mul_f32_e32 v249, v27, v218
	v_fma_f32 v246, v246, v88, v120
	v_fma_f32 v247, v247, v89, v121
	v_fma_f32 v248, v248, v90, v122
	v_fma_f32 v249, v249, v91, v123
	v_cvt_pk_bf16_f32 v242, v246, v247
	v_cvt_pk_bf16_f32 v243, v248, v249
	global_store_dwordx2 v162, v[242:243], s[72:73] offset:3072
	v_mul_f32_e32 v246, v28, v218
	v_mul_f32_e32 v247, v29, v218
	v_mul_f32_e32 v248, v30, v218
	v_mul_f32_e32 v249, v31, v218
	v_fma_f32 v246, v246, v92, v124
	v_fma_f32 v247, v247, v93, v125
	v_fma_f32 v248, v248, v94, v126
	v_fma_f32 v249, v249, v95, v127
	v_cvt_pk_bf16_f32 v244, v246, v247
	v_cvt_pk_bf16_f32 v245, v248, v249
	global_store_dwordx2 v162, v[244:245], s[72:73] offset:3584
	s_add_u32 s72, s72, 0x8000
	s_addc_u32 s73, s73, 0
	s_waitcnt vmcnt(32)
	v_mov_b32_e32 v250, 0
	v_mov_b32_e32 v251, 0
	v_lshlrev_b32_e32 v246, 16, v166
	v_and_b32_e32 v247, 0xffff0000, v166
	v_lshlrev_b32_e32 v248, 16, v167
	v_and_b32_e32 v249, 0xffff0000, v167
	v_fmac_f32_e32 v250, v246, v246
	v_fmac_f32_e32 v251, v247, v247
	v_fmac_f32_e32 v250, v248, v248
	v_fmac_f32_e32 v251, v249, v249
	v_lshlrev_b32_e32 v246, 16, v168
	v_and_b32_e32 v247, 0xffff0000, v168
	v_lshlrev_b32_e32 v248, 16, v169
	v_and_b32_e32 v249, 0xffff0000, v169
	v_fmac_f32_e32 v250, v246, v246
	v_fmac_f32_e32 v251, v247, v247
	v_fmac_f32_e32 v250, v248, v248
	v_fmac_f32_e32 v251, v249, v249
	v_lshlrev_b32_e32 v246, 16, v170
	v_and_b32_e32 v247, 0xffff0000, v170
	v_lshlrev_b32_e32 v248, 16, v171
	v_and_b32_e32 v249, 0xffff0000, v171
	v_fmac_f32_e32 v250, v246, v246
	v_fmac_f32_e32 v251, v247, v247
	v_fmac_f32_e32 v250, v248, v248
	v_fmac_f32_e32 v251, v249, v249
	v_lshlrev_b32_e32 v246, 16, v172
	v_and_b32_e32 v247, 0xffff0000, v172
	v_lshlrev_b32_e32 v248, 16, v173
	v_and_b32_e32 v249, 0xffff0000, v173
	v_fmac_f32_e32 v250, v246, v246
	v_fmac_f32_e32 v251, v247, v247
	v_fmac_f32_e32 v250, v248, v248
	v_fmac_f32_e32 v251, v249, v249
	v_lshlrev_b32_e32 v246, 16, v174
	v_and_b32_e32 v247, 0xffff0000, v174
	v_lshlrev_b32_e32 v248, 16, v175
	v_and_b32_e32 v249, 0xffff0000, v175
	v_fmac_f32_e32 v250, v246, v246
	v_fmac_f32_e32 v251, v247, v247
	v_fmac_f32_e32 v250, v248, v248
	v_fmac_f32_e32 v251, v249, v249
	v_lshlrev_b32_e32 v246, 16, v176
	v_and_b32_e32 v247, 0xffff0000, v176
	v_lshlrev_b32_e32 v248, 16, v177
	v_and_b32_e32 v249, 0xffff0000, v177
	v_fmac_f32_e32 v250, v246, v246
	v_fmac_f32_e32 v251, v247, v247
	v_fmac_f32_e32 v250, v248, v248
	v_fmac_f32_e32 v251, v249, v249
	v_lshlrev_b32_e32 v246, 16, v178
	v_and_b32_e32 v247, 0xffff0000, v178
	v_lshlrev_b32_e32 v248, 16, v179
	v_and_b32_e32 v249, 0xffff0000, v179
	v_fmac_f32_e32 v250, v246, v246
	v_fmac_f32_e32 v251, v247, v247
	v_fmac_f32_e32 v250, v248, v248
	v_fmac_f32_e32 v251, v249, v249
	v_lshlrev_b32_e32 v246, 16, v180
	v_and_b32_e32 v247, 0xffff0000, v180
	v_lshlrev_b32_e32 v248, 16, v181
	v_and_b32_e32 v249, 0xffff0000, v181
	v_fmac_f32_e32 v250, v246, v246
	v_fmac_f32_e32 v251, v247, v247
	v_fmac_f32_e32 v250, v248, v248
	v_fmac_f32_e32 v251, v249, v249
	v_add_f32_e32 v250, v250, v251
	s_nop 1
	v_add_f32_dpp v218, v250, v250 quad_perm:[1,0,3,2] row_mask:0xf bank_mask:0xf bound_ctrl:1
	s_nop 1
	v_add_f32_dpp v218, v218, v218 quad_perm:[2,3,0,1] row_mask:0xf bank_mask:0xf bound_ctrl:1
	s_nop 1
	v_add_f32_dpp v218, v218, v218 row_ror:4 row_mask:0xf bank_mask:0xf bound_ctrl:1
	s_nop 1
	v_add_f32_dpp v218, v218, v218 row_ror:8 row_mask:0xf bank_mask:0xf bound_ctrl:1
	s_nop 1
	v_readlane_b32 s8, v218, 0
	v_readlane_b32 s9, v218, 16
	v_readlane_b32 s10, v218, 32
	v_readlane_b32 s11, v218, 48
	s_nop 1
	v_mov_b32_e32 v218, s8
	v_add_f32_e32 v218, s9, v218
	v_mov_b32_e32 v219, s10
	v_add_f32_e32 v219, s11, v219
	v_add_f32_e32 v218, v218, v219
	v_mul_f32_e32 v218, 0x3a000000, v218
	v_add_f32_e32 v218, 0x358637bd, v218
	v_rsq_f32_e32 v218, v218
	s_nop 0
	v_lshlrev_b32_e32 v246, 16, v166
	v_and_b32_e32 v247, 0xffff0000, v166
	v_lshlrev_b32_e32 v248, 16, v167
	v_and_b32_e32 v249, 0xffff0000, v167
	v_mul_f32_e32 v246, v246, v218
	v_mul_f32_e32 v247, v247, v218
	v_mul_f32_e32 v248, v248, v218
	v_mul_f32_e32 v249, v249, v218
	v_lshlrev_b32_e32 v0, 16, v182
	v_and_b32_e32 v1, 0xffff0000, v182
	v_lshlrev_b32_e32 v2, 16, v183
	v_and_b32_e32 v3, 0xffff0000, v183
	v_fmac_f32_e32 v0, v246, v32
	v_fmac_f32_e32 v1, v247, v33
	v_fmac_f32_e32 v2, v248, v34
	v_fmac_f32_e32 v3, v249, v35
	v_lshlrev_b32_e32 v246, 16, v168
	v_and_b32_e32 v247, 0xffff0000, v168
	v_lshlrev_b32_e32 v248, 16, v169
	v_and_b32_e32 v249, 0xffff0000, v169
	v_mul_f32_e32 v246, v246, v218
	v_mul_f32_e32 v247, v247, v218
	v_mul_f32_e32 v248, v248, v218
	v_mul_f32_e32 v249, v249, v218
	v_lshlrev_b32_e32 v4, 16, v184
	v_and_b32_e32 v5, 0xffff0000, v184
	v_lshlrev_b32_e32 v6, 16, v185
	v_and_b32_e32 v7, 0xffff0000, v185
	v_fmac_f32_e32 v4, v246, v36
	v_fmac_f32_e32 v5, v247, v37
	v_fmac_f32_e32 v6, v248, v38
	v_fmac_f32_e32 v7, v249, v39
	v_lshlrev_b32_e32 v246, 16, v170
	v_and_b32_e32 v247, 0xffff0000, v170
	v_lshlrev_b32_e32 v248, 16, v171
	v_and_b32_e32 v249, 0xffff0000, v171
	v_mul_f32_e32 v246, v246, v218
	v_mul_f32_e32 v247, v247, v218
	v_mul_f32_e32 v248, v248, v218
	v_mul_f32_e32 v249, v249, v218
	v_lshlrev_b32_e32 v8, 16, v186
	v_and_b32_e32 v9, 0xffff0000, v186
	v_lshlrev_b32_e32 v10, 16, v187
	v_and_b32_e32 v11, 0xffff0000, v187
	v_fmac_f32_e32 v8, v246, v40
	v_fmac_f32_e32 v9, v247, v41
	v_fmac_f32_e32 v10, v248, v42
	v_fmac_f32_e32 v11, v249, v43
	v_lshlrev_b32_e32 v246, 16, v172
	v_and_b32_e32 v247, 0xffff0000, v172
	v_lshlrev_b32_e32 v248, 16, v173
	v_and_b32_e32 v249, 0xffff0000, v173
	v_mul_f32_e32 v246, v246, v218
	v_mul_f32_e32 v247, v247, v218
	v_mul_f32_e32 v248, v248, v218
	v_mul_f32_e32 v249, v249, v218
	v_lshlrev_b32_e32 v12, 16, v188
	v_and_b32_e32 v13, 0xffff0000, v188
	v_lshlrev_b32_e32 v14, 16, v189
	v_and_b32_e32 v15, 0xffff0000, v189
	v_fmac_f32_e32 v12, v246, v44
	v_fmac_f32_e32 v13, v247, v45
	v_fmac_f32_e32 v14, v248, v46
	v_fmac_f32_e32 v15, v249, v47
	v_lshlrev_b32_e32 v246, 16, v174
	v_and_b32_e32 v247, 0xffff0000, v174
	v_lshlrev_b32_e32 v248, 16, v175
	v_and_b32_e32 v249, 0xffff0000, v175
	v_mul_f32_e32 v246, v246, v218
	v_mul_f32_e32 v247, v247, v218
	v_mul_f32_e32 v248, v248, v218
	v_mul_f32_e32 v249, v249, v218
	v_lshlrev_b32_e32 v16, 16, v190
	v_and_b32_e32 v17, 0xffff0000, v190
	v_lshlrev_b32_e32 v18, 16, v191
	v_and_b32_e32 v19, 0xffff0000, v191
	v_fmac_f32_e32 v16, v246, v48
	v_fmac_f32_e32 v17, v247, v49
	v_fmac_f32_e32 v18, v248, v50
	v_fmac_f32_e32 v19, v249, v51
	v_lshlrev_b32_e32 v246, 16, v176
	v_and_b32_e32 v247, 0xffff0000, v176
	v_lshlrev_b32_e32 v248, 16, v177
	v_and_b32_e32 v249, 0xffff0000, v177
	v_mul_f32_e32 v246, v246, v218
	v_mul_f32_e32 v247, v247, v218
	v_mul_f32_e32 v248, v248, v218
	v_mul_f32_e32 v249, v249, v218
	v_lshlrev_b32_e32 v20, 16, v192
	v_and_b32_e32 v21, 0xffff0000, v192
	v_lshlrev_b32_e32 v22, 16, v193
	v_and_b32_e32 v23, 0xffff0000, v193
	v_fmac_f32_e32 v20, v246, v52
	v_fmac_f32_e32 v21, v247, v53
	v_fmac_f32_e32 v22, v248, v54
	v_fmac_f32_e32 v23, v249, v55
	v_lshlrev_b32_e32 v246, 16, v178
	v_and_b32_e32 v247, 0xffff0000, v178
	v_lshlrev_b32_e32 v248, 16, v179
	v_and_b32_e32 v249, 0xffff0000, v179
	v_mul_f32_e32 v246, v246, v218
	v_mul_f32_e32 v247, v247, v218
	v_mul_f32_e32 v248, v248, v218
	v_mul_f32_e32 v249, v249, v218
	v_lshlrev_b32_e32 v24, 16, v194
	v_and_b32_e32 v25, 0xffff0000, v194
	v_lshlrev_b32_e32 v26, 16, v195
	v_and_b32_e32 v27, 0xffff0000, v195
	v_fmac_f32_e32 v24, v246, v56
	v_fmac_f32_e32 v25, v247, v57
	v_fmac_f32_e32 v26, v248, v58
	v_fmac_f32_e32 v27, v249, v59
	v_lshlrev_b32_e32 v246, 16, v180
	v_and_b32_e32 v247, 0xffff0000, v180
	v_lshlrev_b32_e32 v248, 16, v181
	v_and_b32_e32 v249, 0xffff0000, v181
	v_mul_f32_e32 v246, v246, v218
	v_mul_f32_e32 v247, v247, v218
	v_mul_f32_e32 v248, v248, v218
	v_mul_f32_e32 v249, v249, v218
	v_lshlrev_b32_e32 v28, 16, v196
	v_and_b32_e32 v29, 0xffff0000, v196
	v_lshlrev_b32_e32 v30, 16, v197
	v_and_b32_e32 v31, 0xffff0000, v197
	v_fmac_f32_e32 v28, v246, v60
	v_fmac_f32_e32 v29, v247, v61
	v_fmac_f32_e32 v30, v248, v62
	v_fmac_f32_e32 v31, v249, v63
	v_mov_b32_e32 v250, 0
	v_mov_b32_e32 v251, 0
	v_cvt_pk_bf16_f32 v238, v0, v1
	v_cvt_pk_bf16_f32 v239, v2, v3
	v_fmac_f32_e32 v250, v0, v0
	v_fmac_f32_e32 v251, v1, v1
	v_fmac_f32_e32 v250, v2, v2
	v_fmac_f32_e32 v251, v3, v3
	global_store_dwordx2 v162, v[238:239], s[70:71]
	v_cvt_pk_bf16_f32 v240, v4, v5
	v_cvt_pk_bf16_f32 v241, v6, v7
	v_fmac_f32_e32 v250, v4, v4
	v_fmac_f32_e32 v251, v5, v5
	v_fmac_f32_e32 v250, v6, v6
	v_fmac_f32_e32 v251, v7, v7
	global_store_dwordx2 v162, v[240:241], s[70:71] offset:512
	v_cvt_pk_bf16_f32 v242, v8, v9
	v_cvt_pk_bf16_f32 v243, v10, v11
	v_fmac_f32_e32 v250, v8, v8
	v_fmac_f32_e32 v251, v9, v9
	v_fmac_f32_e32 v250, v10, v10
	v_fmac_f32_e32 v251, v11, v11
	global_store_dwordx2 v162, v[242:243], s[70:71] offset:1024
	v_cvt_pk_bf16_f32 v244, v12, v13
	v_cvt_pk_bf16_f32 v245, v14, v15
	v_fmac_f32_e32 v250, v12, v12
	v_fmac_f32_e32 v251, v13, v13
	v_fmac_f32_e32 v250, v14, v14
	v_fmac_f32_e32 v251, v15, v15
	global_store_dwordx2 v162, v[244:245], s[70:71] offset:1536
	v_cvt_pk_bf16_f32 v238, v16, v17
	v_cvt_pk_bf16_f32 v239, v18, v19
	v_fmac_f32_e32 v250, v16, v16
	v_fmac_f32_e32 v251, v17, v17
	v_fmac_f32_e32 v250, v18, v18
	v_fmac_f32_e32 v251, v19, v19
	global_store_dwordx2 v162, v[238:239], s[70:71] offset:2048
	v_cvt_pk_bf16_f32 v240, v20, v21
	v_cvt_pk_bf16_f32 v241, v22, v23
	v_fmac_f32_e32 v250, v20, v20
	v_fmac_f32_e32 v251, v21, v21
	v_fmac_f32_e32 v250, v22, v22
	v_fmac_f32_e32 v251, v23, v23
	global_store_dwordx2 v162, v[240:241], s[70:71] offset:2560
	v_cvt_pk_bf16_f32 v242, v24, v25
	v_cvt_pk_bf16_f32 v243, v26, v27
	v_fmac_f32_e32 v250, v24, v24
	v_fmac_f32_e32 v251, v25, v25
	v_fmac_f32_e32 v250, v26, v26
	v_fmac_f32_e32 v251, v27, v27
	global_store_dwordx2 v162, v[242:243], s[70:71] offset:3072
	v_cvt_pk_bf16_f32 v244, v28, v29
	v_cvt_pk_bf16_f32 v245, v30, v31
	v_fmac_f32_e32 v250, v28, v28
	v_fmac_f32_e32 v251, v29, v29
	v_fmac_f32_e32 v250, v30, v30
	v_fmac_f32_e32 v251, v31, v31
	global_store_dwordx2 v162, v[244:245], s[70:71] offset:3584
	s_add_u32 s70, s70, 0x8000
	s_addc_u32 s71, s71, 0
	v_add_f32_e32 v250, v250, v251
	s_nop 1
	v_add_f32_dpp v218, v250, v250 quad_perm:[1,0,3,2] row_mask:0xf bank_mask:0xf bound_ctrl:1
	s_nop 1
	v_add_f32_dpp v218, v218, v218 quad_perm:[2,3,0,1] row_mask:0xf bank_mask:0xf bound_ctrl:1
	s_nop 1
	v_add_f32_dpp v218, v218, v218 row_ror:4 row_mask:0xf bank_mask:0xf bound_ctrl:1
	s_nop 1
	v_add_f32_dpp v218, v218, v218 row_ror:8 row_mask:0xf bank_mask:0xf bound_ctrl:1
	s_nop 1
	v_readlane_b32 s8, v218, 0
	v_readlane_b32 s9, v218, 16
	v_readlane_b32 s10, v218, 32
	v_readlane_b32 s11, v218, 48
	s_nop 1
	v_mov_b32_e32 v218, s8
	v_add_f32_e32 v218, s9, v218
	v_mov_b32_e32 v219, s10
	v_add_f32_e32 v219, s11, v219
	v_add_f32_e32 v218, v218, v219
	v_mul_f32_e32 v218, 0x3a000000, v218
	v_add_f32_e32 v218, 0x358637bd, v218
	v_rsq_f32_e32 v218, v218
	s_nop 0
	v_mul_f32_e32 v246, v0, v218
	v_mul_f32_e32 v247, v1, v218
	v_mul_f32_e32 v248, v2, v218
	v_mul_f32_e32 v249, v3, v218
	v_fma_f32 v246, v246, v64, v96
	v_fma_f32 v247, v247, v65, v97
	v_fma_f32 v248, v248, v66, v98
	v_fma_f32 v249, v249, v67, v99
	v_cvt_pk_bf16_f32 v238, v246, v247
	v_cvt_pk_bf16_f32 v239, v248, v249
	global_store_dwordx2 v162, v[238:239], s[72:73]
	v_mul_f32_e32 v246, v4, v218
	v_mul_f32_e32 v247, v5, v218
	v_mul_f32_e32 v248, v6, v218
	v_mul_f32_e32 v249, v7, v218
	v_fma_f32 v246, v246, v68, v100
	v_fma_f32 v247, v247, v69, v101
	v_fma_f32 v248, v248, v70, v102
	v_fma_f32 v249, v249, v71, v103
	v_cvt_pk_bf16_f32 v240, v246, v247
	v_cvt_pk_bf16_f32 v241, v248, v249
	global_store_dwordx2 v162, v[240:241], s[72:73] offset:512
	v_mul_f32_e32 v246, v8, v218
	v_mul_f32_e32 v247, v9, v218
	v_mul_f32_e32 v248, v10, v218
	v_mul_f32_e32 v249, v11, v218
	v_fma_f32 v246, v246, v72, v104
	v_fma_f32 v247, v247, v73, v105
	v_fma_f32 v248, v248, v74, v106
	v_fma_f32 v249, v249, v75, v107
	v_cvt_pk_bf16_f32 v242, v246, v247
	v_cvt_pk_bf16_f32 v243, v248, v249
	global_store_dwordx2 v162, v[242:243], s[72:73] offset:1024
	v_mul_f32_e32 v246, v12, v218
	v_mul_f32_e32 v247, v13, v218
	v_mul_f32_e32 v248, v14, v218
	v_mul_f32_e32 v249, v15, v218
	v_fma_f32 v246, v246, v76, v108
	v_fma_f32 v247, v247, v77, v109
	v_fma_f32 v248, v248, v78, v110
	v_fma_f32 v249, v249, v79, v111
	v_cvt_pk_bf16_f32 v244, v246, v247
	v_cvt_pk_bf16_f32 v245, v248, v249
	global_store_dwordx2 v162, v[244:245], s[72:73] offset:1536
	v_mul_f32_e32 v246, v16, v218
	v_mul_f32_e32 v247, v17, v218
	v_mul_f32_e32 v248, v18, v218
	v_mul_f32_e32 v249, v19, v218
	v_fma_f32 v246, v246, v80, v112
	v_fma_f32 v247, v247, v81, v113
	v_fma_f32 v248, v248, v82, v114
	v_fma_f32 v249, v249, v83, v115
	v_cvt_pk_bf16_f32 v238, v246, v247
	v_cvt_pk_bf16_f32 v239, v248, v249
	global_store_dwordx2 v162, v[238:239], s[72:73] offset:2048
	v_mul_f32_e32 v246, v20, v218
	v_mul_f32_e32 v247, v21, v218
	v_mul_f32_e32 v248, v22, v218
	v_mul_f32_e32 v249, v23, v218
	v_fma_f32 v246, v246, v84, v116
	v_fma_f32 v247, v247, v85, v117
	v_fma_f32 v248, v248, v86, v118
	v_fma_f32 v249, v249, v87, v119
	v_cvt_pk_bf16_f32 v240, v246, v247
	v_cvt_pk_bf16_f32 v241, v248, v249
	global_store_dwordx2 v162, v[240:241], s[72:73] offset:2560
	v_mul_f32_e32 v246, v24, v218
	v_mul_f32_e32 v247, v25, v218
	v_mul_f32_e32 v248, v26, v218
	v_mul_f32_e32 v249, v27, v218
	v_fma_f32 v246, v246, v88, v120
	v_fma_f32 v247, v247, v89, v121
	v_fma_f32 v248, v248, v90, v122
	v_fma_f32 v249, v249, v91, v123
	v_cvt_pk_bf16_f32 v242, v246, v247
	v_cvt_pk_bf16_f32 v243, v248, v249
	global_store_dwordx2 v162, v[242:243], s[72:73] offset:3072
	v_mul_f32_e32 v246, v28, v218
	v_mul_f32_e32 v247, v29, v218
	v_mul_f32_e32 v248, v30, v218
	v_mul_f32_e32 v249, v31, v218
	v_fma_f32 v246, v246, v92, v124
	v_fma_f32 v247, v247, v93, v125
	v_fma_f32 v248, v248, v94, v126
	v_fma_f32 v249, v249, v95, v127
	v_cvt_pk_bf16_f32 v244, v246, v247
	v_cvt_pk_bf16_f32 v245, v248, v249
	global_store_dwordx2 v162, v[244:245], s[72:73] offset:3584
	s_add_u32 s72, s72, 0x8000
	s_addc_u32 s73, s73, 0
	s_branch .Lmp_done
.Lmp_V2:
	global_load_dwordx2 v[128:129], v162, s[56:57]
	global_load_dwordx2 v[130:131], v162, s[56:57] offset:512
	global_load_dwordx2 v[132:133], v162, s[56:57] offset:1024
	global_load_dwordx2 v[134:135], v162, s[56:57] offset:1536
	global_load_dwordx2 v[136:137], v162, s[56:57] offset:2048
	global_load_dwordx2 v[138:139], v162, s[56:57] offset:2560
	global_load_dwordx2 v[140:141], v162, s[56:57] offset:3072
	global_load_dwordx2 v[142:143], v162, s[56:57] offset:3584
	global_load_dwordx4 v[198:201], v163, s[58:59]
	global_load_dwordx4 v[202:205], v163, s[58:59] offset:1024
	global_load_dwordx4 v[206:209], v163, s[58:59] offset:2048
	global_load_dwordx4 v[210:213], v163, s[58:59] offset:3072
	s_add_u32 s10, s58, 0x1000
	s_addc_u32 s11, s59, 0
	global_load_dwordx4 v[214:217], v163, s[10:11]
	global_load_dwordx4 v[226:229], v163, s[10:11] offset:1024
	global_load_dwordx4 v[230:233], v163, s[10:11] offset:2048
	global_load_dwordx4 v[234:237], v163, s[10:11] offset:3072
	s_add_u32 s58, s58, 0x10000
	s_addc_u32 s59, s59, 0
	s_add_u32 s56, s56, 0x8000
	s_addc_u32 s57, s57, 0
	global_load_dwordx2 v[166:167], v162, s[56:57]
	global_load_dwordx2 v[168:169], v162, s[56:57] offset:512
	global_load_dwordx2 v[170:171], v162, s[56:57] offset:1024
	global_load_dwordx2 v[172:173], v162, s[56:57] offset:1536
	global_load_dwordx2 v[174:175], v162, s[56:57] offset:2048
	global_load_dwordx2 v[176:177], v162, s[56:57] offset:2560
	global_load_dwordx2 v[178:179], v162, s[56:57] offset:3072
	global_load_dwordx2 v[180:181], v162, s[56:57] offset:3584
	global_load_dwordx4 v[144:147], v163, s[58:59]
	global_load_dwordx4 v[148:151], v163, s[58:59] offset:1024
	global_load_dwordx4 v[152:155], v163, s[58:59] offset:2048
	global_load_dwordx4 v[156:159], v163, s[58:59] offset:3072
	s_add_u32 s10, s58, 0x1000
	s_addc_u32 s11, s59, 0
	global_load_dwordx4 v[182:185], v163, s[10:11]
	global_load_dwordx4 v[186:189], v163, s[10:11] offset:1024
	global_load_dwordx4 v[190:193], v163, s[10:11] offset:2048
	global_load_dwordx4 v[194:197], v163, s[10:11] offset:3072
	s_add_u32 s58, s58, 0x10000
	s_addc_u32 s59, s59, 0
	s_add_u32 s56, s56, 0x8000
	s_addc_u32 s57, s57, 0
	s_waitcnt vmcnt(16)
.Lmp_V2_loop:
	s_waitcnt vmcnt(32)
	v_mov_b32_e32 v250, 0
	v_mov_b32_e32 v251, 0
	v_lshlrev_b32_e32 v246, 16, v128
	v_and_b32_e32 v247, 0xffff0000, v128
	v_lshlrev_b32_e32 v248, 16, v129
	v_and_b32_e32 v249, 0xffff0000, v129
	v_fmac_f32_e32 v250, v246, v246
	v_fmac_f32_e32 v251, v247, v247
	v_fmac_f32_e32 v250, v248, v248
	v_fmac_f32_e32 v251, v249, v249
	v_lshlrev_b32_e32 v246, 16, v130
	v_and_b32_e32 v247, 0xffff0000, v130
	v_lshlrev_b32_e32 v248, 16, v131
	v_and_b32_e32 v249, 0xffff0000, v131
	v_fmac_f32_e32 v250, v246, v246
	v_fmac_f32_e32 v251, v247, v247
	v_fmac_f32_e32 v250, v248, v248
	v_fmac_f32_e32 v251, v249, v249
	v_lshlrev_b32_e32 v246, 16, v132
	v_and_b32_e32 v247, 0xffff0000, v132
	v_lshlrev_b32_e32 v248, 16, v133
	v_and_b32_e32 v249, 0xffff0000, v133
	v_fmac_f32_e32 v250, v246, v246
	v_fmac_f32_e32 v251, v247, v247
	v_fmac_f32_e32 v250, v248, v248
	v_fmac_f32_e32 v251, v249, v249
	v_lshlrev_b32_e32 v246, 16, v134
	v_and_b32_e32 v247, 0xffff0000, v134
	v_lshlrev_b32_e32 v248, 16, v135
	v_and_b32_e32 v249, 0xffff0000, v135
	v_fmac_f32_e32 v250, v246, v246
	v_fmac_f32_e32 v251, v247, v247
	v_fmac_f32_e32 v250, v248, v248
	v_fmac_f32_e32 v251, v249, v249
	v_lshlrev_b32_e32 v246, 16, v136
	v_and_b32_e32 v247, 0xffff0000, v136
	v_lshlrev_b32_e32 v248, 16, v137
	v_and_b32_e32 v249, 0xffff0000, v137
	v_fmac_f32_e32 v250, v246, v246
	v_fmac_f32_e32 v251, v247, v247
	v_fmac_f32_e32 v250, v248, v248
	v_fmac_f32_e32 v251, v249, v249
	v_lshlrev_b32_e32 v246, 16, v138
	v_and_b32_e32 v247, 0xffff0000, v138
	v_lshlrev_b32_e32 v248, 16, v139
	v_and_b32_e32 v249, 0xffff0000, v139
	v_fmac_f32_e32 v250, v246, v246
	v_fmac_f32_e32 v251, v247, v247
	v_fmac_f32_e32 v250, v248, v248
	v_fmac_f32_e32 v251, v249, v249
	v_lshlrev_b32_e32 v246, 16, v140
	v_and_b32_e32 v247, 0xffff0000, v140
	v_lshlrev_b32_e32 v248, 16, v141
	v_and_b32_e32 v249, 0xffff0000, v141
	v_fmac_f32_e32 v250, v246, v246
	v_fmac_f32_e32 v251, v247, v247
	v_fmac_f32_e32 v250, v248, v248
	v_fmac_f32_e32 v251, v249, v249
	v_lshlrev_b32_e32 v246, 16, v142
	v_and_b32_e32 v247, 0xffff0000, v142
	v_lshlrev_b32_e32 v248, 16, v143
	v_and_b32_e32 v249, 0xffff0000, v143
	v_fmac_f32_e32 v250, v246, v246
	v_fmac_f32_e32 v251, v247, v247
	v_fmac_f32_e32 v250, v248, v248
	v_fmac_f32_e32 v251, v249, v249
	v_add_f32_e32 v250, v250, v251
	s_nop 1
	v_add_f32_dpp v218, v250, v250 quad_perm:[1,0,3,2] row_mask:0xf bank_mask:0xf bound_ctrl:1
	s_nop 1
	v_add_f32_dpp v218, v218, v218 quad_perm:[2,3,0,1] row_mask:0xf bank_mask:0xf bound_ctrl:1
	s_nop 1
	v_add_f32_dpp v218, v218, v218 row_ror:4 row_mask:0xf bank_mask:0xf bound_ctrl:1
	s_nop 1
	v_add_f32_dpp v218, v218, v218 row_ror:8 row_mask:0xf bank_mask:0xf bound_ctrl:1
	s_nop 1
	v_readlane_b32 s8, v218, 0
	v_readlane_b32 s9, v218, 16
	v_readlane_b32 s10, v218, 32
	v_readlane_b32 s11, v218, 48
	s_nop 1
	v_mov_b32_e32 v218, s8
	v_add_f32_e32 v218, s9, v218
	v_mov_b32_e32 v219, s10
	v_add_f32_e32 v219, s11, v219
	v_add_f32_e32 v218, v218, v219
	v_mul_f32_e32 v218, 0x3a000000, v218
	v_add_f32_e32 v218, 0x358637bd, v218
	v_rsq_f32_e32 v218, v218
	s_nop 0
	v_lshlrev_b32_e32 v246, 16, v128
	v_and_b32_e32 v247, 0xffff0000, v128
	v_lshlrev_b32_e32 v248, 16, v129
	v_and_b32_e32 v249, 0xffff0000, v129
	v_mul_f32_e32 v246, v246, v218
	v_mul_f32_e32 v247, v247, v218
	v_mul_f32_e32 v248, v248, v218
	v_mul_f32_e32 v249, v249, v218
	v_fma_f32 v0, v246, v32, v198
	v_fma_f32 v1, v247, v33, v199
	v_fma_f32 v2, v248, v34, v200
	v_fma_f32 v3, v249, v35, v201
	v_lshlrev_b32_e32 v246, 16, v130
	v_and_b32_e32 v247, 0xffff0000, v130
	v_lshlrev_b32_e32 v248, 16, v131
	v_and_b32_e32 v249, 0xffff0000, v131
	v_mul_f32_e32 v246, v246, v218
	v_mul_f32_e32 v247, v247, v218
	v_mul_f32_e32 v248, v248, v218
	v_mul_f32_e32 v249, v249, v218
	v_fma_f32 v4, v246, v36, v202
	v_fma_f32 v5, v247, v37, v203
	v_fma_f32 v6, v248, v38, v204
	v_fma_f32 v7, v249, v39, v205
	v_lshlrev_b32_e32 v246, 16, v132
	v_and_b32_e32 v247, 0xffff0000, v132
	v_lshlrev_b32_e32 v248, 16, v133
	v_and_b32_e32 v249, 0xffff0000, v133
	v_mul_f32_e32 v246, v246, v218
	v_mul_f32_e32 v247, v247, v218
	v_mul_f32_e32 v248, v248, v218
	v_mul_f32_e32 v249, v249, v218
	v_fma_f32 v8, v246, v40, v206
	v_fma_f32 v9, v247, v41, v207
	v_fma_f32 v10, v248, v42, v208
	v_fma_f32 v11, v249, v43, v209
	v_lshlrev_b32_e32 v246, 16, v134
	v_and_b32_e32 v247, 0xffff0000, v134
	v_lshlrev_b32_e32 v248, 16, v135
	v_and_b32_e32 v249, 0xffff0000, v135
	v_mul_f32_e32 v246, v246, v218
	v_mul_f32_e32 v247, v247, v218
	v_mul_f32_e32 v248, v248, v218
	v_mul_f32_e32 v249, v249, v218
	v_fma_f32 v12, v246, v44, v210
	v_fma_f32 v13, v247, v45, v211
	v_fma_f32 v14, v248, v46, v212
	v_fma_f32 v15, v249, v47, v213
	v_lshlrev_b32_e32 v246, 16, v136
	v_and_b32_e32 v247, 0xffff0000, v136
	v_lshlrev_b32_e32 v248, 16, v137
	v_and_b32_e32 v249, 0xffff0000, v137
	v_mul_f32_e32 v246, v246, v218
	v_mul_f32_e32 v247, v247, v218
	v_mul_f32_e32 v248, v248, v218
	v_mul_f32_e32 v249, v249, v218
	v_fma_f32 v16, v246, v48, v214
	v_fma_f32 v17, v247, v49, v215
	v_fma_f32 v18, v248, v50, v216
	v_fma_f32 v19, v249, v51, v217
	v_lshlrev_b32_e32 v246, 16, v138
	v_and_b32_e32 v247, 0xffff0000, v138
	v_lshlrev_b32_e32 v248, 16, v139
	v_and_b32_e32 v249, 0xffff0000, v139
	v_mul_f32_e32 v246, v246, v218
	v_mul_f32_e32 v247, v247, v218
	v_mul_f32_e32 v248, v248, v218
	v_mul_f32_e32 v249, v249, v218
	v_fma_f32 v20, v246, v52, v226
	v_fma_f32 v21, v247, v53, v227
	v_fma_f32 v22, v248, v54, v228
	v_fma_f32 v23, v249, v55, v229
	v_lshlrev_b32_e32 v246, 16, v140
	v_and_b32_e32 v247, 0xffff0000, v140
	v_lshlrev_b32_e32 v248, 16, v141
	v_and_b32_e32 v249, 0xffff0000, v141
	v_mul_f32_e32 v246, v246, v218
	v_mul_f32_e32 v247, v247, v218
	v_mul_f32_e32 v248, v248, v218
	v_mul_f32_e32 v249, v249, v218
	v_fma_f32 v24, v246, v56, v230
	v_fma_f32 v25, v247, v57, v231
	v_fma_f32 v26, v248, v58, v232
	v_fma_f32 v27, v249, v59, v233
	v_lshlrev_b32_e32 v246, 16, v142
	v_and_b32_e32 v247, 0xffff0000, v142
	v_lshlrev_b32_e32 v248, 16, v143
	v_and_b32_e32 v249, 0xffff0000, v143
	v_mul_f32_e32 v246, v246, v218
	v_mul_f32_e32 v247, v247, v218
	v_mul_f32_e32 v248, v248, v218
	v_mul_f32_e32 v249, v249, v218
	v_fma_f32 v28, v246, v60, v234
	v_fma_f32 v29, v247, v61, v235
	v_fma_f32 v30, v248, v62, v236
	v_fma_f32 v31, v249, v63, v237
	global_load_dwordx2 v[128:129], v162, s[56:57]
	global_load_dwordx2 v[130:131], v162, s[56:57] offset:512
	global_load_dwordx2 v[132:133], v162, s[56:57] offset:1024
	global_load_dwordx2 v[134:135], v162, s[56:57] offset:1536
	global_load_dwordx2 v[136:137], v162, s[56:57] offset:2048
	global_load_dwordx2 v[138:139], v162, s[56:57] offset:2560
	global_load_dwordx2 v[140:141], v162, s[56:57] offset:3072
	global_load_dwordx2 v[142:143], v162, s[56:57] offset:3584
	global_load_dwordx4 v[198:201], v163, s[58:59]
	global_load_dwordx4 v[202:205], v163, s[58:59] offset:1024
	global_load_dwordx4 v[206:209], v163, s[58:59] offset:2048
	global_load_dwordx4 v[210:213], v163, s[58:59] offset:3072
	s_add_u32 s10, s58, 0x1000
	s_addc_u32 s11, s59, 0
	global_load_dwordx4 v[214:217], v163, s[10:11]
	global_load_dwordx4 v[226:229], v163, s[10:11] offset:1024
	global_load_dwordx4 v[230:233], v163, s[10:11] offset:2048
	global_load_dwordx4 v[234:237], v163, s[10:11] offset:3072
	s_add_u32 s58, s58, 0x10000
	s_addc_u32 s59, s59, 0
	s_add_u32 s56, s56, 0x8000
	s_addc_u32 s57, s57, 0
	v_mov_b32_e32 v250, 0
	v_mov_b32_e32 v251, 0
	v_cvt_pk_bf16_f32 v238, v0, v1
	v_cvt_pk_bf16_f32 v239, v2, v3
	v_fmac_f32_e32 v250, v0, v0
	v_fmac_f32_e32 v251, v1, v1
	v_fmac_f32_e32 v250, v2, v2
	v_fmac_f32_e32 v251, v3, v3
	global_store_dwordx2 v162, v[238:239], s[70:71]
	v_cvt_pk_bf16_f32 v240, v4, v5
	v_cvt_pk_bf16_f32 v241, v6, v7
	v_fmac_f32_e32 v250, v4, v4
	v_fmac_f32_e32 v251, v5, v5
	v_fmac_f32_e32 v250, v6, v6
	v_fmac_f32_e32 v251, v7, v7
	global_store_dwordx2 v162, v[240:241], s[70:71] offset:512
	v_cvt_pk_bf16_f32 v242, v8, v9
	v_cvt_pk_bf16_f32 v243, v10, v11
	v_fmac_f32_e32 v250, v8, v8
	v_fmac_f32_e32 v251, v9, v9
	v_fmac_f32_e32 v250, v10, v10
	v_fmac_f32_e32 v251, v11, v11
	global_store_dwordx2 v162, v[242:243], s[70:71] offset:1024
	v_cvt_pk_bf16_f32 v244, v12, v13
	v_cvt_pk_bf16_f32 v245, v14, v15
	v_fmac_f32_e32 v250, v12, v12
	v_fmac_f32_e32 v251, v13, v13
	v_fmac_f32_e32 v250, v14, v14
	v_fmac_f32_e32 v251, v15, v15
	global_store_dwordx2 v162, v[244:245], s[70:71] offset:1536
	v_cvt_pk_bf16_f32 v238, v16, v17
	v_cvt_pk_bf16_f32 v239, v18, v19
	v_fmac_f32_e32 v250, v16, v16
	v_fmac_f32_e32 v251, v17, v17
	v_fmac_f32_e32 v250, v18, v18
	v_fmac_f32_e32 v251, v19, v19
	global_store_dwordx2 v162, v[238:239], s[70:71] offset:2048
	v_cvt_pk_bf16_f32 v240, v20, v21
	v_cvt_pk_bf16_f32 v241, v22, v23
	v_fmac_f32_e32 v250, v20, v20
	v_fmac_f32_e32 v251, v21, v21
	v_fmac_f32_e32 v250, v22, v22
	v_fmac_f32_e32 v251, v23, v23
	global_store_dwordx2 v162, v[240:241], s[70:71] offset:2560
	v_cvt_pk_bf16_f32 v242, v24, v25
	v_cvt_pk_bf16_f32 v243, v26, v27
	v_fmac_f32_e32 v250, v24, v24
	v_fmac_f32_e32 v251, v25, v25
	v_fmac_f32_e32 v250, v26, v26
	v_fmac_f32_e32 v251, v27, v27
	global_store_dwordx2 v162, v[242:243], s[70:71] offset:3072
	v_cvt_pk_bf16_f32 v244, v28, v29
	v_cvt_pk_bf16_f32 v245, v30, v31
	v_fmac_f32_e32 v250, v28, v28
	v_fmac_f32_e32 v251, v29, v29
	v_fmac_f32_e32 v250, v30, v30
	v_fmac_f32_e32 v251, v31, v31
	global_store_dwordx2 v162, v[244:245], s[70:71] offset:3584
	s_add_u32 s70, s70, 0x8000
	s_addc_u32 s71, s71, 0
	v_add_f32_e32 v250, v250, v251
	s_nop 1
	v_add_f32_dpp v218, v250, v250 quad_perm:[1,0,3,2] row_mask:0xf bank_mask:0xf bound_ctrl:1
	s_nop 1
	v_add_f32_dpp v218, v218, v218 quad_perm:[2,3,0,1] row_mask:0xf bank_mask:0xf bound_ctrl:1
	s_nop 1
	v_add_f32_dpp v218, v218, v218 row_ror:4 row_mask:0xf bank_mask:0xf bound_ctrl:1
	s_nop 1
	v_add_f32_dpp v218, v218, v218 row_ror:8 row_mask:0xf bank_mask:0xf bound_ctrl:1
	s_nop 1
	v_readlane_b32 s8, v218, 0
	v_readlane_b32 s9, v218, 16
	v_readlane_b32 s10, v218, 32
	v_readlane_b32 s11, v218, 48
	s_nop 1
	v_mov_b32_e32 v218, s8
	v_add_f32_e32 v218, s9, v218
	v_mov_b32_e32 v219, s10
	v_add_f32_e32 v219, s11, v219
	v_add_f32_e32 v218, v218, v219
	v_mul_f32_e32 v218, 0x3a000000, v218
	v_add_f32_e32 v218, 0x358637bd, v218
	v_rsq_f32_e32 v218, v218
	s_nop 0
	v_mul_f32_e32 v246, v0, v218
	v_mul_f32_e32 v247, v1, v218
	v_mul_f32_e32 v248, v2, v218
	v_mul_f32_e32 v249, v3, v218
	v_fma_f32 v246, v246, v64, v96
	v_fma_f32 v247, v247, v65, v97
	v_fma_f32 v248, v248, v66, v98
	v_fma_f32 v249, v249, v67, v99
	v_cvt_pk_bf16_f32 v238, v246, v247
	v_cvt_pk_bf16_f32 v239, v248, v249
	global_store_dwordx2 v162, v[238:239], s[72:73]
	v_mul_f32_e32 v246, v4, v218
	v_mul_f32_e32 v247, v5, v218
	v_mul_f32_e32 v248, v6, v218
	v_mul_f32_e32 v249, v7, v218
	v_fma_f32 v246, v246, v68, v100
	v_fma_f32 v247, v247, v69, v101
	v_fma_f32 v248, v248, v70, v102
	v_fma_f32 v249, v249, v71, v103
	v_cvt_pk_bf16_f32 v240, v246, v247
	v_cvt_pk_bf16_f32 v241, v248, v249
	global_store_dwordx2 v162, v[240:241], s[72:73] offset:512
	v_mul_f32_e32 v246, v8, v218
	v_mul_f32_e32 v247, v9, v218
	v_mul_f32_e32 v248, v10, v218
	v_mul_f32_e32 v249, v11, v218
	v_fma_f32 v246, v246, v72, v104
	v_fma_f32 v247, v247, v73, v105
	v_fma_f32 v248, v248, v74, v106
	v_fma_f32 v249, v249, v75, v107
	v_cvt_pk_bf16_f32 v242, v246, v247
	v_cvt_pk_bf16_f32 v243, v248, v249
	global_store_dwordx2 v162, v[242:243], s[72:73] offset:1024
	v_mul_f32_e32 v246, v12, v218
	v_mul_f32_e32 v247, v13, v218
	v_mul_f32_e32 v248, v14, v218
	v_mul_f32_e32 v249, v15, v218
	v_fma_f32 v246, v246, v76, v108
	v_fma_f32 v247, v247, v77, v109
	v_fma_f32 v248, v248, v78, v110
	v_fma_f32 v249, v249, v79, v111
	v_cvt_pk_bf16_f32 v244, v246, v247
	v_cvt_pk_bf16_f32 v245, v248, v249
	global_store_dwordx2 v162, v[244:245], s[72:73] offset:1536
	v_mul_f32_e32 v246, v16, v218
	v_mul_f32_e32 v247, v17, v218
	v_mul_f32_e32 v248, v18, v218
	v_mul_f32_e32 v249, v19, v218
	v_fma_f32 v246, v246, v80, v112
	v_fma_f32 v247, v247, v81, v113
	v_fma_f32 v248, v248, v82, v114
	v_fma_f32 v249, v249, v83, v115
	v_cvt_pk_bf16_f32 v238, v246, v247
	v_cvt_pk_bf16_f32 v239, v248, v249
	global_store_dwordx2 v162, v[238:239], s[72:73] offset:2048
	v_mul_f32_e32 v246, v20, v218
	v_mul_f32_e32 v247, v21, v218
	v_mul_f32_e32 v248, v22, v218
	v_mul_f32_e32 v249, v23, v218
	v_fma_f32 v246, v246, v84, v116
	v_fma_f32 v247, v247, v85, v117
	v_fma_f32 v248, v248, v86, v118
	v_fma_f32 v249, v249, v87, v119
	v_cvt_pk_bf16_f32 v240, v246, v247
	v_cvt_pk_bf16_f32 v241, v248, v249
	global_store_dwordx2 v162, v[240:241], s[72:73] offset:2560
	v_mul_f32_e32 v246, v24, v218
	v_mul_f32_e32 v247, v25, v218
	v_mul_f32_e32 v248, v26, v218
	v_mul_f32_e32 v249, v27, v218
	v_fma_f32 v246, v246, v88, v120
	v_fma_f32 v247, v247, v89, v121
	v_fma_f32 v248, v248, v90, v122
	v_fma_f32 v249, v249, v91, v123
	v_cvt_pk_bf16_f32 v242, v246, v247
	v_cvt_pk_bf16_f32 v243, v248, v249
	global_store_dwordx2 v162, v[242:243], s[72:73] offset:3072
	v_mul_f32_e32 v246, v28, v218
	v_mul_f32_e32 v247, v29, v218
	v_mul_f32_e32 v248, v30, v218
	v_mul_f32_e32 v249, v31, v218
	v_fma_f32 v246, v246, v92, v124
	v_fma_f32 v247, v247, v93, v125
	v_fma_f32 v248, v248, v94, v126
	v_fma_f32 v249, v249, v95, v127
	v_cvt_pk_bf16_f32 v244, v246, v247
	v_cvt_pk_bf16_f32 v245, v248, v249
	global_store_dwordx2 v162, v[244:245], s[72:73] offset:3584
	s_add_u32 s72, s72, 0x8000
	s_addc_u32 s73, s73, 0
	s_waitcnt vmcnt(32)
	v_mov_b32_e32 v250, 0
	v_mov_b32_e32 v251, 0
	v_lshlrev_b32_e32 v246, 16, v166
	v_and_b32_e32 v247, 0xffff0000, v166
	v_lshlrev_b32_e32 v248, 16, v167
	v_and_b32_e32 v249, 0xffff0000, v167
	v_fmac_f32_e32 v250, v246, v246
	v_fmac_f32_e32 v251, v247, v247
	v_fmac_f32_e32 v250, v248, v248
	v_fmac_f32_e32 v251, v249, v249
	v_lshlrev_b32_e32 v246, 16, v168
	v_and_b32_e32 v247, 0xffff0000, v168
	v_lshlrev_b32_e32 v248, 16, v169
	v_and_b32_e32 v249, 0xffff0000, v169
	v_fmac_f32_e32 v250, v246, v246
	v_fmac_f32_e32 v251, v247, v247
	v_fmac_f32_e32 v250, v248, v248
	v_fmac_f32_e32 v251, v249, v249
	v_lshlrev_b32_e32 v246, 16, v170
	v_and_b32_e32 v247, 0xffff0000, v170
	v_lshlrev_b32_e32 v248, 16, v171
	v_and_b32_e32 v249, 0xffff0000, v171
	v_fmac_f32_e32 v250, v246, v246
	v_fmac_f32_e32 v251, v247, v247
	v_fmac_f32_e32 v250, v248, v248
	v_fmac_f32_e32 v251, v249, v249
	v_lshlrev_b32_e32 v246, 16, v172
	v_and_b32_e32 v247, 0xffff0000, v172
	v_lshlrev_b32_e32 v248, 16, v173
	v_and_b32_e32 v249, 0xffff0000, v173
	v_fmac_f32_e32 v250, v246, v246
	v_fmac_f32_e32 v251, v247, v247
	v_fmac_f32_e32 v250, v248, v248
	v_fmac_f32_e32 v251, v249, v249
	v_lshlrev_b32_e32 v246, 16, v174
	v_and_b32_e32 v247, 0xffff0000, v174
	v_lshlrev_b32_e32 v248, 16, v175
	v_and_b32_e32 v249, 0xffff0000, v175
	v_fmac_f32_e32 v250, v246, v246
	v_fmac_f32_e32 v251, v247, v247
	v_fmac_f32_e32 v250, v248, v248
	v_fmac_f32_e32 v251, v249, v249
	v_lshlrev_b32_e32 v246, 16, v176
	v_and_b32_e32 v247, 0xffff0000, v176
	v_lshlrev_b32_e32 v248, 16, v177
	v_and_b32_e32 v249, 0xffff0000, v177
	v_fmac_f32_e32 v250, v246, v246
	v_fmac_f32_e32 v251, v247, v247
	v_fmac_f32_e32 v250, v248, v248
	v_fmac_f32_e32 v251, v249, v249
	v_lshlrev_b32_e32 v246, 16, v178
	v_and_b32_e32 v247, 0xffff0000, v178
	v_lshlrev_b32_e32 v248, 16, v179
	v_and_b32_e32 v249, 0xffff0000, v179
	v_fmac_f32_e32 v250, v246, v246
	v_fmac_f32_e32 v251, v247, v247
	v_fmac_f32_e32 v250, v248, v248
	v_fmac_f32_e32 v251, v249, v249
	v_lshlrev_b32_e32 v246, 16, v180
	v_and_b32_e32 v247, 0xffff0000, v180
	v_lshlrev_b32_e32 v248, 16, v181
	v_and_b32_e32 v249, 0xffff0000, v181
	v_fmac_f32_e32 v250, v246, v246
	v_fmac_f32_e32 v251, v247, v247
	v_fmac_f32_e32 v250, v248, v248
	v_fmac_f32_e32 v251, v249, v249
	v_add_f32_e32 v250, v250, v251
	s_nop 1
	v_add_f32_dpp v218, v250, v250 quad_perm:[1,0,3,2] row_mask:0xf bank_mask:0xf bound_ctrl:1
	s_nop 1
	v_add_f32_dpp v218, v218, v218 quad_perm:[2,3,0,1] row_mask:0xf bank_mask:0xf bound_ctrl:1
	s_nop 1
	v_add_f32_dpp v218, v218, v218 row_ror:4 row_mask:0xf bank_mask:0xf bound_ctrl:1
	s_nop 1
	v_add_f32_dpp v218, v218, v218 row_ror:8 row_mask:0xf bank_mask:0xf bound_ctrl:1
	s_nop 1
	v_readlane_b32 s8, v218, 0
	v_readlane_b32 s9, v218, 16
	v_readlane_b32 s10, v218, 32
	v_readlane_b32 s11, v218, 48
	s_nop 1
	v_mov_b32_e32 v218, s8
	v_add_f32_e32 v218, s9, v218
	v_mov_b32_e32 v219, s10
	v_add_f32_e32 v219, s11, v219
	v_add_f32_e32 v218, v218, v219
	v_mul_f32_e32 v218, 0x3a000000, v218
	v_add_f32_e32 v218, 0x358637bd, v218
	v_rsq_f32_e32 v218, v218
	s_nop 0
	v_lshlrev_b32_e32 v246, 16, v166
	v_and_b32_e32 v247, 0xffff0000, v166
	v_lshlrev_b32_e32 v248, 16, v167
	v_and_b32_e32 v249, 0xffff0000, v167
	v_mul_f32_e32 v246, v246, v218
	v_mul_f32_e32 v247, v247, v218
	v_mul_f32_e32 v248, v248, v218
	v_mul_f32_e32 v249, v249, v218
	v_fma_f32 v0, v246, v32, v144
	v_fma_f32 v1, v247, v33, v145
	v_fma_f32 v2, v248, v34, v146
	v_fma_f32 v3, v249, v35, v147
	v_lshlrev_b32_e32 v246, 16, v168
	v_and_b32_e32 v247, 0xffff0000, v168
	v_lshlrev_b32_e32 v248, 16, v169
	v_and_b32_e32 v249, 0xffff0000, v169
	v_mul_f32_e32 v246, v246, v218
	v_mul_f32_e32 v247, v247, v218
	v_mul_f32_e32 v248, v248, v218
	v_mul_f32_e32 v249, v249, v218
	v_fma_f32 v4, v246, v36, v148
	v_fma_f32 v5, v247, v37, v149
	v_fma_f32 v6, v248, v38, v150
	v_fma_f32 v7, v249, v39, v151
	v_lshlrev_b32_e32 v246, 16, v170
	v_and_b32_e32 v247, 0xffff0000, v170
	v_lshlrev_b32_e32 v248, 16, v171
	v_and_b32_e32 v249, 0xffff0000, v171
	v_mul_f32_e32 v246, v246, v218
	v_mul_f32_e32 v247, v247, v218
	v_mul_f32_e32 v248, v248, v218
	v_mul_f32_e32 v249, v249, v218
	v_fma_f32 v8, v246, v40, v152
	v_fma_f32 v9, v247, v41, v153
	v_fma_f32 v10, v248, v42, v154
	v_fma_f32 v11, v249, v43, v155
	v_lshlrev_b32_e32 v246, 16, v172
	v_and_b32_e32 v247, 0xffff0000, v172
	v_lshlrev_b32_e32 v248, 16, v173
	v_and_b32_e32 v249, 0xffff0000, v173
	v_mul_f32_e32 v246, v246, v218
	v_mul_f32_e32 v247, v247, v218
	v_mul_f32_e32 v248, v248, v218
	v_mul_f32_e32 v249, v249, v218
	v_fma_f32 v12, v246, v44, v156
	v_fma_f32 v13, v247, v45, v157
	v_fma_f32 v14, v248, v46, v158
	v_fma_f32 v15, v249, v47, v159
	v_lshlrev_b32_e32 v246, 16, v174
	v_and_b32_e32 v247, 0xffff0000, v174
	v_lshlrev_b32_e32 v248, 16, v175
	v_and_b32_e32 v249, 0xffff0000, v175
	v_mul_f32_e32 v246, v246, v218
	v_mul_f32_e32 v247, v247, v218
	v_mul_f32_e32 v248, v248, v218
	v_mul_f32_e32 v249, v249, v218
	v_fma_f32 v16, v246, v48, v182
	v_fma_f32 v17, v247, v49, v183
	v_fma_f32 v18, v248, v50, v184
	v_fma_f32 v19, v249, v51, v185
	v_lshlrev_b32_e32 v246, 16, v176
	v_and_b32_e32 v247, 0xffff0000, v176
	v_lshlrev_b32_e32 v248, 16, v177
	v_and_b32_e32 v249, 0xffff0000, v177
	v_mul_f32_e32 v246, v246, v218
	v_mul_f32_e32 v247, v247, v218
	v_mul_f32_e32 v248, v248, v218
	v_mul_f32_e32 v249, v249, v218
	v_fma_f32 v20, v246, v52, v186
	v_fma_f32 v21, v247, v53, v187
	v_fma_f32 v22, v248, v54, v188
	v_fma_f32 v23, v249, v55, v189
	v_lshlrev_b32_e32 v246, 16, v178
	v_and_b32_e32 v247, 0xffff0000, v178
	v_lshlrev_b32_e32 v248, 16, v179
	v_and_b32_e32 v249, 0xffff0000, v179
	v_mul_f32_e32 v246, v246, v218
	v_mul_f32_e32 v247, v247, v218
	v_mul_f32_e32 v248, v248, v218
	v_mul_f32_e32 v249, v249, v218
	v_fma_f32 v24, v246, v56, v190
	v_fma_f32 v25, v247, v57, v191
	v_fma_f32 v26, v248, v58, v192
	v_fma_f32 v27, v249, v59, v193
	v_lshlrev_b32_e32 v246, 16, v180
	v_and_b32_e32 v247, 0xffff0000, v180
	v_lshlrev_b32_e32 v248, 16, v181
	v_and_b32_e32 v249, 0xffff0000, v181
	v_mul_f32_e32 v246, v246, v218
	v_mul_f32_e32 v247, v247, v218
	v_mul_f32_e32 v248, v248, v218
	v_mul_f32_e32 v249, v249, v218
	v_fma_f32 v28, v246, v60, v194
	v_fma_f32 v29, v247, v61, v195
	v_fma_f32 v30, v248, v62, v196
	v_fma_f32 v31, v249, v63, v197
	global_load_dwordx2 v[166:167], v162, s[56:57]
	global_load_dwordx2 v[168:169], v162, s[56:57] offset:512
	global_load_dwordx2 v[170:171], v162, s[56:57] offset:1024
	global_load_dwordx2 v[172:173], v162, s[56:57] offset:1536
	global_load_dwordx2 v[174:175], v162, s[56:57] offset:2048
	global_load_dwordx2 v[176:177], v162, s[56:57] offset:2560
	global_load_dwordx2 v[178:179], v162, s[56:57] offset:3072
	global_load_dwordx2 v[180:181], v162, s[56:57] offset:3584
	global_load_dwordx4 v[144:147], v163, s[58:59]
	global_load_dwordx4 v[148:151], v163, s[58:59] offset:1024
	global_load_dwordx4 v[152:155], v163, s[58:59] offset:2048
	global_load_dwordx4 v[156:159], v163, s[58:59] offset:3072
	s_add_u32 s10, s58, 0x1000
	s_addc_u32 s11, s59, 0
	global_load_dwordx4 v[182:185], v163, s[10:11]
	global_load_dwordx4 v[186:189], v163, s[10:11] offset:1024
	global_load_dwordx4 v[190:193], v163, s[10:11] offset:2048
	global_load_dwordx4 v[194:197], v163, s[10:11] offset:3072
	s_add_u32 s58, s58, 0x10000
	s_addc_u32 s59, s59, 0
	s_add_u32 s56, s56, 0x8000
	s_addc_u32 s57, s57, 0
	v_mov_b32_e32 v250, 0
	v_mov_b32_e32 v251, 0
	v_cvt_pk_bf16_f32 v238, v0, v1
	v_cvt_pk_bf16_f32 v239, v2, v3
	v_fmac_f32_e32 v250, v0, v0
	v_fmac_f32_e32 v251, v1, v1
	v_fmac_f32_e32 v250, v2, v2
	v_fmac_f32_e32 v251, v3, v3
	global_store_dwordx2 v162, v[238:239], s[70:71]
	v_cvt_pk_bf16_f32 v240, v4, v5
	v_cvt_pk_bf16_f32 v241, v6, v7
	v_fmac_f32_e32 v250, v4, v4
	v_fmac_f32_e32 v251, v5, v5
	v_fmac_f32_e32 v250, v6, v6
	v_fmac_f32_e32 v251, v7, v7
	global_store_dwordx2 v162, v[240:241], s[70:71] offset:512
	v_cvt_pk_bf16_f32 v242, v8, v9
	v_cvt_pk_bf16_f32 v243, v10, v11
	v_fmac_f32_e32 v250, v8, v8
	v_fmac_f32_e32 v251, v9, v9
	v_fmac_f32_e32 v250, v10, v10
	v_fmac_f32_e32 v251, v11, v11
	global_store_dwordx2 v162, v[242:243], s[70:71] offset:1024
	v_cvt_pk_bf16_f32 v244, v12, v13
	v_cvt_pk_bf16_f32 v245, v14, v15
	v_fmac_f32_e32 v250, v12, v12
	v_fmac_f32_e32 v251, v13, v13
	v_fmac_f32_e32 v250, v14, v14
	v_fmac_f32_e32 v251, v15, v15
	global_store_dwordx2 v162, v[244:245], s[70:71] offset:1536
	v_cvt_pk_bf16_f32 v238, v16, v17
	v_cvt_pk_bf16_f32 v239, v18, v19
	v_fmac_f32_e32 v250, v16, v16
	v_fmac_f32_e32 v251, v17, v17
	v_fmac_f32_e32 v250, v18, v18
	v_fmac_f32_e32 v251, v19, v19
	global_store_dwordx2 v162, v[238:239], s[70:71] offset:2048
	v_cvt_pk_bf16_f32 v240, v20, v21
	v_cvt_pk_bf16_f32 v241, v22, v23
	v_fmac_f32_e32 v250, v20, v20
	v_fmac_f32_e32 v251, v21, v21
	v_fmac_f32_e32 v250, v22, v22
	v_fmac_f32_e32 v251, v23, v23
	global_store_dwordx2 v162, v[240:241], s[70:71] offset:2560
	v_cvt_pk_bf16_f32 v242, v24, v25
	v_cvt_pk_bf16_f32 v243, v26, v27
	v_fmac_f32_e32 v250, v24, v24
	v_fmac_f32_e32 v251, v25, v25
	v_fmac_f32_e32 v250, v26, v26
	v_fmac_f32_e32 v251, v27, v27
	global_store_dwordx2 v162, v[242:243], s[70:71] offset:3072
	v_cvt_pk_bf16_f32 v244, v28, v29
	v_cvt_pk_bf16_f32 v245, v30, v31
	v_fmac_f32_e32 v250, v28, v28
	v_fmac_f32_e32 v251, v29, v29
	v_fmac_f32_e32 v250, v30, v30
	v_fmac_f32_e32 v251, v31, v31
	global_store_dwordx2 v162, v[244:245], s[70:71] offset:3584
	s_add_u32 s70, s70, 0x8000
	s_addc_u32 s71, s71, 0
	v_add_f32_e32 v250, v250, v251
	s_nop 1
	v_add_f32_dpp v218, v250, v250 quad_perm:[1,0,3,2] row_mask:0xf bank_mask:0xf bound_ctrl:1
	s_nop 1
	v_add_f32_dpp v218, v218, v218 quad_perm:[2,3,0,1] row_mask:0xf bank_mask:0xf bound_ctrl:1
	s_nop 1
	v_add_f32_dpp v218, v218, v218 row_ror:4 row_mask:0xf bank_mask:0xf bound_ctrl:1
	s_nop 1
	v_add_f32_dpp v218, v218, v218 row_ror:8 row_mask:0xf bank_mask:0xf bound_ctrl:1
	s_nop 1
	v_readlane_b32 s8, v218, 0
	v_readlane_b32 s9, v218, 16
	v_readlane_b32 s10, v218, 32
	v_readlane_b32 s11, v218, 48
	s_nop 1
	v_mov_b32_e32 v218, s8
	v_add_f32_e32 v218, s9, v218
	v_mov_b32_e32 v219, s10
	v_add_f32_e32 v219, s11, v219
	v_add_f32_e32 v218, v218, v219
	v_mul_f32_e32 v218, 0x3a000000, v218
	v_add_f32_e32 v218, 0x358637bd, v218
	v_rsq_f32_e32 v218, v218
	s_nop 0
	v_mul_f32_e32 v246, v0, v218
	v_mul_f32_e32 v247, v1, v218
	v_mul_f32_e32 v248, v2, v218
	v_mul_f32_e32 v249, v3, v218
	v_fma_f32 v246, v246, v64, v96
	v_fma_f32 v247, v247, v65, v97
	v_fma_f32 v248, v248, v66, v98
	v_fma_f32 v249, v249, v67, v99
	v_cvt_pk_bf16_f32 v238, v246, v247
	v_cvt_pk_bf16_f32 v239, v248, v249
	global_store_dwordx2 v162, v[238:239], s[72:73]
	v_mul_f32_e32 v246, v4, v218
	v_mul_f32_e32 v247, v5, v218
	v_mul_f32_e32 v248, v6, v218
	v_mul_f32_e32 v249, v7, v218
	v_fma_f32 v246, v246, v68, v100
	v_fma_f32 v247, v247, v69, v101
	v_fma_f32 v248, v248, v70, v102
	v_fma_f32 v249, v249, v71, v103
	v_cvt_pk_bf16_f32 v240, v246, v247
	v_cvt_pk_bf16_f32 v241, v248, v249
	global_store_dwordx2 v162, v[240:241], s[72:73] offset:512
	v_mul_f32_e32 v246, v8, v218
	v_mul_f32_e32 v247, v9, v218
	v_mul_f32_e32 v248, v10, v218
	v_mul_f32_e32 v249, v11, v218
	v_fma_f32 v246, v246, v72, v104
	v_fma_f32 v247, v247, v73, v105
	v_fma_f32 v248, v248, v74, v106
	v_fma_f32 v249, v249, v75, v107
	v_cvt_pk_bf16_f32 v242, v246, v247
	v_cvt_pk_bf16_f32 v243, v248, v249
	global_store_dwordx2 v162, v[242:243], s[72:73] offset:1024
	v_mul_f32_e32 v246, v12, v218
	v_mul_f32_e32 v247, v13, v218
	v_mul_f32_e32 v248, v14, v218
	v_mul_f32_e32 v249, v15, v218
	v_fma_f32 v246, v246, v76, v108
	v_fma_f32 v247, v247, v77, v109
	v_fma_f32 v248, v248, v78, v110
	v_fma_f32 v249, v249, v79, v111
	v_cvt_pk_bf16_f32 v244, v246, v247
	v_cvt_pk_bf16_f32 v245, v248, v249
	global_store_dwordx2 v162, v[244:245], s[72:73] offset:1536
	v_mul_f32_e32 v246, v16, v218
	v_mul_f32_e32 v247, v17, v218
	v_mul_f32_e32 v248, v18, v218
	v_mul_f32_e32 v249, v19, v218
	v_fma_f32 v246, v246, v80, v112
	v_fma_f32 v247, v247, v81, v113
	v_fma_f32 v248, v248, v82, v114
	v_fma_f32 v249, v249, v83, v115
	v_cvt_pk_bf16_f32 v238, v246, v247
	v_cvt_pk_bf16_f32 v239, v248, v249
	global_store_dwordx2 v162, v[238:239], s[72:73] offset:2048
	v_mul_f32_e32 v246, v20, v218
	v_mul_f32_e32 v247, v21, v218
	v_mul_f32_e32 v248, v22, v218
	v_mul_f32_e32 v249, v23, v218
	v_fma_f32 v246, v246, v84, v116
	v_fma_f32 v247, v247, v85, v117
	v_fma_f32 v248, v248, v86, v118
	v_fma_f32 v249, v249, v87, v119
	v_cvt_pk_bf16_f32 v240, v246, v247
	v_cvt_pk_bf16_f32 v241, v248, v249
	global_store_dwordx2 v162, v[240:241], s[72:73] offset:2560
	v_mul_f32_e32 v246, v24, v218
	v_mul_f32_e32 v247, v25, v218
	v_mul_f32_e32 v248, v26, v218
	v_mul_f32_e32 v249, v27, v218
	v_fma_f32 v246, v246, v88, v120
	v_fma_f32 v247, v247, v89, v121
	v_fma_f32 v248, v248, v90, v122
	v_fma_f32 v249, v249, v91, v123
	v_cvt_pk_bf16_f32 v242, v246, v247
	v_cvt_pk_bf16_f32 v243, v248, v249
	global_store_dwordx2 v162, v[242:243], s[72:73] offset:3072
	v_mul_f32_e32 v246, v28, v218
	v_mul_f32_e32 v247, v29, v218
	v_mul_f32_e32 v248, v30, v218
	v_mul_f32_e32 v249, v31, v218
	v_fma_f32 v246, v246, v92, v124
	v_fma_f32 v247, v247, v93, v125
	v_fma_f32 v248, v248, v94, v126
	v_fma_f32 v249, v249, v95, v127
	v_cvt_pk_bf16_f32 v244, v246, v247
	v_cvt_pk_bf16_f32 v245, v248, v249
	global_store_dwordx2 v162, v[244:245], s[72:73] offset:3584
	s_add_u32 s72, s72, 0x8000
	s_addc_u32 s73, s73, 0
	s_add_u32 s76, s76, 1
	s_cmp_lt_u32 s76, 7
	s_cbranch_scc1 .Lmp_V2_loop
	s_waitcnt vmcnt(32)
	v_mov_b32_e32 v250, 0
	v_mov_b32_e32 v251, 0
	v_lshlrev_b32_e32 v246, 16, v128
	v_and_b32_e32 v247, 0xffff0000, v128
	v_lshlrev_b32_e32 v248, 16, v129
	v_and_b32_e32 v249, 0xffff0000, v129
	v_fmac_f32_e32 v250, v246, v246
	v_fmac_f32_e32 v251, v247, v247
	v_fmac_f32_e32 v250, v248, v248
	v_fmac_f32_e32 v251, v249, v249
	v_lshlrev_b32_e32 v246, 16, v130
	v_and_b32_e32 v247, 0xffff0000, v130
	v_lshlrev_b32_e32 v248, 16, v131
	v_and_b32_e32 v249, 0xffff0000, v131
	v_fmac_f32_e32 v250, v246, v246
	v_fmac_f32_e32 v251, v247, v247
	v_fmac_f32_e32 v250, v248, v248
	v_fmac_f32_e32 v251, v249, v249
	v_lshlrev_b32_e32 v246, 16, v132
	v_and_b32_e32 v247, 0xffff0000, v132
	v_lshlrev_b32_e32 v248, 16, v133
	v_and_b32_e32 v249, 0xffff0000, v133
	v_fmac_f32_e32 v250, v246, v246
	v_fmac_f32_e32 v251, v247, v247
	v_fmac_f32_e32 v250, v248, v248
	v_fmac_f32_e32 v251, v249, v249
	v_lshlrev_b32_e32 v246, 16, v134
	v_and_b32_e32 v247, 0xffff0000, v134
	v_lshlrev_b32_e32 v248, 16, v135
	v_and_b32_e32 v249, 0xffff0000, v135
	v_fmac_f32_e32 v250, v246, v246
	v_fmac_f32_e32 v251, v247, v247
	v_fmac_f32_e32 v250, v248, v248
	v_fmac_f32_e32 v251, v249, v249
	v_lshlrev_b32_e32 v246, 16, v136
	v_and_b32_e32 v247, 0xffff0000, v136
	v_lshlrev_b32_e32 v248, 16, v137
	v_and_b32_e32 v249, 0xffff0000, v137
	v_fmac_f32_e32 v250, v246, v246
	v_fmac_f32_e32 v251, v247, v247
	v_fmac_f32_e32 v250, v248, v248
	v_fmac_f32_e32 v251, v249, v249
	v_lshlrev_b32_e32 v246, 16, v138
	v_and_b32_e32 v247, 0xffff0000, v138
	v_lshlrev_b32_e32 v248, 16, v139
	v_and_b32_e32 v249, 0xffff0000, v139
	v_fmac_f32_e32 v250, v246, v246
	v_fmac_f32_e32 v251, v247, v247
	v_fmac_f32_e32 v250, v248, v248
	v_fmac_f32_e32 v251, v249, v249
	v_lshlrev_b32_e32 v246, 16, v140
	v_and_b32_e32 v247, 0xffff0000, v140
	v_lshlrev_b32_e32 v248, 16, v141
	v_and_b32_e32 v249, 0xffff0000, v141
	v_fmac_f32_e32 v250, v246, v246
	v_fmac_f32_e32 v251, v247, v247
	v_fmac_f32_e32 v250, v248, v248
	v_fmac_f32_e32 v251, v249, v249
	v_lshlrev_b32_e32 v246, 16, v142
	v_and_b32_e32 v247, 0xffff0000, v142
	v_lshlrev_b32_e32 v248, 16, v143
	v_and_b32_e32 v249, 0xffff0000, v143
	v_fmac_f32_e32 v250, v246, v246
	v_fmac_f32_e32 v251, v247, v247
	v_fmac_f32_e32 v250, v248, v248
	v_fmac_f32_e32 v251, v249, v249
	v_add_f32_e32 v250, v250, v251
	s_nop 1
	v_add_f32_dpp v218, v250, v250 quad_perm:[1,0,3,2] row_mask:0xf bank_mask:0xf bound_ctrl:1
	s_nop 1
	v_add_f32_dpp v218, v218, v218 quad_perm:[2,3,0,1] row_mask:0xf bank_mask:0xf bound_ctrl:1
	s_nop 1
	v_add_f32_dpp v218, v218, v218 row_ror:4 row_mask:0xf bank_mask:0xf bound_ctrl:1
	s_nop 1
	v_add_f32_dpp v218, v218, v218 row_ror:8 row_mask:0xf bank_mask:0xf bound_ctrl:1
	s_nop 1
	v_readlane_b32 s8, v218, 0
	v_readlane_b32 s9, v218, 16
	v_readlane_b32 s10, v218, 32
	v_readlane_b32 s11, v218, 48
	s_nop 1
	v_mov_b32_e32 v218, s8
	v_add_f32_e32 v218, s9, v218
	v_mov_b32_e32 v219, s10
	v_add_f32_e32 v219, s11, v219
	v_add_f32_e32 v218, v218, v219
	v_mul_f32_e32 v218, 0x3a000000, v218
	v_add_f32_e32 v218, 0x358637bd, v218
	v_rsq_f32_e32 v218, v218
	s_nop 0
	v_lshlrev_b32_e32 v246, 16, v128
	v_and_b32_e32 v247, 0xffff0000, v128
	v_lshlrev_b32_e32 v248, 16, v129
	v_and_b32_e32 v249, 0xffff0000, v129
	v_mul_f32_e32 v246, v246, v218
	v_mul_f32_e32 v247, v247, v218
	v_mul_f32_e32 v248, v248, v218
	v_mul_f32_e32 v249, v249, v218
	v_fma_f32 v0, v246, v32, v198
	v_fma_f32 v1, v247, v33, v199
	v_fma_f32 v2, v248, v34, v200
	v_fma_f32 v3, v249, v35, v201
	v_lshlrev_b32_e32 v246, 16, v130
	v_and_b32_e32 v247, 0xffff0000, v130
	v_lshlrev_b32_e32 v248, 16, v131
	v_and_b32_e32 v249, 0xffff0000, v131
	v_mul_f32_e32 v246, v246, v218
	v_mul_f32_e32 v247, v247, v218
	v_mul_f32_e32 v248, v248, v218
	v_mul_f32_e32 v249, v249, v218
	v_fma_f32 v4, v246, v36, v202
	v_fma_f32 v5, v247, v37, v203
	v_fma_f32 v6, v248, v38, v204
	v_fma_f32 v7, v249, v39, v205
	v_lshlrev_b32_e32 v246, 16, v132
	v_and_b32_e32 v247, 0xffff0000, v132
	v_lshlrev_b32_e32 v248, 16, v133
	v_and_b32_e32 v249, 0xffff0000, v133
	v_mul_f32_e32 v246, v246, v218
	v_mul_f32_e32 v247, v247, v218
	v_mul_f32_e32 v248, v248, v218
	v_mul_f32_e32 v249, v249, v218
	v_fma_f32 v8, v246, v40, v206
	v_fma_f32 v9, v247, v41, v207
	v_fma_f32 v10, v248, v42, v208
	v_fma_f32 v11, v249, v43, v209
	v_lshlrev_b32_e32 v246, 16, v134
	v_and_b32_e32 v247, 0xffff0000, v134
	v_lshlrev_b32_e32 v248, 16, v135
	v_and_b32_e32 v249, 0xffff0000, v135
	v_mul_f32_e32 v246, v246, v218
	v_mul_f32_e32 v247, v247, v218
	v_mul_f32_e32 v248, v248, v218
	v_mul_f32_e32 v249, v249, v218
	v_fma_f32 v12, v246, v44, v210
	v_fma_f32 v13, v247, v45, v211
	v_fma_f32 v14, v248, v46, v212
	v_fma_f32 v15, v249, v47, v213
	v_lshlrev_b32_e32 v246, 16, v136
	v_and_b32_e32 v247, 0xffff0000, v136
	v_lshlrev_b32_e32 v248, 16, v137
	v_and_b32_e32 v249, 0xffff0000, v137
	v_mul_f32_e32 v246, v246, v218
	v_mul_f32_e32 v247, v247, v218
	v_mul_f32_e32 v248, v248, v218
	v_mul_f32_e32 v249, v249, v218
	v_fma_f32 v16, v246, v48, v214
	v_fma_f32 v17, v247, v49, v215
	v_fma_f32 v18, v248, v50, v216
	v_fma_f32 v19, v249, v51, v217
	v_lshlrev_b32_e32 v246, 16, v138
	v_and_b32_e32 v247, 0xffff0000, v138
	v_lshlrev_b32_e32 v248, 16, v139
	v_and_b32_e32 v249, 0xffff0000, v139
	v_mul_f32_e32 v246, v246, v218
	v_mul_f32_e32 v247, v247, v218
	v_mul_f32_e32 v248, v248, v218
	v_mul_f32_e32 v249, v249, v218
	v_fma_f32 v20, v246, v52, v226
	v_fma_f32 v21, v247, v53, v227
	v_fma_f32 v22, v248, v54, v228
	v_fma_f32 v23, v249, v55, v229
	v_lshlrev_b32_e32 v246, 16, v140
	v_and_b32_e32 v247, 0xffff0000, v140
	v_lshlrev_b32_e32 v248, 16, v141
	v_and_b32_e32 v249, 0xffff0000, v141
	v_mul_f32_e32 v246, v246, v218
	v_mul_f32_e32 v247, v247, v218
	v_mul_f32_e32 v248, v248, v218
	v_mul_f32_e32 v249, v249, v218
	v_fma_f32 v24, v246, v56, v230
	v_fma_f32 v25, v247, v57, v231
	v_fma_f32 v26, v248, v58, v232
	v_fma_f32 v27, v249, v59, v233
	v_lshlrev_b32_e32 v246, 16, v142
	v_and_b32_e32 v247, 0xffff0000, v142
	v_lshlrev_b32_e32 v248, 16, v143
	v_and_b32_e32 v249, 0xffff0000, v143
	v_mul_f32_e32 v246, v246, v218
	v_mul_f32_e32 v247, v247, v218
	v_mul_f32_e32 v248, v248, v218
	v_mul_f32_e32 v249, v249, v218
	v_fma_f32 v28, v246, v60, v234
	v_fma_f32 v29, v247, v61, v235
	v_fma_f32 v30, v248, v62, v236
	v_fma_f32 v31, v249, v63, v237
	v_mov_b32_e32 v250, 0
	v_mov_b32_e32 v251, 0
	v_cvt_pk_bf16_f32 v238, v0, v1
	v_cvt_pk_bf16_f32 v239, v2, v3
	v_fmac_f32_e32 v250, v0, v0
	v_fmac_f32_e32 v251, v1, v1
	v_fmac_f32_e32 v250, v2, v2
	v_fmac_f32_e32 v251, v3, v3
	global_store_dwordx2 v162, v[238:239], s[70:71]
	v_cvt_pk_bf16_f32 v240, v4, v5
	v_cvt_pk_bf16_f32 v241, v6, v7
	v_fmac_f32_e32 v250, v4, v4
	v_fmac_f32_e32 v251, v5, v5
	v_fmac_f32_e32 v250, v6, v6
	v_fmac_f32_e32 v251, v7, v7
	global_store_dwordx2 v162, v[240:241], s[70:71] offset:512
	v_cvt_pk_bf16_f32 v242, v8, v9
	v_cvt_pk_bf16_f32 v243, v10, v11
	v_fmac_f32_e32 v250, v8, v8
	v_fmac_f32_e32 v251, v9, v9
	v_fmac_f32_e32 v250, v10, v10
	v_fmac_f32_e32 v251, v11, v11
	global_store_dwordx2 v162, v[242:243], s[70:71] offset:1024
	v_cvt_pk_bf16_f32 v244, v12, v13
	v_cvt_pk_bf16_f32 v245, v14, v15
	v_fmac_f32_e32 v250, v12, v12
	v_fmac_f32_e32 v251, v13, v13
	v_fmac_f32_e32 v250, v14, v14
	v_fmac_f32_e32 v251, v15, v15
	global_store_dwordx2 v162, v[244:245], s[70:71] offset:1536
	v_cvt_pk_bf16_f32 v238, v16, v17
	v_cvt_pk_bf16_f32 v239, v18, v19
	v_fmac_f32_e32 v250, v16, v16
	v_fmac_f32_e32 v251, v17, v17
	v_fmac_f32_e32 v250, v18, v18
	v_fmac_f32_e32 v251, v19, v19
	global_store_dwordx2 v162, v[238:239], s[70:71] offset:2048
	v_cvt_pk_bf16_f32 v240, v20, v21
	v_cvt_pk_bf16_f32 v241, v22, v23
	v_fmac_f32_e32 v250, v20, v20
	v_fmac_f32_e32 v251, v21, v21
	v_fmac_f32_e32 v250, v22, v22
	v_fmac_f32_e32 v251, v23, v23
	global_store_dwordx2 v162, v[240:241], s[70:71] offset:2560
	v_cvt_pk_bf16_f32 v242, v24, v25
	v_cvt_pk_bf16_f32 v243, v26, v27
	v_fmac_f32_e32 v250, v24, v24
	v_fmac_f32_e32 v251, v25, v25
	v_fmac_f32_e32 v250, v26, v26
	v_fmac_f32_e32 v251, v27, v27
	global_store_dwordx2 v162, v[242:243], s[70:71] offset:3072
	v_cvt_pk_bf16_f32 v244, v28, v29
	v_cvt_pk_bf16_f32 v245, v30, v31
	v_fmac_f32_e32 v250, v28, v28
	v_fmac_f32_e32 v251, v29, v29
	v_fmac_f32_e32 v250, v30, v30
	v_fmac_f32_e32 v251, v31, v31
	global_store_dwordx2 v162, v[244:245], s[70:71] offset:3584
	s_add_u32 s70, s70, 0x8000
	s_addc_u32 s71, s71, 0
	v_add_f32_e32 v250, v250, v251
	s_nop 1
	v_add_f32_dpp v218, v250, v250 quad_perm:[1,0,3,2] row_mask:0xf bank_mask:0xf bound_ctrl:1
	s_nop 1
	v_add_f32_dpp v218, v218, v218 quad_perm:[2,3,0,1] row_mask:0xf bank_mask:0xf bound_ctrl:1
	s_nop 1
	v_add_f32_dpp v218, v218, v218 row_ror:4 row_mask:0xf bank_mask:0xf bound_ctrl:1
	s_nop 1
	v_add_f32_dpp v218, v218, v218 row_ror:8 row_mask:0xf bank_mask:0xf bound_ctrl:1
	s_nop 1
	v_readlane_b32 s8, v218, 0
	v_readlane_b32 s9, v218, 16
	v_readlane_b32 s10, v218, 32
	v_readlane_b32 s11, v218, 48
	s_nop 1
	v_mov_b32_e32 v218, s8
	v_add_f32_e32 v218, s9, v218
	v_mov_b32_e32 v219, s10
	v_add_f32_e32 v219, s11, v219
	v_add_f32_e32 v218, v218, v219
	v_mul_f32_e32 v218, 0x3a000000, v218
	v_add_f32_e32 v218, 0x358637bd, v218
	v_rsq_f32_e32 v218, v218
	s_nop 0
	v_mul_f32_e32 v246, v0, v218
	v_mul_f32_e32 v247, v1, v218
	v_mul_f32_e32 v248, v2, v218
	v_mul_f32_e32 v249, v3, v218
	v_fma_f32 v246, v246, v64, v96
	v_fma_f32 v247, v247, v65, v97
	v_fma_f32 v248, v248, v66, v98
	v_fma_f32 v249, v249, v67, v99
	v_cvt_pk_bf16_f32 v238, v246, v247
	v_cvt_pk_bf16_f32 v239, v248, v249
	global_store_dwordx2 v162, v[238:239], s[72:73]
	v_mul_f32_e32 v246, v4, v218
	v_mul_f32_e32 v247, v5, v218
	v_mul_f32_e32 v248, v6, v218
	v_mul_f32_e32 v249, v7, v218
	v_fma_f32 v246, v246, v68, v100
	v_fma_f32 v247, v247, v69, v101
	v_fma_f32 v248, v248, v70, v102
	v_fma_f32 v249, v249, v71, v103
	v_cvt_pk_bf16_f32 v240, v246, v247
	v_cvt_pk_bf16_f32 v241, v248, v249
	global_store_dwordx2 v162, v[240:241], s[72:73] offset:512
	v_mul_f32_e32 v246, v8, v218
	v_mul_f32_e32 v247, v9, v218
	v_mul_f32_e32 v248, v10, v218
	v_mul_f32_e32 v249, v11, v218
	v_fma_f32 v246, v246, v72, v104
	v_fma_f32 v247, v247, v73, v105
	v_fma_f32 v248, v248, v74, v106
	v_fma_f32 v249, v249, v75, v107
	v_cvt_pk_bf16_f32 v242, v246, v247
	v_cvt_pk_bf16_f32 v243, v248, v249
	global_store_dwordx2 v162, v[242:243], s[72:73] offset:1024
	v_mul_f32_e32 v246, v12, v218
	v_mul_f32_e32 v247, v13, v218
	v_mul_f32_e32 v248, v14, v218
	v_mul_f32_e32 v249, v15, v218
	v_fma_f32 v246, v246, v76, v108
	v_fma_f32 v247, v247, v77, v109
	v_fma_f32 v248, v248, v78, v110
	v_fma_f32 v249, v249, v79, v111
	v_cvt_pk_bf16_f32 v244, v246, v247
	v_cvt_pk_bf16_f32 v245, v248, v249
	global_store_dwordx2 v162, v[244:245], s[72:73] offset:1536
	v_mul_f32_e32 v246, v16, v218
	v_mul_f32_e32 v247, v17, v218
	v_mul_f32_e32 v248, v18, v218
	v_mul_f32_e32 v249, v19, v218
	v_fma_f32 v246, v246, v80, v112
	v_fma_f32 v247, v247, v81, v113
	v_fma_f32 v248, v248, v82, v114
	v_fma_f32 v249, v249, v83, v115
	v_cvt_pk_bf16_f32 v238, v246, v247
	v_cvt_pk_bf16_f32 v239, v248, v249
	global_store_dwordx2 v162, v[238:239], s[72:73] offset:2048
	v_mul_f32_e32 v246, v20, v218
	v_mul_f32_e32 v247, v21, v218
	v_mul_f32_e32 v248, v22, v218
	v_mul_f32_e32 v249, v23, v218
	v_fma_f32 v246, v246, v84, v116
	v_fma_f32 v247, v247, v85, v117
	v_fma_f32 v248, v248, v86, v118
	v_fma_f32 v249, v249, v87, v119
	v_cvt_pk_bf16_f32 v240, v246, v247
	v_cvt_pk_bf16_f32 v241, v248, v249
	global_store_dwordx2 v162, v[240:241], s[72:73] offset:2560
	v_mul_f32_e32 v246, v24, v218
	v_mul_f32_e32 v247, v25, v218
	v_mul_f32_e32 v248, v26, v218
	v_mul_f32_e32 v249, v27, v218
	v_fma_f32 v246, v246, v88, v120
	v_fma_f32 v247, v247, v89, v121
	v_fma_f32 v248, v248, v90, v122
	v_fma_f32 v249, v249, v91, v123
	v_cvt_pk_bf16_f32 v242, v246, v247
	v_cvt_pk_bf16_f32 v243, v248, v249
	global_store_dwordx2 v162, v[242:243], s[72:73] offset:3072
	v_mul_f32_e32 v246, v28, v218
	v_mul_f32_e32 v247, v29, v218
	v_mul_f32_e32 v248, v30, v218
	v_mul_f32_e32 v249, v31, v218
	v_fma_f32 v246, v246, v92, v124
	v_fma_f32 v247, v247, v93, v125
	v_fma_f32 v248, v248, v94, v126
	v_fma_f32 v249, v249, v95, v127
	v_cvt_pk_bf16_f32 v244, v246, v247
	v_cvt_pk_bf16_f32 v245, v248, v249
	global_store_dwordx2 v162, v[244:245], s[72:73] offset:3584
	s_add_u32 s72, s72, 0x8000
	s_addc_u32 s73, s73, 0
	s_waitcnt vmcnt(32)
	v_mov_b32_e32 v250, 0
	v_mov_b32_e32 v251, 0
	v_lshlrev_b32_e32 v246, 16, v166
	v_and_b32_e32 v247, 0xffff0000, v166
	v_lshlrev_b32_e32 v248, 16, v167
	v_and_b32_e32 v249, 0xffff0000, v167
	v_fmac_f32_e32 v250, v246, v246
	v_fmac_f32_e32 v251, v247, v247
	v_fmac_f32_e32 v250, v248, v248
	v_fmac_f32_e32 v251, v249, v249
	v_lshlrev_b32_e32 v246, 16, v168
	v_and_b32_e32 v247, 0xffff0000, v168
	v_lshlrev_b32_e32 v248, 16, v169
	v_and_b32_e32 v249, 0xffff0000, v169
	v_fmac_f32_e32 v250, v246, v246
	v_fmac_f32_e32 v251, v247, v247
	v_fmac_f32_e32 v250, v248, v248
	v_fmac_f32_e32 v251, v249, v249
	v_lshlrev_b32_e32 v246, 16, v170
	v_and_b32_e32 v247, 0xffff0000, v170
	v_lshlrev_b32_e32 v248, 16, v171
	v_and_b32_e32 v249, 0xffff0000, v171
	v_fmac_f32_e32 v250, v246, v246
	v_fmac_f32_e32 v251, v247, v247
	v_fmac_f32_e32 v250, v248, v248
	v_fmac_f32_e32 v251, v249, v249
	v_lshlrev_b32_e32 v246, 16, v172
	v_and_b32_e32 v247, 0xffff0000, v172
	v_lshlrev_b32_e32 v248, 16, v173
	v_and_b32_e32 v249, 0xffff0000, v173
	v_fmac_f32_e32 v250, v246, v246
	v_fmac_f32_e32 v251, v247, v247
	v_fmac_f32_e32 v250, v248, v248
	v_fmac_f32_e32 v251, v249, v249
	v_lshlrev_b32_e32 v246, 16, v174
	v_and_b32_e32 v247, 0xffff0000, v174
	v_lshlrev_b32_e32 v248, 16, v175
	v_and_b32_e32 v249, 0xffff0000, v175
	v_fmac_f32_e32 v250, v246, v246
	v_fmac_f32_e32 v251, v247, v247
	v_fmac_f32_e32 v250, v248, v248
	v_fmac_f32_e32 v251, v249, v249
	v_lshlrev_b32_e32 v246, 16, v176
	v_and_b32_e32 v247, 0xffff0000, v176
	v_lshlrev_b32_e32 v248, 16, v177
	v_and_b32_e32 v249, 0xffff0000, v177
	v_fmac_f32_e32 v250, v246, v246
	v_fmac_f32_e32 v251, v247, v247
	v_fmac_f32_e32 v250, v248, v248
	v_fmac_f32_e32 v251, v249, v249
	v_lshlrev_b32_e32 v246, 16, v178
	v_and_b32_e32 v247, 0xffff0000, v178
	v_lshlrev_b32_e32 v248, 16, v179
	v_and_b32_e32 v249, 0xffff0000, v179
	v_fmac_f32_e32 v250, v246, v246
	v_fmac_f32_e32 v251, v247, v247
	v_fmac_f32_e32 v250, v248, v248
	v_fmac_f32_e32 v251, v249, v249
	v_lshlrev_b32_e32 v246, 16, v180
	v_and_b32_e32 v247, 0xffff0000, v180
	v_lshlrev_b32_e32 v248, 16, v181
	v_and_b32_e32 v249, 0xffff0000, v181
	v_fmac_f32_e32 v250, v246, v246
	v_fmac_f32_e32 v251, v247, v247
	v_fmac_f32_e32 v250, v248, v248
	v_fmac_f32_e32 v251, v249, v249
	v_add_f32_e32 v250, v250, v251
	s_nop 1
	v_add_f32_dpp v218, v250, v250 quad_perm:[1,0,3,2] row_mask:0xf bank_mask:0xf bound_ctrl:1
	s_nop 1
	v_add_f32_dpp v218, v218, v218 quad_perm:[2,3,0,1] row_mask:0xf bank_mask:0xf bound_ctrl:1
	s_nop 1
	v_add_f32_dpp v218, v218, v218 row_ror:4 row_mask:0xf bank_mask:0xf bound_ctrl:1
	s_nop 1
	v_add_f32_dpp v218, v218, v218 row_ror:8 row_mask:0xf bank_mask:0xf bound_ctrl:1
	s_nop 1
	v_readlane_b32 s8, v218, 0
	v_readlane_b32 s9, v218, 16
	v_readlane_b32 s10, v218, 32
	v_readlane_b32 s11, v218, 48
	s_nop 1
	v_mov_b32_e32 v218, s8
	v_add_f32_e32 v218, s9, v218
	v_mov_b32_e32 v219, s10
	v_add_f32_e32 v219, s11, v219
	v_add_f32_e32 v218, v218, v219
	v_mul_f32_e32 v218, 0x3a000000, v218
	v_add_f32_e32 v218, 0x358637bd, v218
	v_rsq_f32_e32 v218, v218
	s_nop 0
	v_lshlrev_b32_e32 v246, 16, v166
	v_and_b32_e32 v247, 0xffff0000, v166
	v_lshlrev_b32_e32 v248, 16, v167
	v_and_b32_e32 v249, 0xffff0000, v167
	v_mul_f32_e32 v246, v246, v218
	v_mul_f32_e32 v247, v247, v218
	v_mul_f32_e32 v248, v248, v218
	v_mul_f32_e32 v249, v249, v218
	v_fma_f32 v0, v246, v32, v144
	v_fma_f32 v1, v247, v33, v145
	v_fma_f32 v2, v248, v34, v146
	v_fma_f32 v3, v249, v35, v147
	v_lshlrev_b32_e32 v246, 16, v168
	v_and_b32_e32 v247, 0xffff0000, v168
	v_lshlrev_b32_e32 v248, 16, v169
	v_and_b32_e32 v249, 0xffff0000, v169
	v_mul_f32_e32 v246, v246, v218
	v_mul_f32_e32 v247, v247, v218
	v_mul_f32_e32 v248, v248, v218
	v_mul_f32_e32 v249, v249, v218
	v_fma_f32 v4, v246, v36, v148
	v_fma_f32 v5, v247, v37, v149
	v_fma_f32 v6, v248, v38, v150
	v_fma_f32 v7, v249, v39, v151
	v_lshlrev_b32_e32 v246, 16, v170
	v_and_b32_e32 v247, 0xffff0000, v170
	v_lshlrev_b32_e32 v248, 16, v171
	v_and_b32_e32 v249, 0xffff0000, v171
	v_mul_f32_e32 v246, v246, v218
	v_mul_f32_e32 v247, v247, v218
	v_mul_f32_e32 v248, v248, v218
	v_mul_f32_e32 v249, v249, v218
	v_fma_f32 v8, v246, v40, v152
	v_fma_f32 v9, v247, v41, v153
	v_fma_f32 v10, v248, v42, v154
	v_fma_f32 v11, v249, v43, v155
	v_lshlrev_b32_e32 v246, 16, v172
	v_and_b32_e32 v247, 0xffff0000, v172
	v_lshlrev_b32_e32 v248, 16, v173
	v_and_b32_e32 v249, 0xffff0000, v173
	v_mul_f32_e32 v246, v246, v218
	v_mul_f32_e32 v247, v247, v218
	v_mul_f32_e32 v248, v248, v218
	v_mul_f32_e32 v249, v249, v218
	v_fma_f32 v12, v246, v44, v156
	v_fma_f32 v13, v247, v45, v157
	v_fma_f32 v14, v248, v46, v158
	v_fma_f32 v15, v249, v47, v159
	v_lshlrev_b32_e32 v246, 16, v174
	v_and_b32_e32 v247, 0xffff0000, v174
	v_lshlrev_b32_e32 v248, 16, v175
	v_and_b32_e32 v249, 0xffff0000, v175
	v_mul_f32_e32 v246, v246, v218
	v_mul_f32_e32 v247, v247, v218
	v_mul_f32_e32 v248, v248, v218
	v_mul_f32_e32 v249, v249, v218
	v_fma_f32 v16, v246, v48, v182
	v_fma_f32 v17, v247, v49, v183
	v_fma_f32 v18, v248, v50, v184
	v_fma_f32 v19, v249, v51, v185
	v_lshlrev_b32_e32 v246, 16, v176
	v_and_b32_e32 v247, 0xffff0000, v176
	v_lshlrev_b32_e32 v248, 16, v177
	v_and_b32_e32 v249, 0xffff0000, v177
	v_mul_f32_e32 v246, v246, v218
	v_mul_f32_e32 v247, v247, v218
	v_mul_f32_e32 v248, v248, v218
	v_mul_f32_e32 v249, v249, v218
	v_fma_f32 v20, v246, v52, v186
	v_fma_f32 v21, v247, v53, v187
	v_fma_f32 v22, v248, v54, v188
	v_fma_f32 v23, v249, v55, v189
	v_lshlrev_b32_e32 v246, 16, v178
	v_and_b32_e32 v247, 0xffff0000, v178
	v_lshlrev_b32_e32 v248, 16, v179
	v_and_b32_e32 v249, 0xffff0000, v179
	v_mul_f32_e32 v246, v246, v218
	v_mul_f32_e32 v247, v247, v218
	v_mul_f32_e32 v248, v248, v218
	v_mul_f32_e32 v249, v249, v218
	v_fma_f32 v24, v246, v56, v190
	v_fma_f32 v25, v247, v57, v191
	v_fma_f32 v26, v248, v58, v192
	v_fma_f32 v27, v249, v59, v193
	v_lshlrev_b32_e32 v246, 16, v180
	v_and_b32_e32 v247, 0xffff0000, v180
	v_lshlrev_b32_e32 v248, 16, v181
	v_and_b32_e32 v249, 0xffff0000, v181
	v_mul_f32_e32 v246, v246, v218
	v_mul_f32_e32 v247, v247, v218
	v_mul_f32_e32 v248, v248, v218
	v_mul_f32_e32 v249, v249, v218
	v_fma_f32 v28, v246, v60, v194
	v_fma_f32 v29, v247, v61, v195
	v_fma_f32 v30, v248, v62, v196
	v_fma_f32 v31, v249, v63, v197
	v_mov_b32_e32 v250, 0
	v_mov_b32_e32 v251, 0
	v_cvt_pk_bf16_f32 v238, v0, v1
	v_cvt_pk_bf16_f32 v239, v2, v3
	v_fmac_f32_e32 v250, v0, v0
	v_fmac_f32_e32 v251, v1, v1
	v_fmac_f32_e32 v250, v2, v2
	v_fmac_f32_e32 v251, v3, v3
	global_store_dwordx2 v162, v[238:239], s[70:71]
	v_cvt_pk_bf16_f32 v240, v4, v5
	v_cvt_pk_bf16_f32 v241, v6, v7
	v_fmac_f32_e32 v250, v4, v4
	v_fmac_f32_e32 v251, v5, v5
	v_fmac_f32_e32 v250, v6, v6
	v_fmac_f32_e32 v251, v7, v7
	global_store_dwordx2 v162, v[240:241], s[70:71] offset:512
	v_cvt_pk_bf16_f32 v242, v8, v9
	v_cvt_pk_bf16_f32 v243, v10, v11
	v_fmac_f32_e32 v250, v8, v8
	v_fmac_f32_e32 v251, v9, v9
	v_fmac_f32_e32 v250, v10, v10
	v_fmac_f32_e32 v251, v11, v11
	global_store_dwordx2 v162, v[242:243], s[70:71] offset:1024
	v_cvt_pk_bf16_f32 v244, v12, v13
	v_cvt_pk_bf16_f32 v245, v14, v15
	v_fmac_f32_e32 v250, v12, v12
	v_fmac_f32_e32 v251, v13, v13
	v_fmac_f32_e32 v250, v14, v14
	v_fmac_f32_e32 v251, v15, v15
	global_store_dwordx2 v162, v[244:245], s[70:71] offset:1536
	v_cvt_pk_bf16_f32 v238, v16, v17
	v_cvt_pk_bf16_f32 v239, v18, v19
	v_fmac_f32_e32 v250, v16, v16
	v_fmac_f32_e32 v251, v17, v17
	v_fmac_f32_e32 v250, v18, v18
	v_fmac_f32_e32 v251, v19, v19
	global_store_dwordx2 v162, v[238:239], s[70:71] offset:2048
	v_cvt_pk_bf16_f32 v240, v20, v21
	v_cvt_pk_bf16_f32 v241, v22, v23
	v_fmac_f32_e32 v250, v20, v20
	v_fmac_f32_e32 v251, v21, v21
	v_fmac_f32_e32 v250, v22, v22
	v_fmac_f32_e32 v251, v23, v23
	global_store_dwordx2 v162, v[240:241], s[70:71] offset:2560
	v_cvt_pk_bf16_f32 v242, v24, v25
	v_cvt_pk_bf16_f32 v243, v26, v27
	v_fmac_f32_e32 v250, v24, v24
	v_fmac_f32_e32 v251, v25, v25
	v_fmac_f32_e32 v250, v26, v26
	v_fmac_f32_e32 v251, v27, v27
	global_store_dwordx2 v162, v[242:243], s[70:71] offset:3072
	v_cvt_pk_bf16_f32 v244, v28, v29
	v_cvt_pk_bf16_f32 v245, v30, v31
	v_fmac_f32_e32 v250, v28, v28
	v_fmac_f32_e32 v251, v29, v29
	v_fmac_f32_e32 v250, v30, v30
	v_fmac_f32_e32 v251, v31, v31
	global_store_dwordx2 v162, v[244:245], s[70:71] offset:3584
	s_add_u32 s70, s70, 0x8000
	s_addc_u32 s71, s71, 0
	v_add_f32_e32 v250, v250, v251
	s_nop 1
	v_add_f32_dpp v218, v250, v250 quad_perm:[1,0,3,2] row_mask:0xf bank_mask:0xf bound_ctrl:1
	s_nop 1
	v_add_f32_dpp v218, v218, v218 quad_perm:[2,3,0,1] row_mask:0xf bank_mask:0xf bound_ctrl:1
	s_nop 1
	v_add_f32_dpp v218, v218, v218 row_ror:4 row_mask:0xf bank_mask:0xf bound_ctrl:1
	s_nop 1
	v_add_f32_dpp v218, v218, v218 row_ror:8 row_mask:0xf bank_mask:0xf bound_ctrl:1
	s_nop 1
	v_readlane_b32 s8, v218, 0
	v_readlane_b32 s9, v218, 16
	v_readlane_b32 s10, v218, 32
	v_readlane_b32 s11, v218, 48
	s_nop 1
	v_mov_b32_e32 v218, s8
	v_add_f32_e32 v218, s9, v218
	v_mov_b32_e32 v219, s10
	v_add_f32_e32 v219, s11, v219
	v_add_f32_e32 v218, v218, v219
	v_mul_f32_e32 v218, 0x3a000000, v218
	v_add_f32_e32 v218, 0x358637bd, v218
	v_rsq_f32_e32 v218, v218
	s_nop 0
	v_mul_f32_e32 v246, v0, v218
	v_mul_f32_e32 v247, v1, v218
	v_mul_f32_e32 v248, v2, v218
	v_mul_f32_e32 v249, v3, v218
	v_fma_f32 v246, v246, v64, v96
	v_fma_f32 v247, v247, v65, v97
	v_fma_f32 v248, v248, v66, v98
	v_fma_f32 v249, v249, v67, v99
	v_cvt_pk_bf16_f32 v238, v246, v247
	v_cvt_pk_bf16_f32 v239, v248, v249
	global_store_dwordx2 v162, v[238:239], s[72:73]
	v_mul_f32_e32 v246, v4, v218
	v_mul_f32_e32 v247, v5, v218
	v_mul_f32_e32 v248, v6, v218
	v_mul_f32_e32 v249, v7, v218
	v_fma_f32 v246, v246, v68, v100
	v_fma_f32 v247, v247, v69, v101
	v_fma_f32 v248, v248, v70, v102
	v_fma_f32 v249, v249, v71, v103
	v_cvt_pk_bf16_f32 v240, v246, v247
	v_cvt_pk_bf16_f32 v241, v248, v249
	global_store_dwordx2 v162, v[240:241], s[72:73] offset:512
	v_mul_f32_e32 v246, v8, v218
	v_mul_f32_e32 v247, v9, v218
	v_mul_f32_e32 v248, v10, v218
	v_mul_f32_e32 v249, v11, v218
	v_fma_f32 v246, v246, v72, v104
	v_fma_f32 v247, v247, v73, v105
	v_fma_f32 v248, v248, v74, v106
	v_fma_f32 v249, v249, v75, v107
	v_cvt_pk_bf16_f32 v242, v246, v247
	v_cvt_pk_bf16_f32 v243, v248, v249
	global_store_dwordx2 v162, v[242:243], s[72:73] offset:1024
	v_mul_f32_e32 v246, v12, v218
	v_mul_f32_e32 v247, v13, v218
	v_mul_f32_e32 v248, v14, v218
	v_mul_f32_e32 v249, v15, v218
	v_fma_f32 v246, v246, v76, v108
	v_fma_f32 v247, v247, v77, v109
	v_fma_f32 v248, v248, v78, v110
	v_fma_f32 v249, v249, v79, v111
	v_cvt_pk_bf16_f32 v244, v246, v247
	v_cvt_pk_bf16_f32 v245, v248, v249
	global_store_dwordx2 v162, v[244:245], s[72:73] offset:1536
	v_mul_f32_e32 v246, v16, v218
	v_mul_f32_e32 v247, v17, v218
	v_mul_f32_e32 v248, v18, v218
	v_mul_f32_e32 v249, v19, v218
	v_fma_f32 v246, v246, v80, v112
	v_fma_f32 v247, v247, v81, v113
	v_fma_f32 v248, v248, v82, v114
	v_fma_f32 v249, v249, v83, v115
	v_cvt_pk_bf16_f32 v238, v246, v247
	v_cvt_pk_bf16_f32 v239, v248, v249
	global_store_dwordx2 v162, v[238:239], s[72:73] offset:2048
	v_mul_f32_e32 v246, v20, v218
	v_mul_f32_e32 v247, v21, v218
	v_mul_f32_e32 v248, v22, v218
	v_mul_f32_e32 v249, v23, v218
	v_fma_f32 v246, v246, v84, v116
	v_fma_f32 v247, v247, v85, v117
	v_fma_f32 v248, v248, v86, v118
	v_fma_f32 v249, v249, v87, v119
	v_cvt_pk_bf16_f32 v240, v246, v247
	v_cvt_pk_bf16_f32 v241, v248, v249
	global_store_dwordx2 v162, v[240:241], s[72:73] offset:2560
	v_mul_f32_e32 v246, v24, v218
	v_mul_f32_e32 v247, v25, v218
	v_mul_f32_e32 v248, v26, v218
	v_mul_f32_e32 v249, v27, v218
	v_fma_f32 v246, v246, v88, v120
	v_fma_f32 v247, v247, v89, v121
	v_fma_f32 v248, v248, v90, v122
	v_fma_f32 v249, v249, v91, v123
	v_cvt_pk_bf16_f32 v242, v246, v247
	v_cvt_pk_bf16_f32 v243, v248, v249
	global_store_dwordx2 v162, v[242:243], s[72:73] offset:3072
	v_mul_f32_e32 v246, v28, v218
	v_mul_f32_e32 v247, v29, v218
	v_mul_f32_e32 v248, v30, v218
	v_mul_f32_e32 v249, v31, v218
	v_fma_f32 v246, v246, v92, v124
	v_fma_f32 v247, v247, v93, v125
	v_fma_f32 v248, v248, v94, v126
	v_fma_f32 v249, v249, v95, v127
	v_cvt_pk_bf16_f32 v244, v246, v247
	v_cvt_pk_bf16_f32 v245, v248, v249
	global_store_dwordx2 v162, v[244:245], s[72:73] offset:3584
	s_add_u32 s72, s72, 0x8000
	s_addc_u32 s73, s73, 0
	s_branch .Lmp_done

.Lmp_V3_loop:
	s_waitcnt vmcnt(24)
	v_mov_b32_e32 v250, 0
	v_mov_b32_e32 v251, 0
	v_lshlrev_b32_e32 v246, 16, v128
	v_and_b32_e32 v247, 0xffff0000, v128
	v_lshlrev_b32_e32 v248, 16, v129
	v_and_b32_e32 v249, 0xffff0000, v129
	v_fmac_f32_e32 v250, v246, v246
	v_fmac_f32_e32 v251, v247, v247
	v_fmac_f32_e32 v250, v248, v248
	v_fmac_f32_e32 v251, v249, v249
	v_lshlrev_b32_e32 v246, 16, v130
	v_and_b32_e32 v247, 0xffff0000, v130
	v_lshlrev_b32_e32 v248, 16, v131
	v_and_b32_e32 v249, 0xffff0000, v131
	v_fmac_f32_e32 v250, v246, v246
	v_fmac_f32_e32 v251, v247, v247
	v_fmac_f32_e32 v250, v248, v248
	v_fmac_f32_e32 v251, v249, v249
	v_lshlrev_b32_e32 v246, 16, v132
	v_and_b32_e32 v247, 0xffff0000, v132
	v_lshlrev_b32_e32 v248, 16, v133
	v_and_b32_e32 v249, 0xffff0000, v133
	v_fmac_f32_e32 v250, v246, v246
	v_fmac_f32_e32 v251, v247, v247
	v_fmac_f32_e32 v250, v248, v248
	v_fmac_f32_e32 v251, v249, v249
	v_lshlrev_b32_e32 v246, 16, v134
	v_and_b32_e32 v247, 0xffff0000, v134
	v_lshlrev_b32_e32 v248, 16, v135
	v_and_b32_e32 v249, 0xffff0000, v135
	v_fmac_f32_e32 v250, v246, v246
	v_fmac_f32_e32 v251, v247, v247
	v_fmac_f32_e32 v250, v248, v248
	v_fmac_f32_e32 v251, v249, v249
	v_lshlrev_b32_e32 v246, 16, v136
	v_and_b32_e32 v247, 0xffff0000, v136
	v_lshlrev_b32_e32 v248, 16, v137
	v_and_b32_e32 v249, 0xffff0000, v137
	v_fmac_f32_e32 v250, v246, v246
	v_fmac_f32_e32 v251, v247, v247
	v_fmac_f32_e32 v250, v248, v248
	v_fmac_f32_e32 v251, v249, v249
	v_lshlrev_b32_e32 v246, 16, v138
	v_and_b32_e32 v247, 0xffff0000, v138
	v_lshlrev_b32_e32 v248, 16, v139
	v_and_b32_e32 v249, 0xffff0000, v139
	v_fmac_f32_e32 v250, v246, v246
	v_fmac_f32_e32 v251, v247, v247
	v_fmac_f32_e32 v250, v248, v248
	v_fmac_f32_e32 v251, v249, v249
	v_lshlrev_b32_e32 v246, 16, v140
	v_and_b32_e32 v247, 0xffff0000, v140
	v_lshlrev_b32_e32 v248, 16, v141
	v_and_b32_e32 v249, 0xffff0000, v141
	v_fmac_f32_e32 v250, v246, v246
	v_fmac_f32_e32 v251, v247, v247
	v_fmac_f32_e32 v250, v248, v248
	v_fmac_f32_e32 v251, v249, v249
	v_lshlrev_b32_e32 v246, 16, v142
	v_and_b32_e32 v247, 0xffff0000, v142
	v_lshlrev_b32_e32 v248, 16, v143
	v_and_b32_e32 v249, 0xffff0000, v143
	v_fmac_f32_e32 v250, v246, v246
	v_fmac_f32_e32 v251, v247, v247
	v_fmac_f32_e32 v250, v248, v248
	v_fmac_f32_e32 v251, v249, v249
	v_add_f32_e32 v250, v250, v251
	s_nop 1
	v_add_f32_dpp v218, v250, v250 quad_perm:[1,0,3,2] row_mask:0xf bank_mask:0xf bound_ctrl:1
	s_nop 1
	v_add_f32_dpp v218, v218, v218 quad_perm:[2,3,0,1] row_mask:0xf bank_mask:0xf bound_ctrl:1
	s_nop 1
	v_add_f32_dpp v218, v218, v218 row_ror:4 row_mask:0xf bank_mask:0xf bound_ctrl:1
	s_nop 1
	v_add_f32_dpp v218, v218, v218 row_ror:8 row_mask:0xf bank_mask:0xf bound_ctrl:1
	s_nop 1
	v_readlane_b32 s8, v218, 0
	v_readlane_b32 s9, v218, 16
	v_readlane_b32 s10, v218, 32
	v_readlane_b32 s11, v218, 48
	s_nop 1
	v_mov_b32_e32 v218, s8
	v_add_f32_e32 v218, s9, v218
	v_mov_b32_e32 v219, s10
	v_add_f32_e32 v219, s11, v219
	v_add_f32_e32 v218, v218, v219
	v_mul_f32_e32 v218, 0x3a000000, v218
	v_add_f32_e32 v218, 0x358637bd, v218
	v_rsq_f32_e32 v218, v218
	s_nop 0
	v_lshlrev_b32_e32 v246, 16, v128
	v_and_b32_e32 v247, 0xffff0000, v128
	v_lshlrev_b32_e32 v248, 16, v129
	v_and_b32_e32 v249, 0xffff0000, v129
	v_mul_f32_e32 v246, v246, v218
	v_mul_f32_e32 v247, v247, v218
	v_mul_f32_e32 v248, v248, v218
	v_mul_f32_e32 v249, v249, v218
	v_lshlrev_b32_e32 v0, 16, v144
	v_and_b32_e32 v1, 0xffff0000, v144
	v_lshlrev_b32_e32 v2, 16, v145
	v_and_b32_e32 v3, 0xffff0000, v145
	v_fmac_f32_e32 v0, v246, v32
	v_fmac_f32_e32 v1, v247, v33
	v_fmac_f32_e32 v2, v248, v34
	v_fmac_f32_e32 v3, v249, v35
	v_lshlrev_b32_e32 v246, 16, v130
	v_and_b32_e32 v247, 0xffff0000, v130
	v_lshlrev_b32_e32 v248, 16, v131
	v_and_b32_e32 v249, 0xffff0000, v131
	v_mul_f32_e32 v246, v246, v218
	v_mul_f32_e32 v247, v247, v218
	v_mul_f32_e32 v248, v248, v218
	v_mul_f32_e32 v249, v249, v218
	v_lshlrev_b32_e32 v4, 16, v146
	v_and_b32_e32 v5, 0xffff0000, v146
	v_lshlrev_b32_e32 v6, 16, v147
	v_and_b32_e32 v7, 0xffff0000, v147
	v_fmac_f32_e32 v4, v246, v36
	v_fmac_f32_e32 v5, v247, v37
	v_fmac_f32_e32 v6, v248, v38
	v_fmac_f32_e32 v7, v249, v39
	v_lshlrev_b32_e32 v246, 16, v132
	v_and_b32_e32 v247, 0xffff0000, v132
	v_lshlrev_b32_e32 v248, 16, v133
	v_and_b32_e32 v249, 0xffff0000, v133
	v_mul_f32_e32 v246, v246, v218
	v_mul_f32_e32 v247, v247, v218
	v_mul_f32_e32 v248, v248, v218
	v_mul_f32_e32 v249, v249, v218
	v_lshlrev_b32_e32 v8, 16, v148
	v_and_b32_e32 v9, 0xffff0000, v148
	v_lshlrev_b32_e32 v10, 16, v149
	v_and_b32_e32 v11, 0xffff0000, v149
	v_fmac_f32_e32 v8, v246, v40
	v_fmac_f32_e32 v9, v247, v41
	v_fmac_f32_e32 v10, v248, v42
	v_fmac_f32_e32 v11, v249, v43
	v_lshlrev_b32_e32 v246, 16, v134
	v_and_b32_e32 v247, 0xffff0000, v134
	v_lshlrev_b32_e32 v248, 16, v135
	v_and_b32_e32 v249, 0xffff0000, v135
	v_mul_f32_e32 v246, v246, v218
	v_mul_f32_e32 v247, v247, v218
	v_mul_f32_e32 v248, v248, v218
	v_mul_f32_e32 v249, v249, v218
	v_lshlrev_b32_e32 v12, 16, v150
	v_and_b32_e32 v13, 0xffff0000, v150
	v_lshlrev_b32_e32 v14, 16, v151
	v_and_b32_e32 v15, 0xffff0000, v151
	v_fmac_f32_e32 v12, v246, v44
	v_fmac_f32_e32 v13, v247, v45
	v_fmac_f32_e32 v14, v248, v46
	v_fmac_f32_e32 v15, v249, v47
	v_lshlrev_b32_e32 v246, 16, v136
	v_and_b32_e32 v247, 0xffff0000, v136
	v_lshlrev_b32_e32 v248, 16, v137
	v_and_b32_e32 v249, 0xffff0000, v137
	v_mul_f32_e32 v246, v246, v218
	v_mul_f32_e32 v247, v247, v218
	v_mul_f32_e32 v248, v248, v218
	v_mul_f32_e32 v249, v249, v218
	v_lshlrev_b32_e32 v16, 16, v152
	v_and_b32_e32 v17, 0xffff0000, v152
	v_lshlrev_b32_e32 v18, 16, v153
	v_and_b32_e32 v19, 0xffff0000, v153
	v_fmac_f32_e32 v16, v246, v48
	v_fmac_f32_e32 v17, v247, v49
	v_fmac_f32_e32 v18, v248, v50
	v_fmac_f32_e32 v19, v249, v51
	v_lshlrev_b32_e32 v246, 16, v138
	v_and_b32_e32 v247, 0xffff0000, v138
	v_lshlrev_b32_e32 v248, 16, v139
	v_and_b32_e32 v249, 0xffff0000, v139
	v_mul_f32_e32 v246, v246, v218
	v_mul_f32_e32 v247, v247, v218
	v_mul_f32_e32 v248, v248, v218
	v_mul_f32_e32 v249, v249, v218
	v_lshlrev_b32_e32 v20, 16, v154
	v_and_b32_e32 v21, 0xffff0000, v154
	v_lshlrev_b32_e32 v22, 16, v155
	v_and_b32_e32 v23, 0xffff0000, v155
	v_fmac_f32_e32 v20, v246, v52
	v_fmac_f32_e32 v21, v247, v53
	v_fmac_f32_e32 v22, v248, v54
	v_fmac_f32_e32 v23, v249, v55
	v_lshlrev_b32_e32 v246, 16, v140
	v_and_b32_e32 v247, 0xffff0000, v140
	v_lshlrev_b32_e32 v248, 16, v141
	v_and_b32_e32 v249, 0xffff0000, v141
	v_mul_f32_e32 v246, v246, v218
	v_mul_f32_e32 v247, v247, v218
	v_mul_f32_e32 v248, v248, v218
	v_mul_f32_e32 v249, v249, v218
	v_lshlrev_b32_e32 v24, 16, v156
	v_and_b32_e32 v25, 0xffff0000, v156
	v_lshlrev_b32_e32 v26, 16, v157
	v_and_b32_e32 v27, 0xffff0000, v157
	v_fmac_f32_e32 v24, v246, v56
	v_fmac_f32_e32 v25, v247, v57
	v_fmac_f32_e32 v26, v248, v58
	v_fmac_f32_e32 v27, v249, v59
	v_lshlrev_b32_e32 v246, 16, v142
	v_and_b32_e32 v247, 0xffff0000, v142
	v_lshlrev_b32_e32 v248, 16, v143
	v_and_b32_e32 v249, 0xffff0000, v143
	v_mul_f32_e32 v246, v246, v218
	v_mul_f32_e32 v247, v247, v218
	v_mul_f32_e32 v248, v248, v218
	v_mul_f32_e32 v249, v249, v218
	v_lshlrev_b32_e32 v28, 16, v158
	v_and_b32_e32 v29, 0xffff0000, v158
	v_lshlrev_b32_e32 v30, 16, v159
	v_and_b32_e32 v31, 0xffff0000, v159
	v_fmac_f32_e32 v28, v246, v60
	v_fmac_f32_e32 v29, v247, v61
	v_fmac_f32_e32 v30, v248, v62
	v_fmac_f32_e32 v31, v249, v63
	global_load_dwordx2 v[128:129], v162, s[56:57]
	global_load_dwordx2 v[130:131], v162, s[56:57] offset:512
	global_load_dwordx2 v[132:133], v162, s[56:57] offset:1024
	global_load_dwordx2 v[134:135], v162, s[56:57] offset:1536
	global_load_dwordx2 v[136:137], v162, s[56:57] offset:2048
	global_load_dwordx2 v[138:139], v162, s[56:57] offset:2560
	global_load_dwordx2 v[140:141], v162, s[56:57] offset:3072
	global_load_dwordx2 v[142:143], v162, s[56:57] offset:3584
	global_load_dwordx2 v[144:145], v162, s[58:59]
	global_load_dwordx2 v[146:147], v162, s[58:59] offset:512
	global_load_dwordx2 v[148:149], v162, s[58:59] offset:1024
	global_load_dwordx2 v[150:151], v162, s[58:59] offset:1536
	global_load_dwordx2 v[152:153], v162, s[58:59] offset:2048
	global_load_dwordx2 v[154:155], v162, s[58:59] offset:2560
	global_load_dwordx2 v[156:157], v162, s[58:59] offset:3072
	global_load_dwordx2 v[158:159], v162, s[58:59] offset:3584
	s_add_u32 s58, s58, 0x8000
	s_addc_u32 s59, s59, 0
	s_add_u32 s56, s56, 0x8000
	s_addc_u32 s57, s57, 0
	global_store_dwordx4 v163, v[0:3], s[70:71]
	global_store_dwordx4 v163, v[4:7], s[70:71] offset:1024
	global_store_dwordx4 v163, v[8:11], s[70:71] offset:2048
	global_store_dwordx4 v163, v[12:15], s[70:71] offset:3072
	s_add_u32 s10, s70, 0x1000
	s_addc_u32 s11, s71, 0
	global_store_dwordx4 v163, v[16:19], s[10:11]
	global_store_dwordx4 v163, v[20:23], s[10:11] offset:1024
	global_store_dwordx4 v163, v[24:27], s[10:11] offset:2048
	global_store_dwordx4 v163, v[28:31], s[10:11] offset:3072
	s_add_u32 s70, s70, 0x10000
	s_addc_u32 s71, s71, 0
	s_waitcnt vmcnt(24)
	v_mov_b32_e32 v250, 0
	v_mov_b32_e32 v251, 0
	v_lshlrev_b32_e32 v246, 16, v166
	v_and_b32_e32 v247, 0xffff0000, v166
	v_lshlrev_b32_e32 v248, 16, v167
	v_and_b32_e32 v249, 0xffff0000, v167
	v_fmac_f32_e32 v250, v246, v246
	v_fmac_f32_e32 v251, v247, v247
	v_fmac_f32_e32 v250, v248, v248
	v_fmac_f32_e32 v251, v249, v249
	v_lshlrev_b32_e32 v246, 16, v168
	v_and_b32_e32 v247, 0xffff0000, v168
	v_lshlrev_b32_e32 v248, 16, v169
	v_and_b32_e32 v249, 0xffff0000, v169
	v_fmac_f32_e32 v250, v246, v246
	v_fmac_f32_e32 v251, v247, v247
	v_fmac_f32_e32 v250, v248, v248
	v_fmac_f32_e32 v251, v249, v249
	v_lshlrev_b32_e32 v246, 16, v170
	v_and_b32_e32 v247, 0xffff0000, v170
	v_lshlrev_b32_e32 v248, 16, v171
	v_and_b32_e32 v249, 0xffff0000, v171
	v_fmac_f32_e32 v250, v246, v246
	v_fmac_f32_e32 v251, v247, v247
	v_fmac_f32_e32 v250, v248, v248
	v_fmac_f32_e32 v251, v249, v249
	v_lshlrev_b32_e32 v246, 16, v172
	v_and_b32_e32 v247, 0xffff0000, v172
	v_lshlrev_b32_e32 v248, 16, v173
	v_and_b32_e32 v249, 0xffff0000, v173
	v_fmac_f32_e32 v250, v246, v246
	v_fmac_f32_e32 v251, v247, v247
	v_fmac_f32_e32 v250, v248, v248
	v_fmac_f32_e32 v251, v249, v249
	v_lshlrev_b32_e32 v246, 16, v174
	v_and_b32_e32 v247, 0xffff0000, v174
	v_lshlrev_b32_e32 v248, 16, v175
	v_and_b32_e32 v249, 0xffff0000, v175
	v_fmac_f32_e32 v250, v246, v246
	v_fmac_f32_e32 v251, v247, v247
	v_fmac_f32_e32 v250, v248, v248
	v_fmac_f32_e32 v251, v249, v249
	v_lshlrev_b32_e32 v246, 16, v176
	v_and_b32_e32 v247, 0xffff0000, v176
	v_lshlrev_b32_e32 v248, 16, v177
	v_and_b32_e32 v249, 0xffff0000, v177
	v_fmac_f32_e32 v250, v246, v246
	v_fmac_f32_e32 v251, v247, v247
	v_fmac_f32_e32 v250, v248, v248
	v_fmac_f32_e32 v251, v249, v249
	v_lshlrev_b32_e32 v246, 16, v178
	v_and_b32_e32 v247, 0xffff0000, v178
	v_lshlrev_b32_e32 v248, 16, v179
	v_and_b32_e32 v249, 0xffff0000, v179
	v_fmac_f32_e32 v250, v246, v246
	v_fmac_f32_e32 v251, v247, v247
	v_fmac_f32_e32 v250, v248, v248
	v_fmac_f32_e32 v251, v249, v249
	v_lshlrev_b32_e32 v246, 16, v180
	v_and_b32_e32 v247, 0xffff0000, v180
	v_lshlrev_b32_e32 v248, 16, v181
	v_and_b32_e32 v249, 0xffff0000, v181
	v_fmac_f32_e32 v250, v246, v246
	v_fmac_f32_e32 v251, v247, v247
	v_fmac_f32_e32 v250, v248, v248
	v_fmac_f32_e32 v251, v249, v249
	v_add_f32_e32 v250, v250, v251
	s_nop 1
	v_add_f32_dpp v218, v250, v250 quad_perm:[1,0,3,2] row_mask:0xf bank_mask:0xf bound_ctrl:1
	s_nop 1
	v_add_f32_dpp v218, v218, v218 quad_perm:[2,3,0,1] row_mask:0xf bank_mask:0xf bound_ctrl:1
	s_nop 1
	v_add_f32_dpp v218, v218, v218 row_ror:4 row_mask:0xf bank_mask:0xf bound_ctrl:1
	s_nop 1
	v_add_f32_dpp v218, v218, v218 row_ror:8 row_mask:0xf bank_mask:0xf bound_ctrl:1
	s_nop 1
	v_readlane_b32 s8, v218, 0
	v_readlane_b32 s9, v218, 16
	v_readlane_b32 s10, v218, 32
	v_readlane_b32 s11, v218, 48
	s_nop 1
	v_mov_b32_e32 v218, s8
	v_add_f32_e32 v218, s9, v218
	v_mov_b32_e32 v219, s10
	v_add_f32_e32 v219, s11, v219
	v_add_f32_e32 v218, v218, v219
	v_mul_f32_e32 v218, 0x3a000000, v218
	v_add_f32_e32 v218, 0x358637bd, v218
	v_rsq_f32_e32 v218, v218
	s_nop 0
	v_lshlrev_b32_e32 v246, 16, v166
	v_and_b32_e32 v247, 0xffff0000, v166
	v_lshlrev_b32_e32 v248, 16, v167
	v_and_b32_e32 v249, 0xffff0000, v167
	v_mul_f32_e32 v246, v246, v218
	v_mul_f32_e32 v247, v247, v218
	v_mul_f32_e32 v248, v248, v218
	v_mul_f32_e32 v249, v249, v218
	v_lshlrev_b32_e32 v0, 16, v182
	v_and_b32_e32 v1, 0xffff0000, v182
	v_lshlrev_b32_e32 v2, 16, v183
	v_and_b32_e32 v3, 0xffff0000, v183
	v_fmac_f32_e32 v0, v246, v32
	v_fmac_f32_e32 v1, v247, v33
	v_fmac_f32_e32 v2, v248, v34
	v_fmac_f32_e32 v3, v249, v35
	v_lshlrev_b32_e32 v246, 16, v168
	v_and_b32_e32 v247, 0xffff0000, v168
	v_lshlrev_b32_e32 v248, 16, v169
	v_and_b32_e32 v249, 0xffff0000, v169
	v_mul_f32_e32 v246, v246, v218
	v_mul_f32_e32 v247, v247, v218
	v_mul_f32_e32 v248, v248, v218
	v_mul_f32_e32 v249, v249, v218
	v_lshlrev_b32_e32 v4, 16, v184
	v_and_b32_e32 v5, 0xffff0000, v184
	v_lshlrev_b32_e32 v6, 16, v185
	v_and_b32_e32 v7, 0xffff0000, v185
	v_fmac_f32_e32 v4, v246, v36
	v_fmac_f32_e32 v5, v247, v37
	v_fmac_f32_e32 v6, v248, v38
	v_fmac_f32_e32 v7, v249, v39
	v_lshlrev_b32_e32 v246, 16, v170
	v_and_b32_e32 v247, 0xffff0000, v170
	v_lshlrev_b32_e32 v248, 16, v171
	v_and_b32_e32 v249, 0xffff0000, v171
	v_mul_f32_e32 v246, v246, v218
	v_mul_f32_e32 v247, v247, v218
	v_mul_f32_e32 v248, v248, v218
	v_mul_f32_e32 v249, v249, v218
	v_lshlrev_b32_e32 v8, 16, v186
	v_and_b32_e32 v9, 0xffff0000, v186
	v_lshlrev_b32_e32 v10, 16, v187
	v_and_b32_e32 v11, 0xffff0000, v187
	v_fmac_f32_e32 v8, v246, v40
	v_fmac_f32_e32 v9, v247, v41
	v_fmac_f32_e32 v10, v248, v42
	v_fmac_f32_e32 v11, v249, v43
	v_lshlrev_b32_e32 v246, 16, v172
	v_and_b32_e32 v247, 0xffff0000, v172
	v_lshlrev_b32_e32 v248, 16, v173
	v_and_b32_e32 v249, 0xffff0000, v173
	v_mul_f32_e32 v246, v246, v218
	v_mul_f32_e32 v247, v247, v218
	v_mul_f32_e32 v248, v248, v218
	v_mul_f32_e32 v249, v249, v218
	v_lshlrev_b32_e32 v12, 16, v188
	v_and_b32_e32 v13, 0xffff0000, v188
	v_lshlrev_b32_e32 v14, 16, v189
	v_and_b32_e32 v15, 0xffff0000, v189
	v_fmac_f32_e32 v12, v246, v44
	v_fmac_f32_e32 v13, v247, v45
	v_fmac_f32_e32 v14, v248, v46
	v_fmac_f32_e32 v15, v249, v47
	v_lshlrev_b32_e32 v246, 16, v174
	v_and_b32_e32 v247, 0xffff0000, v174
	v_lshlrev_b32_e32 v248, 16, v175
	v_and_b32_e32 v249, 0xffff0000, v175
	v_mul_f32_e32 v246, v246, v218
	v_mul_f32_e32 v247, v247, v218
	v_mul_f32_e32 v248, v248, v218
	v_mul_f32_e32 v249, v249, v218
	v_lshlrev_b32_e32 v16, 16, v190
	v_and_b32_e32 v17, 0xffff0000, v190
	v_lshlrev_b32_e32 v18, 16, v191
	v_and_b32_e32 v19, 0xffff0000, v191
	v_fmac_f32_e32 v16, v246, v48
	v_fmac_f32_e32 v17, v247, v49
	v_fmac_f32_e32 v18, v248, v50
	v_fmac_f32_e32 v19, v249, v51
	v_lshlrev_b32_e32 v246, 16, v176
	v_and_b32_e32 v247, 0xffff0000, v176
	v_lshlrev_b32_e32 v248, 16, v177
	v_and_b32_e32 v249, 0xffff0000, v177
	v_mul_f32_e32 v246, v246, v218
	v_mul_f32_e32 v247, v247, v218
	v_mul_f32_e32 v248, v248, v218
	v_mul_f32_e32 v249, v249, v218
	v_lshlrev_b32_e32 v20, 16, v192
	v_and_b32_e32 v21, 0xffff0000, v192
	v_lshlrev_b32_e32 v22, 16, v193
	v_and_b32_e32 v23, 0xffff0000, v193
	v_fmac_f32_e32 v20, v246, v52
	v_fmac_f32_e32 v21, v247, v53
	v_fmac_f32_e32 v22, v248, v54
	v_fmac_f32_e32 v23, v249, v55
	v_lshlrev_b32_e32 v246, 16, v178
	v_and_b32_e32 v247, 0xffff0000, v178
	v_lshlrev_b32_e32 v248, 16, v179
	v_and_b32_e32 v249, 0xffff0000, v179
	v_mul_f32_e32 v246, v246, v218
	v_mul_f32_e32 v247, v247, v218
	v_mul_f32_e32 v248, v248, v218
	v_mul_f32_e32 v249, v249, v218
	v_lshlrev_b32_e32 v24, 16, v194
	v_and_b32_e32 v25, 0xffff0000, v194
	v_lshlrev_b32_e32 v26, 16, v195
	v_and_b32_e32 v27, 0xffff0000, v195
	v_fmac_f32_e32 v24, v246, v56
	v_fmac_f32_e32 v25, v247, v57
	v_fmac_f32_e32 v26, v248, v58
	v_fmac_f32_e32 v27, v249, v59
	v_lshlrev_b32_e32 v246, 16, v180
	v_and_b32_e32 v247, 0xffff0000, v180
	v_lshlrev_b32_e32 v248, 16, v181
	v_and_b32_e32 v249, 0xffff0000, v181
	v_mul_f32_e32 v246, v246, v218
	v_mul_f32_e32 v247, v247, v218
	v_mul_f32_e32 v248, v248, v218
	v_mul_f32_e32 v249, v249, v218
	v_lshlrev_b32_e32 v28, 16, v196
	v_and_b32_e32 v29, 0xffff0000, v196
	v_lshlrev_b32_e32 v30, 16, v197
	v_and_b32_e32 v31, 0xffff0000, v197
	v_fmac_f32_e32 v28, v246, v60
	v_fmac_f32_e32 v29, v247, v61
	v_fmac_f32_e32 v30, v248, v62
	v_fmac_f32_e32 v31, v249, v63
	global_load_dwordx2 v[166:167], v162, s[56:57]
	global_load_dwordx2 v[168:169], v162, s[56:57] offset:512
	global_load_dwordx2 v[170:171], v162, s[56:57] offset:1024
	global_load_dwordx2 v[172:173], v162, s[56:57] offset:1536
	global_load_dwordx2 v[174:175], v162, s[56:57] offset:2048
	global_load_dwordx2 v[176:177], v162, s[56:57] offset:2560
	global_load_dwordx2 v[178:179], v162, s[56:57] offset:3072
	global_load_dwordx2 v[180:181], v162, s[56:57] offset:3584
	global_load_dwordx2 v[182:183], v162, s[58:59]
	global_load_dwordx2 v[184:185], v162, s[58:59] offset:512
	global_load_dwordx2 v[186:187], v162, s[58:59] offset:1024
	global_load_dwordx2 v[188:189], v162, s[58:59] offset:1536
	global_load_dwordx2 v[190:191], v162, s[58:59] offset:2048
	global_load_dwordx2 v[192:193], v162, s[58:59] offset:2560
	global_load_dwordx2 v[194:195], v162, s[58:59] offset:3072
	global_load_dwordx2 v[196:197], v162, s[58:59] offset:3584
	s_add_u32 s58, s58, 0x8000
	s_addc_u32 s59, s59, 0
	s_add_u32 s56, s56, 0x8000
	s_addc_u32 s57, s57, 0
	global_store_dwordx4 v163, v[0:3], s[70:71]
	global_store_dwordx4 v163, v[4:7], s[70:71] offset:1024
	global_store_dwordx4 v163, v[8:11], s[70:71] offset:2048
	global_store_dwordx4 v163, v[12:15], s[70:71] offset:3072
	s_add_u32 s10, s70, 0x1000
	s_addc_u32 s11, s71, 0
	global_store_dwordx4 v163, v[16:19], s[10:11]
	global_store_dwordx4 v163, v[20:23], s[10:11] offset:1024
	global_store_dwordx4 v163, v[24:27], s[10:11] offset:2048
	global_store_dwordx4 v163, v[28:31], s[10:11] offset:3072
	s_add_u32 s70, s70, 0x10000
	s_addc_u32 s71, s71, 0
	s_add_u32 s76, s76, 1
	s_cmp_lt_u32 s76, 7
	s_cbranch_scc1 .Lmp_V3_loop
	s_waitcnt vmcnt(24)
	v_mov_b32_e32 v250, 0
	v_mov_b32_e32 v251, 0
	v_lshlrev_b32_e32 v246, 16, v128
	v_and_b32_e32 v247, 0xffff0000, v128
	v_lshlrev_b32_e32 v248, 16, v129
	v_and_b32_e32 v249, 0xffff0000, v129
	v_fmac_f32_e32 v250, v246, v246
	v_fmac_f32_e32 v251, v247, v247
	v_fmac_f32_e32 v250, v248, v248
	v_fmac_f32_e32 v251, v249, v249
	v_lshlrev_b32_e32 v246, 16, v130
	v_and_b32_e32 v247, 0xffff0000, v130
	v_lshlrev_b32_e32 v248, 16, v131
	v_and_b32_e32 v249, 0xffff0000, v131
	v_fmac_f32_e32 v250, v246, v246
	v_fmac_f32_e32 v251, v247, v247
	v_fmac_f32_e32 v250, v248, v248
	v_fmac_f32_e32 v251, v249, v249
	v_lshlrev_b32_e32 v246, 16, v132
	v_and_b32_e32 v247, 0xffff0000, v132
	v_lshlrev_b32_e32 v248, 16, v133
	v_and_b32_e32 v249, 0xffff0000, v133
	v_fmac_f32_e32 v250, v246, v246
	v_fmac_f32_e32 v251, v247, v247
	v_fmac_f32_e32 v250, v248, v248
	v_fmac_f32_e32 v251, v249, v249
	v_lshlrev_b32_e32 v246, 16, v134
	v_and_b32_e32 v247, 0xffff0000, v134
	v_lshlrev_b32_e32 v248, 16, v135
	v_and_b32_e32 v249, 0xffff0000, v135
	v_fmac_f32_e32 v250, v246, v246
	v_fmac_f32_e32 v251, v247, v247
	v_fmac_f32_e32 v250, v248, v248
	v_fmac_f32_e32 v251, v249, v249
	v_lshlrev_b32_e32 v246, 16, v136
	v_and_b32_e32 v247, 0xffff0000, v136
	v_lshlrev_b32_e32 v248, 16, v137
	v_and_b32_e32 v249, 0xffff0000, v137
	v_fmac_f32_e32 v250, v246, v246
	v_fmac_f32_e32 v251, v247, v247
	v_fmac_f32_e32 v250, v248, v248
	v_fmac_f32_e32 v251, v249, v249
	v_lshlrev_b32_e32 v246, 16, v138
	v_and_b32_e32 v247, 0xffff0000, v138
	v_lshlrev_b32_e32 v248, 16, v139
	v_and_b32_e32 v249, 0xffff0000, v139
	v_fmac_f32_e32 v250, v246, v246
	v_fmac_f32_e32 v251, v247, v247
	v_fmac_f32_e32 v250, v248, v248
	v_fmac_f32_e32 v251, v249, v249
	v_lshlrev_b32_e32 v246, 16, v140
	v_and_b32_e32 v247, 0xffff0000, v140
	v_lshlrev_b32_e32 v248, 16, v141
	v_and_b32_e32 v249, 0xffff0000, v141
	v_fmac_f32_e32 v250, v246, v246
	v_fmac_f32_e32 v251, v247, v247
	v_fmac_f32_e32 v250, v248, v248
	v_fmac_f32_e32 v251, v249, v249
	v_lshlrev_b32_e32 v246, 16, v142
	v_and_b32_e32 v247, 0xffff0000, v142
	v_lshlrev_b32_e32 v248, 16, v143
	v_and_b32_e32 v249, 0xffff0000, v143
	v_fmac_f32_e32 v250, v246, v246
	v_fmac_f32_e32 v251, v247, v247
	v_fmac_f32_e32 v250, v248, v248
	v_fmac_f32_e32 v251, v249, v249
	v_add_f32_e32 v250, v250, v251
	s_nop 1
	v_add_f32_dpp v218, v250, v250 quad_perm:[1,0,3,2] row_mask:0xf bank_mask:0xf bound_ctrl:1
	s_nop 1
	v_add_f32_dpp v218, v218, v218 quad_perm:[2,3,0,1] row_mask:0xf bank_mask:0xf bound_ctrl:1
	s_nop 1
	v_add_f32_dpp v218, v218, v218 row_ror:4 row_mask:0xf bank_mask:0xf bound_ctrl:1
	s_nop 1
	v_add_f32_dpp v218, v218, v218 row_ror:8 row_mask:0xf bank_mask:0xf bound_ctrl:1
	s_nop 1
	v_readlane_b32 s8, v218, 0
	v_readlane_b32 s9, v218, 16
	v_readlane_b32 s10, v218, 32
	v_readlane_b32 s11, v218, 48
	s_nop 1
	v_mov_b32_e32 v218, s8
	v_add_f32_e32 v218, s9, v218
	v_mov_b32_e32 v219, s10
	v_add_f32_e32 v219, s11, v219
	v_add_f32_e32 v218, v218, v219
	v_mul_f32_e32 v218, 0x3a000000, v218
	v_add_f32_e32 v218, 0x358637bd, v218
	v_rsq_f32_e32 v218, v218
	s_nop 0
	v_lshlrev_b32_e32 v246, 16, v128
	v_and_b32_e32 v247, 0xffff0000, v128
	v_lshlrev_b32_e32 v248, 16, v129
	v_and_b32_e32 v249, 0xffff0000, v129
	v_mul_f32_e32 v246, v246, v218
	v_mul_f32_e32 v247, v247, v218
	v_mul_f32_e32 v248, v248, v218
	v_mul_f32_e32 v249, v249, v218
	v_lshlrev_b32_e32 v0, 16, v144
	v_and_b32_e32 v1, 0xffff0000, v144
	v_lshlrev_b32_e32 v2, 16, v145
	v_and_b32_e32 v3, 0xffff0000, v145
	v_fmac_f32_e32 v0, v246, v32
	v_fmac_f32_e32 v1, v247, v33
	v_fmac_f32_e32 v2, v248, v34
	v_fmac_f32_e32 v3, v249, v35
	v_lshlrev_b32_e32 v246, 16, v130
	v_and_b32_e32 v247, 0xffff0000, v130
	v_lshlrev_b32_e32 v248, 16, v131
	v_and_b32_e32 v249, 0xffff0000, v131
	v_mul_f32_e32 v246, v246, v218
	v_mul_f32_e32 v247, v247, v218
	v_mul_f32_e32 v248, v248, v218
	v_mul_f32_e32 v249, v249, v218
	v_lshlrev_b32_e32 v4, 16, v146
	v_and_b32_e32 v5, 0xffff0000, v146
	v_lshlrev_b32_e32 v6, 16, v147
	v_and_b32_e32 v7, 0xffff0000, v147
	v_fmac_f32_e32 v4, v246, v36
	v_fmac_f32_e32 v5, v247, v37
	v_fmac_f32_e32 v6, v248, v38
	v_fmac_f32_e32 v7, v249, v39
	v_lshlrev_b32_e32 v246, 16, v132
	v_and_b32_e32 v247, 0xffff0000, v132
	v_lshlrev_b32_e32 v248, 16, v133
	v_and_b32_e32 v249, 0xffff0000, v133
	v_mul_f32_e32 v246, v246, v218
	v_mul_f32_e32 v247, v247, v218
	v_mul_f32_e32 v248, v248, v218
	v_mul_f32_e32 v249, v249, v218
	v_lshlrev_b32_e32 v8, 16, v148
	v_and_b32_e32 v9, 0xffff0000, v148
	v_lshlrev_b32_e32 v10, 16, v149
	v_and_b32_e32 v11, 0xffff0000, v149
	v_fmac_f32_e32 v8, v246, v40
	v_fmac_f32_e32 v9, v247, v41
	v_fmac_f32_e32 v10, v248, v42
	v_fmac_f32_e32 v11, v249, v43
	v_lshlrev_b32_e32 v246, 16, v134
	v_and_b32_e32 v247, 0xffff0000, v134
	v_lshlrev_b32_e32 v248, 16, v135
	v_and_b32_e32 v249, 0xffff0000, v135
	v_mul_f32_e32 v246, v246, v218
	v_mul_f32_e32 v247, v247, v218
	v_mul_f32_e32 v248, v248, v218
	v_mul_f32_e32 v249, v249, v218
	v_lshlrev_b32_e32 v12, 16, v150
	v_and_b32_e32 v13, 0xffff0000, v150
	v_lshlrev_b32_e32 v14, 16, v151
	v_and_b32_e32 v15, 0xffff0000, v151
	v_fmac_f32_e32 v12, v246, v44
	v_fmac_f32_e32 v13, v247, v45
	v_fmac_f32_e32 v14, v248, v46
	v_fmac_f32_e32 v15, v249, v47
	v_lshlrev_b32_e32 v246, 16, v136
	v_and_b32_e32 v247, 0xffff0000, v136
	v_lshlrev_b32_e32 v248, 16, v137
	v_and_b32_e32 v249, 0xffff0000, v137
	v_mul_f32_e32 v246, v246, v218
	v_mul_f32_e32 v247, v247, v218
	v_mul_f32_e32 v248, v248, v218
	v_mul_f32_e32 v249, v249, v218
	v_lshlrev_b32_e32 v16, 16, v152
	v_and_b32_e32 v17, 0xffff0000, v152
	v_lshlrev_b32_e32 v18, 16, v153
	v_and_b32_e32 v19, 0xffff0000, v153
	v_fmac_f32_e32 v16, v246, v48
	v_fmac_f32_e32 v17, v247, v49
	v_fmac_f32_e32 v18, v248, v50
	v_fmac_f32_e32 v19, v249, v51
	v_lshlrev_b32_e32 v246, 16, v138
	v_and_b32_e32 v247, 0xffff0000, v138
	v_lshlrev_b32_e32 v248, 16, v139
	v_and_b32_e32 v249, 0xffff0000, v139
	v_mul_f32_e32 v246, v246, v218
	v_mul_f32_e32 v247, v247, v218
	v_mul_f32_e32 v248, v248, v218
	v_mul_f32_e32 v249, v249, v218
	v_lshlrev_b32_e32 v20, 16, v154
	v_and_b32_e32 v21, 0xffff0000, v154
	v_lshlrev_b32_e32 v22, 16, v155
	v_and_b32_e32 v23, 0xffff0000, v155
	v_fmac_f32_e32 v20, v246, v52
	v_fmac_f32_e32 v21, v247, v53
	v_fmac_f32_e32 v22, v248, v54
	v_fmac_f32_e32 v23, v249, v55
	v_lshlrev_b32_e32 v246, 16, v140
	v_and_b32_e32 v247, 0xffff0000, v140
	v_lshlrev_b32_e32 v248, 16, v141
	v_and_b32_e32 v249, 0xffff0000, v141
	v_mul_f32_e32 v246, v246, v218
	v_mul_f32_e32 v247, v247, v218
	v_mul_f32_e32 v248, v248, v218
	v_mul_f32_e32 v249, v249, v218
	v_lshlrev_b32_e32 v24, 16, v156
	v_and_b32_e32 v25, 0xffff0000, v156
	v_lshlrev_b32_e32 v26, 16, v157
	v_and_b32_e32 v27, 0xffff0000, v157
	v_fmac_f32_e32 v24, v246, v56
	v_fmac_f32_e32 v25, v247, v57
	v_fmac_f32_e32 v26, v248, v58
	v_fmac_f32_e32 v27, v249, v59
	v_lshlrev_b32_e32 v246, 16, v142
	v_and_b32_e32 v247, 0xffff0000, v142
	v_lshlrev_b32_e32 v248, 16, v143
	v_and_b32_e32 v249, 0xffff0000, v143
	v_mul_f32_e32 v246, v246, v218
	v_mul_f32_e32 v247, v247, v218
	v_mul_f32_e32 v248, v248, v218
	v_mul_f32_e32 v249, v249, v218
	v_lshlrev_b32_e32 v28, 16, v158
	v_and_b32_e32 v29, 0xffff0000, v158
	v_lshlrev_b32_e32 v30, 16, v159
	v_and_b32_e32 v31, 0xffff0000, v159
	v_fmac_f32_e32 v28, v246, v60
	v_fmac_f32_e32 v29, v247, v61
	v_fmac_f32_e32 v30, v248, v62
	v_fmac_f32_e32 v31, v249, v63
	global_store_dwordx4 v163, v[0:3], s[70:71]
	global_store_dwordx4 v163, v[4:7], s[70:71] offset:1024
	global_store_dwordx4 v163, v[8:11], s[70:71] offset:2048
	global_store_dwordx4 v163, v[12:15], s[70:71] offset:3072
	s_add_u32 s10, s70, 0x1000
	s_addc_u32 s11, s71, 0
	global_store_dwordx4 v163, v[16:19], s[10:11]
	global_store_dwordx4 v163, v[20:23], s[10:11] offset:1024
	global_store_dwordx4 v163, v[24:27], s[10:11] offset:2048
	global_store_dwordx4 v163, v[28:31], s[10:11] offset:3072
	s_add_u32 s70, s70, 0x10000
	s_addc_u32 s71, s71, 0
	s_waitcnt vmcnt(16)
	v_mov_b32_e32 v250, 0
	v_mov_b32_e32 v251, 0
	v_lshlrev_b32_e32 v246, 16, v166
	v_and_b32_e32 v247, 0xffff0000, v166
	v_lshlrev_b32_e32 v248, 16, v167
	v_and_b32_e32 v249, 0xffff0000, v167
	v_fmac_f32_e32 v250, v246, v246
	v_fmac_f32_e32 v251, v247, v247
	v_fmac_f32_e32 v250, v248, v248
	v_fmac_f32_e32 v251, v249, v249
	v_lshlrev_b32_e32 v246, 16, v168
	v_and_b32_e32 v247, 0xffff0000, v168
	v_lshlrev_b32_e32 v248, 16, v169
	v_and_b32_e32 v249, 0xffff0000, v169
	v_fmac_f32_e32 v250, v246, v246
	v_fmac_f32_e32 v251, v247, v247
	v_fmac_f32_e32 v250, v248, v248
	v_fmac_f32_e32 v251, v249, v249
	v_lshlrev_b32_e32 v246, 16, v170
	v_and_b32_e32 v247, 0xffff0000, v170
	v_lshlrev_b32_e32 v248, 16, v171
	v_and_b32_e32 v249, 0xffff0000, v171
	v_fmac_f32_e32 v250, v246, v246
	v_fmac_f32_e32 v251, v247, v247
	v_fmac_f32_e32 v250, v248, v248
	v_fmac_f32_e32 v251, v249, v249
	v_lshlrev_b32_e32 v246, 16, v172
	v_and_b32_e32 v247, 0xffff0000, v172
	v_lshlrev_b32_e32 v248, 16, v173
	v_and_b32_e32 v249, 0xffff0000, v173
	v_fmac_f32_e32 v250, v246, v246
	v_fmac_f32_e32 v251, v247, v247
	v_fmac_f32_e32 v250, v248, v248
	v_fmac_f32_e32 v251, v249, v249
	v_lshlrev_b32_e32 v246, 16, v174
	v_and_b32_e32 v247, 0xffff0000, v174
	v_lshlrev_b32_e32 v248, 16, v175
	v_and_b32_e32 v249, 0xffff0000, v175
	v_fmac_f32_e32 v250, v246, v246
	v_fmac_f32_e32 v251, v247, v247
	v_fmac_f32_e32 v250, v248, v248
	v_fmac_f32_e32 v251, v249, v249
	v_lshlrev_b32_e32 v246, 16, v176
	v_and_b32_e32 v247, 0xffff0000, v176
	v_lshlrev_b32_e32 v248, 16, v177
	v_and_b32_e32 v249, 0xffff0000, v177
	v_fmac_f32_e32 v250, v246, v246
	v_fmac_f32_e32 v251, v247, v247
	v_fmac_f32_e32 v250, v248, v248
	v_fmac_f32_e32 v251, v249, v249
	v_lshlrev_b32_e32 v246, 16, v178
	v_and_b32_e32 v247, 0xffff0000, v178
	v_lshlrev_b32_e32 v248, 16, v179
	v_and_b32_e32 v249, 0xffff0000, v179
	v_fmac_f32_e32 v250, v246, v246
	v_fmac_f32_e32 v251, v247, v247
	v_fmac_f32_e32 v250, v248, v248
	v_fmac_f32_e32 v251, v249, v249
	v_lshlrev_b32_e32 v246, 16, v180
	v_and_b32_e32 v247, 0xffff0000, v180
	v_lshlrev_b32_e32 v248, 16, v181
	v_and_b32_e32 v249, 0xffff0000, v181
	v_fmac_f32_e32 v250, v246, v246
	v_fmac_f32_e32 v251, v247, v247
	v_fmac_f32_e32 v250, v248, v248
	v_fmac_f32_e32 v251, v249, v249
	v_add_f32_e32 v250, v250, v251
	s_nop 1
	v_add_f32_dpp v218, v250, v250 quad_perm:[1,0,3,2] row_mask:0xf bank_mask:0xf bound_ctrl:1
	s_nop 1
	v_add_f32_dpp v218, v218, v218 quad_perm:[2,3,0,1] row_mask:0xf bank_mask:0xf bound_ctrl:1
	s_nop 1
	v_add_f32_dpp v218, v218, v218 row_ror:4 row_mask:0xf bank_mask:0xf bound_ctrl:1
	s_nop 1
	v_add_f32_dpp v218, v218, v218 row_ror:8 row_mask:0xf bank_mask:0xf bound_ctrl:1
	s_nop 1
	v_readlane_b32 s8, v218, 0
	v_readlane_b32 s9, v218, 16
	v_readlane_b32 s10, v218, 32
	v_readlane_b32 s11, v218, 48
	s_nop 1
	v_mov_b32_e32 v218, s8
	v_add_f32_e32 v218, s9, v218
	v_mov_b32_e32 v219, s10
	v_add_f32_e32 v219, s11, v219
	v_add_f32_e32 v218, v218, v219
	v_mul_f32_e32 v218, 0x3a000000, v218
	v_add_f32_e32 v218, 0x358637bd, v218
	v_rsq_f32_e32 v218, v218
	s_nop 0
	v_lshlrev_b32_e32 v246, 16, v166
	v_and_b32_e32 v247, 0xffff0000, v166
	v_lshlrev_b32_e32 v248, 16, v167
	v_and_b32_e32 v249, 0xffff0000, v167
	v_mul_f32_e32 v246, v246, v218
	v_mul_f32_e32 v247, v247, v218
	v_mul_f32_e32 v248, v248, v218
	v_mul_f32_e32 v249, v249, v218
	v_lshlrev_b32_e32 v0, 16, v182
	v_and_b32_e32 v1, 0xffff0000, v182
	v_lshlrev_b32_e32 v2, 16, v183
	v_and_b32_e32 v3, 0xffff0000, v183
	v_fmac_f32_e32 v0, v246, v32
	v_fmac_f32_e32 v1, v247, v33
	v_fmac_f32_e32 v2, v248, v34
	v_fmac_f32_e32 v3, v249, v35
	v_lshlrev_b32_e32 v246, 16, v168
	v_and_b32_e32 v247, 0xffff0000, v168
	v_lshlrev_b32_e32 v248, 16, v169
	v_and_b32_e32 v249, 0xffff0000, v169
	v_mul_f32_e32 v246, v246, v218
	v_mul_f32_e32 v247, v247, v218
	v_mul_f32_e32 v248, v248, v218
	v_mul_f32_e32 v249, v249, v218
	v_lshlrev_b32_e32 v4, 16, v184
	v_and_b32_e32 v5, 0xffff0000, v184
	v_lshlrev_b32_e32 v6, 16, v185
	v_and_b32_e32 v7, 0xffff0000, v185
	v_fmac_f32_e32 v4, v246, v36
	v_fmac_f32_e32 v5, v247, v37
	v_fmac_f32_e32 v6, v248, v38
	v_fmac_f32_e32 v7, v249, v39
	v_lshlrev_b32_e32 v246, 16, v170
	v_and_b32_e32 v247, 0xffff0000, v170
	v_lshlrev_b32_e32 v248, 16, v171
	v_and_b32_e32 v249, 0xffff0000, v171
	v_mul_f32_e32 v246, v246, v218
	v_mul_f32_e32 v247, v247, v218
	v_mul_f32_e32 v248, v248, v218
	v_mul_f32_e32 v249, v249, v218
	v_lshlrev_b32_e32 v8, 16, v186
	v_and_b32_e32 v9, 0xffff0000, v186
	v_lshlrev_b32_e32 v10, 16, v187
	v_and_b32_e32 v11, 0xffff0000, v187
	v_fmac_f32_e32 v8, v246, v40
	v_fmac_f32_e32 v9, v247, v41
	v_fmac_f32_e32 v10, v248, v42
	v_fmac_f32_e32 v11, v249, v43
	v_lshlrev_b32_e32 v246, 16, v172
	v_and_b32_e32 v247, 0xffff0000, v172
	v_lshlrev_b32_e32 v248, 16, v173
	v_and_b32_e32 v249, 0xffff0000, v173
	v_mul_f32_e32 v246, v246, v218
	v_mul_f32_e32 v247, v247, v218
	v_mul_f32_e32 v248, v248, v218
	v_mul_f32_e32 v249, v249, v218
	v_lshlrev_b32_e32 v12, 16, v188
	v_and_b32_e32 v13, 0xffff0000, v188
	v_lshlrev_b32_e32 v14, 16, v189
	v_and_b32_e32 v15, 0xffff0000, v189
	v_fmac_f32_e32 v12, v246, v44
	v_fmac_f32_e32 v13, v247, v45
	v_fmac_f32_e32 v14, v248, v46
	v_fmac_f32_e32 v15, v249, v47
	v_lshlrev_b32_e32 v246, 16, v174
	v_and_b32_e32 v247, 0xffff0000, v174
	v_lshlrev_b32_e32 v248, 16, v175
	v_and_b32_e32 v249, 0xffff0000, v175
	v_mul_f32_e32 v246, v246, v218
	v_mul_f32_e32 v247, v247, v218
	v_mul_f32_e32 v248, v248, v218
	v_mul_f32_e32 v249, v249, v218
	v_lshlrev_b32_e32 v16, 16, v190
	v_and_b32_e32 v17, 0xffff0000, v190
	v_lshlrev_b32_e32 v18, 16, v191
	v_and_b32_e32 v19, 0xffff0000, v191
	v_fmac_f32_e32 v16, v246, v48
	v_fmac_f32_e32 v17, v247, v49
	v_fmac_f32_e32 v18, v248, v50
	v_fmac_f32_e32 v19, v249, v51
	v_lshlrev_b32_e32 v246, 16, v176
	v_and_b32_e32 v247, 0xffff0000, v176
	v_lshlrev_b32_e32 v248, 16, v177
	v_and_b32_e32 v249, 0xffff0000, v177
	v_mul_f32_e32 v246, v246, v218
	v_mul_f32_e32 v247, v247, v218
	v_mul_f32_e32 v248, v248, v218
	v_mul_f32_e32 v249, v249, v218
	v_lshlrev_b32_e32 v20, 16, v192
	v_and_b32_e32 v21, 0xffff0000, v192
	v_lshlrev_b32_e32 v22, 16, v193
	v_and_b32_e32 v23, 0xffff0000, v193
	v_fmac_f32_e32 v20, v246, v52
	v_fmac_f32_e32 v21, v247, v53
	v_fmac_f32_e32 v22, v248, v54
	v_fmac_f32_e32 v23, v249, v55
	v_lshlrev_b32_e32 v246, 16, v178
	v_and_b32_e32 v247, 0xffff0000, v178
	v_lshlrev_b32_e32 v248, 16, v179
	v_and_b32_e32 v249, 0xffff0000, v179
	v_mul_f32_e32 v246, v246, v218
	v_mul_f32_e32 v247, v247, v218
	v_mul_f32_e32 v248, v248, v218
	v_mul_f32_e32 v249, v249, v218
	v_lshlrev_b32_e32 v24, 16, v194
	v_and_b32_e32 v25, 0xffff0000, v194
	v_lshlrev_b32_e32 v26, 16, v195
	v_and_b32_e32 v27, 0xffff0000, v195
	v_fmac_f32_e32 v24, v246, v56
	v_fmac_f32_e32 v25, v247, v57
	v_fmac_f32_e32 v26, v248, v58
	v_fmac_f32_e32 v27, v249, v59
	v_lshlrev_b32_e32 v246, 16, v180
	v_and_b32_e32 v247, 0xffff0000, v180
	v_lshlrev_b32_e32 v248, 16, v181
	v_and_b32_e32 v249, 0xffff0000, v181
	v_mul_f32_e32 v246, v246, v218
	v_mul_f32_e32 v247, v247, v218
	v_mul_f32_e32 v248, v248, v218
	v_mul_f32_e32 v249, v249, v218
	v_lshlrev_b32_e32 v28, 16, v196
	v_and_b32_e32 v29, 0xffff0000, v196
	v_lshlrev_b32_e32 v30, 16, v197
	v_and_b32_e32 v31, 0xffff0000, v197
	v_fmac_f32_e32 v28, v246, v60
	v_fmac_f32_e32 v29, v247, v61
	v_fmac_f32_e32 v30, v248, v62
	v_fmac_f32_e32 v31, v249, v63
	global_store_dwordx4 v163, v[0:3], s[70:71]
	global_store_dwordx4 v163, v[4:7], s[70:71] offset:1024
	global_store_dwordx4 v163, v[8:11], s[70:71] offset:2048
	global_store_dwordx4 v163, v[12:15], s[70:71] offset:3072
	s_add_u32 s10, s70, 0x1000
	s_addc_u32 s11, s71, 0
	global_store_dwordx4 v163, v[16:19], s[10:11]
	global_store_dwordx4 v163, v[20:23], s[10:11] offset:1024
	global_store_dwordx4 v163, v[24:27], s[10:11] offset:2048
	global_store_dwordx4 v163, v[28:31], s[10:11] offset:3072
	s_add_u32 s70, s70, 0x10000
	s_addc_u32 s71, s71, 0
	s_branch .Lmp_done
.Lmp_done:
	s_cmp_eq_u32 s99, 0
	s_cbranch_scc1 .Lmp_ret1
	s_add_i32 s16, s68, 1

.LBB0_1190:
	s_andn2_b64 s[20:21], s[20:21], exec
	s_and_b64 s[36:37], s[36:37], exec
	s_or_b64 s[20:21], s[20:21], s[36:37]
	s_and_saveexec_b64 s[36:37], s[34:35]
	s_cbranch_execz .LBB0_1185
	v_mov_b64_e32 v[2:3], s[12:13]
	flat_load_dword v1, v[2:3] sc1
	s_add_i32 s41, s41, 1
	s_or_b64 s[20:21], s[20:21], exec
	s_waitcnt vmcnt(0) lgkmcnt(0)
	v_cmp_ne_u32_e32 vcc, v1, v0
	s_orn2_b64 s[30:31], vcc, exec
	s_branch .LBB0_1185
.LBB0_1194:
	s_or_b64 exec, exec, s[14:15]
	s_xor_b64 s[12:13], s[18:19], -1
	s_and_saveexec_b64 s[14:15], s[12:13]
	s_xor_b64 s[14:15], exec, s[14:15]
	s_cbranch_execz .LBB0_1196
	v_mov_b64_e32 v[0:1], s[6:7]
	flat_atomic_add v[0:1], v220 offset:512
